# v37 + packed f32 math (v_pk_mul/fma/add_f32) in the swiglu, sigmoid-gate and gelu/plain tile epilogues
# speedup vs baseline: 1.0061x; 1.0061x over previous
;     __device__ __forceinline__ void operator()(const f32x4 (&acc)[2][2][4][2], const Unit& u, int wr, int wc, int fr, int fq) const {
;     ...
;             else {
;                 unsigned char* gb8 = wsb + (pn < 14 ? WS_GA : WS_GB) + ((pn - 10) & 3) * 256 + cl;
; #pragma unroll
;                 for (int ai = 0; ai < 2; ++ai)
; #pragma unroll
;                     for (int m = 0; m < 4; ++m) { unsigned char* rowp = gb8 + (size_t)(row0 + ai * HALF + m * 16) * 1024; const float nrf = -1.4426950408889634f * rsr[ai * HALF + m * 16];
; #pragma unroll
;                         for (int bj = 0; bj < 2; ++bj) { u32x2 w; w.x = 0u; w.y = 0u;
; #pragma unroll
;                             for (int e = 0; e < 4; ++e) { const float x0 = acc[ai][bj][m][0][e], x1 = acc[ai][bj][m][1][e];
;                                 const float r0 = 255.0f * __builtin_amdgcn_rcpf(1.0f + __builtin_amdgcn_exp2f(nrf * x0)), r1 = 255.0f * __builtin_amdgcn_rcpf(1.0f + __builtin_amdgcn_exp2f(nrf * x1));
;                                 w.x |= (unsigned)(r0 + 0.5f) << (8 * e); w.y |= (unsigned)(r1 + 0.5f) << (8 * e); }
;                             *(u32x2*)(rowp + bj * HALF) = w; }
;                         asm volatile("" ::: "memory"); }
.LBB0_398:
	s_and_b32 s0, s70, -4
	v_lshl_add_u32 v132, s18, 8, v202
	s_cmp_lg_u32 s0, 4
	s_mov_b64 s[0:1], -1
	s_cbranch_scc0 .LBB0_538
	s_cmp_gt_i32 s70, 9
	s_cbranch_scc0 .LBB0_401
	ds_read_b32 v160, v205
	s_cmp_lt_u32 s70, 14
	s_brev_b32 s0, 8
	s_cselect_b32 s0, s0, 0x11000000
	s_add_u32 s0, s16, s0
	s_addc_u32 s1, s17, 0
	s_lshl_b32 s8, s70, 8
	s_and_b32 s8, s8, 0x300
	s_xor_b32 s8, s8, 0x200
	s_add_u32 s0, s0, s8
	s_addc_u32 s1, s1, 0
	v_ashrrev_i32_e32 v133, 31, v132
	v_lshlrev_b64 v[134:135], 10, v[132:133]
	v_lshl_add_u64 v[136:137], s[0:1], 0, v[172:173]
	v_lshl_add_u64 v[134:135], v[136:137], 0, v[134:135]
	s_mov_b32 s8, 0x3b808081
	s_waitcnt lgkmcnt(0)
	ds_read_b32 v161, v205 offset:64
	v_mul_f32_e32 v160, 0xbfb8aa3b, v160
	v_pk_mul_f32 v[140:141], v[128:129], v[160:161] op_sel_hi:[1,0]
	v_pk_mul_f32 v[142:143], v[130:131], v[160:161] op_sel_hi:[1,0]
	v_pk_mul_f32 v[144:145], v[124:125], v[160:161] op_sel_hi:[1,0]
	v_pk_mul_f32 v[146:147], v[126:127], v[160:161] op_sel_hi:[1,0]
	v_pk_mul_f32 v[148:149], v[120:121], v[160:161] op_sel_hi:[1,0]
	v_pk_mul_f32 v[150:151], v[122:123], v[160:161] op_sel_hi:[1,0]
	v_pk_mul_f32 v[152:153], v[116:117], v[160:161] op_sel_hi:[1,0]
	v_pk_mul_f32 v[154:155], v[118:119], v[160:161] op_sel_hi:[1,0]
	v_exp_f32_e32 v140, v140
	v_exp_f32_e32 v141, v141
	v_exp_f32_e32 v142, v142
	v_exp_f32_e32 v143, v143
	v_exp_f32_e32 v144, v144
	v_exp_f32_e32 v145, v145
	v_exp_f32_e32 v146, v146
	v_exp_f32_e32 v147, v147
	v_exp_f32_e32 v148, v148
	v_exp_f32_e32 v149, v149
	v_exp_f32_e32 v150, v150
	v_exp_f32_e32 v151, v151
	v_exp_f32_e32 v152, v152
	v_exp_f32_e32 v153, v153
	v_exp_f32_e32 v154, v154
	v_exp_f32_e32 v155, v155
	v_pk_fma_f32 v[140:141], v[140:141], s[8:9], s[8:9] op_sel_hi:[1,0,0]
	v_pk_fma_f32 v[142:143], v[142:143], s[8:9], s[8:9] op_sel_hi:[1,0,0]
	v_pk_fma_f32 v[144:145], v[144:145], s[8:9], s[8:9] op_sel_hi:[1,0,0]
	v_pk_fma_f32 v[146:147], v[146:147], s[8:9], s[8:9] op_sel_hi:[1,0,0]
	v_pk_fma_f32 v[148:149], v[148:149], s[8:9], s[8:9] op_sel_hi:[1,0,0]
	v_pk_fma_f32 v[150:151], v[150:151], s[8:9], s[8:9] op_sel_hi:[1,0,0]
	v_pk_fma_f32 v[152:153], v[152:153], s[8:9], s[8:9] op_sel_hi:[1,0,0]
	v_pk_fma_f32 v[154:155], v[154:155], s[8:9], s[8:9] op_sel_hi:[1,0,0]
	v_rcp_f32_e32 v140, v140
	v_rcp_f32_e32 v141, v141
	v_rcp_f32_e32 v142, v142
	v_rcp_f32_e32 v143, v143
	v_rcp_f32_e32 v144, v144
	v_rcp_f32_e32 v145, v145
	v_rcp_f32_e32 v146, v146
	v_rcp_f32_e32 v147, v147
	v_rcp_f32_e32 v148, v148
	v_rcp_f32_e32 v149, v149
	v_rcp_f32_e32 v150, v150
	v_rcp_f32_e32 v151, v151
	v_rcp_f32_e32 v152, v152
	v_rcp_f32_e32 v153, v153
	v_rcp_f32_e32 v154, v154
	v_rcp_f32_e32 v155, v155
	v_cvt_rpi_i32_f32_sdwa v156, v140 dst_sel:BYTE_0 dst_unused:UNUSED_PAD src0_sel:DWORD
	v_cvt_rpi_i32_f32_sdwa v157, v144 dst_sel:BYTE_0 dst_unused:UNUSED_PAD src0_sel:DWORD
	v_cvt_rpi_i32_f32_sdwa v158, v148 dst_sel:BYTE_0 dst_unused:UNUSED_PAD src0_sel:DWORD
	v_cvt_rpi_i32_f32_sdwa v159, v152 dst_sel:BYTE_0 dst_unused:UNUSED_PAD src0_sel:DWORD
	v_cvt_rpi_i32_f32_sdwa v156, v141 dst_sel:BYTE_1 dst_unused:UNUSED_PRESERVE src0_sel:DWORD
	v_cvt_rpi_i32_f32_sdwa v157, v145 dst_sel:BYTE_1 dst_unused:UNUSED_PRESERVE src0_sel:DWORD
	v_cvt_rpi_i32_f32_sdwa v158, v149 dst_sel:BYTE_1 dst_unused:UNUSED_PRESERVE src0_sel:DWORD
	v_cvt_rpi_i32_f32_sdwa v159, v153 dst_sel:BYTE_1 dst_unused:UNUSED_PRESERVE src0_sel:DWORD
	v_cvt_rpi_i32_f32_sdwa v156, v142 dst_sel:BYTE_2 dst_unused:UNUSED_PRESERVE src0_sel:DWORD
	v_cvt_rpi_i32_f32_sdwa v157, v146 dst_sel:BYTE_2 dst_unused:UNUSED_PRESERVE src0_sel:DWORD
	v_cvt_rpi_i32_f32_sdwa v158, v150 dst_sel:BYTE_2 dst_unused:UNUSED_PRESERVE src0_sel:DWORD
	v_cvt_rpi_i32_f32_sdwa v159, v154 dst_sel:BYTE_2 dst_unused:UNUSED_PRESERVE src0_sel:DWORD
	v_cvt_rpi_i32_f32_sdwa v156, v143 dst_sel:BYTE_3 dst_unused:UNUSED_PRESERVE src0_sel:DWORD
	v_cvt_rpi_i32_f32_sdwa v157, v147 dst_sel:BYTE_3 dst_unused:UNUSED_PRESERVE src0_sel:DWORD
	v_cvt_rpi_i32_f32_sdwa v158, v151 dst_sel:BYTE_3 dst_unused:UNUSED_PRESERVE src0_sel:DWORD
	v_cvt_rpi_i32_f32_sdwa v159, v155 dst_sel:BYTE_3 dst_unused:UNUSED_PRESERVE src0_sel:DWORD
	s_nop 0
	global_store_dwordx2 v[134:135], v[156:157], off
	global_store_dwordx2 v[134:135], v[158:159], off offset:128
	s_nop 1
	s_waitcnt lgkmcnt(0)
;     __device__ __forceinline__ void operator()(const f32x4 (&acc)[2][2][4][2], const Unit& u, int wr, int wc, int fr, int fq) const {
;     ...
;                     for (int m = 0; m < 4; ++m) { unsigned char* rowp = gb8 + (size_t)(row0 + ai * HALF + m * 16) * 1024; const float nrf = -1.4426950408889634f * rsr[ai * HALF + m * 16];
; #pragma unroll
;                         for (int bj = 0; bj < 2; ++bj) { u32x2 w; w.x = 0u; w.y = 0u;
; #pragma unroll
;                             for (int e = 0; e < 4; ++e) { const float x0 = acc[ai][bj][m][0][e], x1 = acc[ai][bj][m][1][e];
;                                 const float r0 = 255.0f * __builtin_amdgcn_rcpf(1.0f + __builtin_amdgcn_exp2f(nrf * x0)), r1 = 255.0f * __builtin_amdgcn_rcpf(1.0f + __builtin_amdgcn_exp2f(nrf * x1));
;                                 w.x |= (unsigned)(r0 + 0.5f) << (8 * e); w.y |= (unsigned)(r1 + 0.5f) << (8 * e); }
;                             *(u32x2*)(rowp + bj * HALF) = w; }
	v_mov_b32_e32 v160, v161
	ds_read_b32 v161, v205 offset:128
	v_mul_f32_e32 v160, 0xbfb8aa3b, v160
	v_pk_mul_f32 v[140:141], v[112:113], v[160:161] op_sel_hi:[1,0]
	v_pk_mul_f32 v[142:143], v[114:115], v[160:161] op_sel_hi:[1,0]
	v_pk_mul_f32 v[144:145], v[108:109], v[160:161] op_sel_hi:[1,0]
	v_pk_mul_f32 v[146:147], v[110:111], v[160:161] op_sel_hi:[1,0]
	v_pk_mul_f32 v[148:149], v[104:105], v[160:161] op_sel_hi:[1,0]
	v_pk_mul_f32 v[150:151], v[106:107], v[160:161] op_sel_hi:[1,0]
	v_pk_mul_f32 v[152:153], v[100:101], v[160:161] op_sel_hi:[1,0]
	v_pk_mul_f32 v[154:155], v[102:103], v[160:161] op_sel_hi:[1,0]
	v_exp_f32_e32 v140, v140
	v_exp_f32_e32 v141, v141
	v_exp_f32_e32 v142, v142
	v_exp_f32_e32 v143, v143
	v_exp_f32_e32 v144, v144
	v_exp_f32_e32 v145, v145
	v_exp_f32_e32 v146, v146
	v_exp_f32_e32 v147, v147
	v_exp_f32_e32 v148, v148
	v_exp_f32_e32 v149, v149
	v_exp_f32_e32 v150, v150
	v_exp_f32_e32 v151, v151
	v_exp_f32_e32 v152, v152
	v_exp_f32_e32 v153, v153
	v_exp_f32_e32 v154, v154
	v_exp_f32_e32 v155, v155
	v_pk_fma_f32 v[140:141], v[140:141], s[8:9], s[8:9] op_sel_hi:[1,0,0]
	v_pk_fma_f32 v[142:143], v[142:143], s[8:9], s[8:9] op_sel_hi:[1,0,0]
	v_pk_fma_f32 v[144:145], v[144:145], s[8:9], s[8:9] op_sel_hi:[1,0,0]
	v_pk_fma_f32 v[146:147], v[146:147], s[8:9], s[8:9] op_sel_hi:[1,0,0]
	v_pk_fma_f32 v[148:149], v[148:149], s[8:9], s[8:9] op_sel_hi:[1,0,0]
	v_pk_fma_f32 v[150:151], v[150:151], s[8:9], s[8:9] op_sel_hi:[1,0,0]
	v_pk_fma_f32 v[152:153], v[152:153], s[8:9], s[8:9] op_sel_hi:[1,0,0]
	v_pk_fma_f32 v[154:155], v[154:155], s[8:9], s[8:9] op_sel_hi:[1,0,0]
	v_rcp_f32_e32 v140, v140
	v_rcp_f32_e32 v141, v141
	v_rcp_f32_e32 v142, v142
	v_rcp_f32_e32 v143, v143
	v_rcp_f32_e32 v144, v144
	v_rcp_f32_e32 v145, v145
	v_rcp_f32_e32 v146, v146
	v_rcp_f32_e32 v147, v147
	v_rcp_f32_e32 v148, v148
	v_rcp_f32_e32 v149, v149
	v_rcp_f32_e32 v150, v150
	v_rcp_f32_e32 v151, v151
	v_rcp_f32_e32 v152, v152
	v_rcp_f32_e32 v153, v153
	v_rcp_f32_e32 v154, v154
	v_rcp_f32_e32 v155, v155
	s_mov_b64 s[0:1], 0x4000
	v_lshl_add_u64 v[136:137], v[134:135], 0, s[0:1]
	v_cvt_rpi_i32_f32_sdwa v156, v140 dst_sel:BYTE_0 dst_unused:UNUSED_PAD src0_sel:DWORD
	v_cvt_rpi_i32_f32_sdwa v157, v144 dst_sel:BYTE_0 dst_unused:UNUSED_PAD src0_sel:DWORD
	v_cvt_rpi_i32_f32_sdwa v158, v148 dst_sel:BYTE_0 dst_unused:UNUSED_PAD src0_sel:DWORD
	v_cvt_rpi_i32_f32_sdwa v159, v152 dst_sel:BYTE_0 dst_unused:UNUSED_PAD src0_sel:DWORD
	v_cvt_rpi_i32_f32_sdwa v156, v141 dst_sel:BYTE_1 dst_unused:UNUSED_PRESERVE src0_sel:DWORD
	v_cvt_rpi_i32_f32_sdwa v157, v145 dst_sel:BYTE_1 dst_unused:UNUSED_PRESERVE src0_sel:DWORD
	v_cvt_rpi_i32_f32_sdwa v158, v149 dst_sel:BYTE_1 dst_unused:UNUSED_PRESERVE src0_sel:DWORD
	v_cvt_rpi_i32_f32_sdwa v159, v153 dst_sel:BYTE_1 dst_unused:UNUSED_PRESERVE src0_sel:DWORD
	v_cvt_rpi_i32_f32_sdwa v156, v142 dst_sel:BYTE_2 dst_unused:UNUSED_PRESERVE src0_sel:DWORD
	v_cvt_rpi_i32_f32_sdwa v157, v146 dst_sel:BYTE_2 dst_unused:UNUSED_PRESERVE src0_sel:DWORD
	v_cvt_rpi_i32_f32_sdwa v158, v150 dst_sel:BYTE_2 dst_unused:UNUSED_PRESERVE src0_sel:DWORD
	v_cvt_rpi_i32_f32_sdwa v159, v154 dst_sel:BYTE_2 dst_unused:UNUSED_PRESERVE src0_sel:DWORD
	v_cvt_rpi_i32_f32_sdwa v156, v143 dst_sel:BYTE_3 dst_unused:UNUSED_PRESERVE src0_sel:DWORD
	v_cvt_rpi_i32_f32_sdwa v157, v147 dst_sel:BYTE_3 dst_unused:UNUSED_PRESERVE src0_sel:DWORD
	v_cvt_rpi_i32_f32_sdwa v158, v151 dst_sel:BYTE_3 dst_unused:UNUSED_PRESERVE src0_sel:DWORD
	v_cvt_rpi_i32_f32_sdwa v159, v155 dst_sel:BYTE_3 dst_unused:UNUSED_PRESERVE src0_sel:DWORD
	s_nop 0
	global_store_dwordx2 v[136:137], v[156:157], off
	global_store_dwordx2 v[136:137], v[158:159], off offset:128
	s_nop 1
	s_waitcnt lgkmcnt(0)
	v_mov_b32_e32 v160, v161
	ds_read_b32 v161, v205 offset:192
	v_mul_f32_e32 v160, 0xbfb8aa3b, v160
	v_pk_mul_f32 v[140:141], v[96:97], v[160:161] op_sel_hi:[1,0]
	v_pk_mul_f32 v[142:143], v[98:99], v[160:161] op_sel_hi:[1,0]
	v_pk_mul_f32 v[144:145], v[92:93], v[160:161] op_sel_hi:[1,0]
	v_pk_mul_f32 v[146:147], v[94:95], v[160:161] op_sel_hi:[1,0]
	v_pk_mul_f32 v[148:149], v[88:89], v[160:161] op_sel_hi:[1,0]
	v_pk_mul_f32 v[150:151], v[90:91], v[160:161] op_sel_hi:[1,0]
	v_pk_mul_f32 v[152:153], v[84:85], v[160:161] op_sel_hi:[1,0]
	v_pk_mul_f32 v[154:155], v[86:87], v[160:161] op_sel_hi:[1,0]
	v_exp_f32_e32 v140, v140
	v_exp_f32_e32 v141, v141
	v_exp_f32_e32 v142, v142
	v_exp_f32_e32 v143, v143
	v_exp_f32_e32 v144, v144
	v_exp_f32_e32 v145, v145
	v_exp_f32_e32 v146, v146
	v_exp_f32_e32 v147, v147
	v_exp_f32_e32 v148, v148
	v_exp_f32_e32 v149, v149
	v_exp_f32_e32 v150, v150
	v_exp_f32_e32 v151, v151
	v_exp_f32_e32 v152, v152
	v_exp_f32_e32 v153, v153
	v_exp_f32_e32 v154, v154
	v_exp_f32_e32 v155, v155
	v_pk_fma_f32 v[140:141], v[140:141], s[8:9], s[8:9] op_sel_hi:[1,0,0]
	v_pk_fma_f32 v[142:143], v[142:143], s[8:9], s[8:9] op_sel_hi:[1,0,0]
	v_pk_fma_f32 v[144:145], v[144:145], s[8:9], s[8:9] op_sel_hi:[1,0,0]
	v_pk_fma_f32 v[146:147], v[146:147], s[8:9], s[8:9] op_sel_hi:[1,0,0]
	v_pk_fma_f32 v[148:149], v[148:149], s[8:9], s[8:9] op_sel_hi:[1,0,0]
	v_pk_fma_f32 v[150:151], v[150:151], s[8:9], s[8:9] op_sel_hi:[1,0,0]
	v_pk_fma_f32 v[152:153], v[152:153], s[8:9], s[8:9] op_sel_hi:[1,0,0]
	v_pk_fma_f32 v[154:155], v[154:155], s[8:9], s[8:9] op_sel_hi:[1,0,0]
	v_rcp_f32_e32 v140, v140
	v_rcp_f32_e32 v141, v141
	v_rcp_f32_e32 v142, v142
	v_rcp_f32_e32 v143, v143
	v_rcp_f32_e32 v144, v144
	v_rcp_f32_e32 v145, v145
	v_rcp_f32_e32 v146, v146
	v_rcp_f32_e32 v147, v147
	v_rcp_f32_e32 v148, v148
	v_rcp_f32_e32 v149, v149
	v_rcp_f32_e32 v150, v150
	v_rcp_f32_e32 v151, v151
	v_rcp_f32_e32 v152, v152
	v_rcp_f32_e32 v153, v153
;     __device__ __forceinline__ void operator()(const f32x4 (&acc)[2][2][4][2], const Unit& u, int wr, int wc, int fr, int fq) const {
;     ...
;                     for (int m = 0; m < 4; ++m) { unsigned char* rowp = gb8 + (size_t)(row0 + ai * HALF + m * 16) * 1024; const float nrf = -1.4426950408889634f * rsr[ai * HALF + m * 16];
; #pragma unroll
;                         for (int bj = 0; bj < 2; ++bj) { u32x2 w; w.x = 0u; w.y = 0u;
; #pragma unroll
;                             for (int e = 0; e < 4; ++e) { const float x0 = acc[ai][bj][m][0][e], x1 = acc[ai][bj][m][1][e];
;                                 const float r0 = 255.0f * __builtin_amdgcn_rcpf(1.0f + __builtin_amdgcn_exp2f(nrf * x0)), r1 = 255.0f * __builtin_amdgcn_rcpf(1.0f + __builtin_amdgcn_exp2f(nrf * x1));
;                                 w.x |= (unsigned)(r0 + 0.5f) << (8 * e); w.y |= (unsigned)(r1 + 0.5f) << (8 * e); }
;                             *(u32x2*)(rowp + bj * HALF) = w; }
	v_rcp_f32_e32 v154, v154
	v_rcp_f32_e32 v155, v155
	s_mov_b64 s[0:1], 0x8000
	v_lshl_add_u64 v[136:137], v[134:135], 0, s[0:1]
	v_cvt_rpi_i32_f32_sdwa v156, v140 dst_sel:BYTE_0 dst_unused:UNUSED_PAD src0_sel:DWORD
	v_cvt_rpi_i32_f32_sdwa v157, v144 dst_sel:BYTE_0 dst_unused:UNUSED_PAD src0_sel:DWORD
	v_cvt_rpi_i32_f32_sdwa v158, v148 dst_sel:BYTE_0 dst_unused:UNUSED_PAD src0_sel:DWORD
	v_cvt_rpi_i32_f32_sdwa v159, v152 dst_sel:BYTE_0 dst_unused:UNUSED_PAD src0_sel:DWORD
	v_cvt_rpi_i32_f32_sdwa v156, v141 dst_sel:BYTE_1 dst_unused:UNUSED_PRESERVE src0_sel:DWORD
	v_cvt_rpi_i32_f32_sdwa v157, v145 dst_sel:BYTE_1 dst_unused:UNUSED_PRESERVE src0_sel:DWORD
	v_cvt_rpi_i32_f32_sdwa v158, v149 dst_sel:BYTE_1 dst_unused:UNUSED_PRESERVE src0_sel:DWORD
	v_cvt_rpi_i32_f32_sdwa v159, v153 dst_sel:BYTE_1 dst_unused:UNUSED_PRESERVE src0_sel:DWORD
	v_cvt_rpi_i32_f32_sdwa v156, v142 dst_sel:BYTE_2 dst_unused:UNUSED_PRESERVE src0_sel:DWORD
	v_cvt_rpi_i32_f32_sdwa v157, v146 dst_sel:BYTE_2 dst_unused:UNUSED_PRESERVE src0_sel:DWORD
	v_cvt_rpi_i32_f32_sdwa v158, v150 dst_sel:BYTE_2 dst_unused:UNUSED_PRESERVE src0_sel:DWORD
	v_cvt_rpi_i32_f32_sdwa v159, v154 dst_sel:BYTE_2 dst_unused:UNUSED_PRESERVE src0_sel:DWORD
	v_cvt_rpi_i32_f32_sdwa v156, v143 dst_sel:BYTE_3 dst_unused:UNUSED_PRESERVE src0_sel:DWORD
	v_cvt_rpi_i32_f32_sdwa v157, v147 dst_sel:BYTE_3 dst_unused:UNUSED_PRESERVE src0_sel:DWORD
	v_cvt_rpi_i32_f32_sdwa v158, v151 dst_sel:BYTE_3 dst_unused:UNUSED_PRESERVE src0_sel:DWORD
	v_cvt_rpi_i32_f32_sdwa v159, v155 dst_sel:BYTE_3 dst_unused:UNUSED_PRESERVE src0_sel:DWORD
	s_nop 0
	global_store_dwordx2 v[136:137], v[156:157], off
	global_store_dwordx2 v[136:137], v[158:159], off offset:128
	s_nop 1
	s_waitcnt lgkmcnt(0)
	v_mov_b32_e32 v160, v161
	ds_read_b32 v161, v205 offset:512
	v_mul_f32_e32 v160, 0xbfb8aa3b, v160
	v_pk_mul_f32 v[140:141], v[80:81], v[160:161] op_sel_hi:[1,0]
	v_pk_mul_f32 v[142:143], v[82:83], v[160:161] op_sel_hi:[1,0]
	v_pk_mul_f32 v[144:145], v[76:77], v[160:161] op_sel_hi:[1,0]
	v_pk_mul_f32 v[146:147], v[78:79], v[160:161] op_sel_hi:[1,0]
	v_pk_mul_f32 v[148:149], v[72:73], v[160:161] op_sel_hi:[1,0]
	v_pk_mul_f32 v[150:151], v[74:75], v[160:161] op_sel_hi:[1,0]
	v_pk_mul_f32 v[152:153], v[68:69], v[160:161] op_sel_hi:[1,0]
	v_pk_mul_f32 v[154:155], v[70:71], v[160:161] op_sel_hi:[1,0]
	v_exp_f32_e32 v140, v140
	v_exp_f32_e32 v141, v141
	v_exp_f32_e32 v142, v142
	v_exp_f32_e32 v143, v143
	v_exp_f32_e32 v144, v144
	v_exp_f32_e32 v145, v145
	v_exp_f32_e32 v146, v146
	v_exp_f32_e32 v147, v147
	v_exp_f32_e32 v148, v148
	v_exp_f32_e32 v149, v149
	v_exp_f32_e32 v150, v150
	v_exp_f32_e32 v151, v151
	v_exp_f32_e32 v152, v152
	v_exp_f32_e32 v153, v153
	v_exp_f32_e32 v154, v154
	v_exp_f32_e32 v155, v155
	v_pk_fma_f32 v[140:141], v[140:141], s[8:9], s[8:9] op_sel_hi:[1,0,0]
	v_pk_fma_f32 v[142:143], v[142:143], s[8:9], s[8:9] op_sel_hi:[1,0,0]
	v_pk_fma_f32 v[144:145], v[144:145], s[8:9], s[8:9] op_sel_hi:[1,0,0]
	v_pk_fma_f32 v[146:147], v[146:147], s[8:9], s[8:9] op_sel_hi:[1,0,0]
	v_pk_fma_f32 v[148:149], v[148:149], s[8:9], s[8:9] op_sel_hi:[1,0,0]
	v_pk_fma_f32 v[150:151], v[150:151], s[8:9], s[8:9] op_sel_hi:[1,0,0]
	v_pk_fma_f32 v[152:153], v[152:153], s[8:9], s[8:9] op_sel_hi:[1,0,0]
	v_pk_fma_f32 v[154:155], v[154:155], s[8:9], s[8:9] op_sel_hi:[1,0,0]
	v_rcp_f32_e32 v140, v140
	v_rcp_f32_e32 v141, v141
	v_rcp_f32_e32 v142, v142
	v_rcp_f32_e32 v143, v143
	v_rcp_f32_e32 v144, v144
	v_rcp_f32_e32 v145, v145
	v_rcp_f32_e32 v146, v146
	v_rcp_f32_e32 v147, v147
	v_rcp_f32_e32 v148, v148
	v_rcp_f32_e32 v149, v149
	v_rcp_f32_e32 v150, v150
	v_rcp_f32_e32 v151, v151
	v_rcp_f32_e32 v152, v152
	v_rcp_f32_e32 v153, v153
	v_rcp_f32_e32 v154, v154
	v_rcp_f32_e32 v155, v155
	s_mov_b64 s[0:1], 0xc000
	v_lshl_add_u64 v[136:137], v[134:135], 0, s[0:1]
	v_cvt_rpi_i32_f32_sdwa v156, v140 dst_sel:BYTE_0 dst_unused:UNUSED_PAD src0_sel:DWORD
	v_cvt_rpi_i32_f32_sdwa v157, v144 dst_sel:BYTE_0 dst_unused:UNUSED_PAD src0_sel:DWORD
	v_cvt_rpi_i32_f32_sdwa v158, v148 dst_sel:BYTE_0 dst_unused:UNUSED_PAD src0_sel:DWORD
	v_cvt_rpi_i32_f32_sdwa v159, v152 dst_sel:BYTE_0 dst_unused:UNUSED_PAD src0_sel:DWORD
	v_cvt_rpi_i32_f32_sdwa v156, v141 dst_sel:BYTE_1 dst_unused:UNUSED_PRESERVE src0_sel:DWORD
	v_cvt_rpi_i32_f32_sdwa v157, v145 dst_sel:BYTE_1 dst_unused:UNUSED_PRESERVE src0_sel:DWORD
	v_cvt_rpi_i32_f32_sdwa v158, v149 dst_sel:BYTE_1 dst_unused:UNUSED_PRESERVE src0_sel:DWORD
	v_cvt_rpi_i32_f32_sdwa v159, v153 dst_sel:BYTE_1 dst_unused:UNUSED_PRESERVE src0_sel:DWORD
	v_cvt_rpi_i32_f32_sdwa v156, v142 dst_sel:BYTE_2 dst_unused:UNUSED_PRESERVE src0_sel:DWORD
	v_cvt_rpi_i32_f32_sdwa v157, v146 dst_sel:BYTE_2 dst_unused:UNUSED_PRESERVE src0_sel:DWORD
	v_cvt_rpi_i32_f32_sdwa v158, v150 dst_sel:BYTE_2 dst_unused:UNUSED_PRESERVE src0_sel:DWORD
	v_cvt_rpi_i32_f32_sdwa v159, v154 dst_sel:BYTE_2 dst_unused:UNUSED_PRESERVE src0_sel:DWORD
	v_cvt_rpi_i32_f32_sdwa v156, v143 dst_sel:BYTE_3 dst_unused:UNUSED_PRESERVE src0_sel:DWORD
	v_cvt_rpi_i32_f32_sdwa v157, v147 dst_sel:BYTE_3 dst_unused:UNUSED_PRESERVE src0_sel:DWORD
	v_cvt_rpi_i32_f32_sdwa v158, v151 dst_sel:BYTE_3 dst_unused:UNUSED_PRESERVE src0_sel:DWORD
	v_cvt_rpi_i32_f32_sdwa v159, v155 dst_sel:BYTE_3 dst_unused:UNUSED_PRESERVE src0_sel:DWORD
	s_nop 0
	global_store_dwordx2 v[136:137], v[156:157], off
	global_store_dwordx2 v[136:137], v[158:159], off offset:128
	s_nop 1
	s_waitcnt lgkmcnt(0)
;     __device__ __forceinline__ void operator()(const f32x4 (&acc)[2][2][4][2], const Unit& u, int wr, int wc, int fr, int fq) const {
;     ...
;                     for (int m = 0; m < 4; ++m) { unsigned char* rowp = gb8 + (size_t)(row0 + ai * HALF + m * 16) * 1024; const float nrf = -1.4426950408889634f * rsr[ai * HALF + m * 16];
; #pragma unroll
;                         for (int bj = 0; bj < 2; ++bj) { u32x2 w; w.x = 0u; w.y = 0u;
; #pragma unroll
;                             for (int e = 0; e < 4; ++e) { const float x0 = acc[ai][bj][m][0][e], x1 = acc[ai][bj][m][1][e];
;                                 const float r0 = 255.0f * __builtin_amdgcn_rcpf(1.0f + __builtin_amdgcn_exp2f(nrf * x0)), r1 = 255.0f * __builtin_amdgcn_rcpf(1.0f + __builtin_amdgcn_exp2f(nrf * x1));
;                                 w.x |= (unsigned)(r0 + 0.5f) << (8 * e); w.y |= (unsigned)(r1 + 0.5f) << (8 * e); }
;                             *(u32x2*)(rowp + bj * HALF) = w; }
	v_mov_b32_e32 v160, v161
	ds_read_b32 v161, v205 offset:576
	v_mul_f32_e32 v160, 0xbfb8aa3b, v160
	v_pk_mul_f32 v[140:141], v[64:65], v[160:161] op_sel_hi:[1,0]
	v_pk_mul_f32 v[142:143], v[66:67], v[160:161] op_sel_hi:[1,0]
	v_pk_mul_f32 v[144:145], v[60:61], v[160:161] op_sel_hi:[1,0]
	v_pk_mul_f32 v[146:147], v[62:63], v[160:161] op_sel_hi:[1,0]
	v_pk_mul_f32 v[148:149], v[56:57], v[160:161] op_sel_hi:[1,0]
	v_pk_mul_f32 v[150:151], v[58:59], v[160:161] op_sel_hi:[1,0]
	v_pk_mul_f32 v[152:153], v[52:53], v[160:161] op_sel_hi:[1,0]
	v_pk_mul_f32 v[154:155], v[54:55], v[160:161] op_sel_hi:[1,0]
	v_exp_f32_e32 v140, v140
	v_exp_f32_e32 v141, v141
	v_exp_f32_e32 v142, v142
	v_exp_f32_e32 v143, v143
	v_exp_f32_e32 v144, v144
	v_exp_f32_e32 v145, v145
	v_exp_f32_e32 v146, v146
	v_exp_f32_e32 v147, v147
	v_exp_f32_e32 v148, v148
	v_exp_f32_e32 v149, v149
	v_exp_f32_e32 v150, v150
	v_exp_f32_e32 v151, v151
	v_exp_f32_e32 v152, v152
	v_exp_f32_e32 v153, v153
	v_exp_f32_e32 v154, v154
	v_exp_f32_e32 v155, v155
	v_pk_fma_f32 v[140:141], v[140:141], s[8:9], s[8:9] op_sel_hi:[1,0,0]
	v_pk_fma_f32 v[142:143], v[142:143], s[8:9], s[8:9] op_sel_hi:[1,0,0]
	v_pk_fma_f32 v[144:145], v[144:145], s[8:9], s[8:9] op_sel_hi:[1,0,0]
	v_pk_fma_f32 v[146:147], v[146:147], s[8:9], s[8:9] op_sel_hi:[1,0,0]
	v_pk_fma_f32 v[148:149], v[148:149], s[8:9], s[8:9] op_sel_hi:[1,0,0]
	v_pk_fma_f32 v[150:151], v[150:151], s[8:9], s[8:9] op_sel_hi:[1,0,0]
	v_pk_fma_f32 v[152:153], v[152:153], s[8:9], s[8:9] op_sel_hi:[1,0,0]
	v_pk_fma_f32 v[154:155], v[154:155], s[8:9], s[8:9] op_sel_hi:[1,0,0]
	v_rcp_f32_e32 v140, v140
	v_rcp_f32_e32 v141, v141
	v_rcp_f32_e32 v142, v142
	v_rcp_f32_e32 v143, v143
	v_rcp_f32_e32 v144, v144
	v_rcp_f32_e32 v145, v145
	v_rcp_f32_e32 v146, v146
	v_rcp_f32_e32 v147, v147
	v_rcp_f32_e32 v148, v148
	v_rcp_f32_e32 v149, v149
	v_rcp_f32_e32 v150, v150
	v_rcp_f32_e32 v151, v151
	v_rcp_f32_e32 v152, v152
	v_rcp_f32_e32 v153, v153
	v_rcp_f32_e32 v154, v154
	v_rcp_f32_e32 v155, v155
	s_mov_b64 s[0:1], 0x20000
	v_lshl_add_u64 v[136:137], v[134:135], 0, s[0:1]
	v_cvt_rpi_i32_f32_sdwa v156, v140 dst_sel:BYTE_0 dst_unused:UNUSED_PAD src0_sel:DWORD
	v_cvt_rpi_i32_f32_sdwa v157, v144 dst_sel:BYTE_0 dst_unused:UNUSED_PAD src0_sel:DWORD
	v_cvt_rpi_i32_f32_sdwa v158, v148 dst_sel:BYTE_0 dst_unused:UNUSED_PAD src0_sel:DWORD
	v_cvt_rpi_i32_f32_sdwa v159, v152 dst_sel:BYTE_0 dst_unused:UNUSED_PAD src0_sel:DWORD
	v_cvt_rpi_i32_f32_sdwa v156, v141 dst_sel:BYTE_1 dst_unused:UNUSED_PRESERVE src0_sel:DWORD
	v_cvt_rpi_i32_f32_sdwa v157, v145 dst_sel:BYTE_1 dst_unused:UNUSED_PRESERVE src0_sel:DWORD
	v_cvt_rpi_i32_f32_sdwa v158, v149 dst_sel:BYTE_1 dst_unused:UNUSED_PRESERVE src0_sel:DWORD
	v_cvt_rpi_i32_f32_sdwa v159, v153 dst_sel:BYTE_1 dst_unused:UNUSED_PRESERVE src0_sel:DWORD
	v_cvt_rpi_i32_f32_sdwa v156, v142 dst_sel:BYTE_2 dst_unused:UNUSED_PRESERVE src0_sel:DWORD
	v_cvt_rpi_i32_f32_sdwa v157, v146 dst_sel:BYTE_2 dst_unused:UNUSED_PRESERVE src0_sel:DWORD
	v_cvt_rpi_i32_f32_sdwa v158, v150 dst_sel:BYTE_2 dst_unused:UNUSED_PRESERVE src0_sel:DWORD
	v_cvt_rpi_i32_f32_sdwa v159, v154 dst_sel:BYTE_2 dst_unused:UNUSED_PRESERVE src0_sel:DWORD
	v_cvt_rpi_i32_f32_sdwa v156, v143 dst_sel:BYTE_3 dst_unused:UNUSED_PRESERVE src0_sel:DWORD
	v_cvt_rpi_i32_f32_sdwa v157, v147 dst_sel:BYTE_3 dst_unused:UNUSED_PRESERVE src0_sel:DWORD
	v_cvt_rpi_i32_f32_sdwa v158, v151 dst_sel:BYTE_3 dst_unused:UNUSED_PRESERVE src0_sel:DWORD
	v_cvt_rpi_i32_f32_sdwa v159, v155 dst_sel:BYTE_3 dst_unused:UNUSED_PRESERVE src0_sel:DWORD
	s_nop 0
	global_store_dwordx2 v[136:137], v[156:157], off
	global_store_dwordx2 v[136:137], v[158:159], off offset:128
	s_nop 1
	s_waitcnt lgkmcnt(0)
	v_mov_b32_e32 v160, v161
	ds_read_b32 v161, v205 offset:640
	v_mul_f32_e32 v160, 0xbfb8aa3b, v160
	v_pk_mul_f32 v[140:141], v[48:49], v[160:161] op_sel_hi:[1,0]
	v_pk_mul_f32 v[142:143], v[50:51], v[160:161] op_sel_hi:[1,0]
	v_pk_mul_f32 v[144:145], v[44:45], v[160:161] op_sel_hi:[1,0]
	v_pk_mul_f32 v[146:147], v[46:47], v[160:161] op_sel_hi:[1,0]
	v_pk_mul_f32 v[148:149], v[40:41], v[160:161] op_sel_hi:[1,0]
	v_pk_mul_f32 v[150:151], v[42:43], v[160:161] op_sel_hi:[1,0]
	v_pk_mul_f32 v[152:153], v[36:37], v[160:161] op_sel_hi:[1,0]
	v_pk_mul_f32 v[154:155], v[38:39], v[160:161] op_sel_hi:[1,0]
	v_exp_f32_e32 v140, v140
	v_exp_f32_e32 v141, v141
	v_exp_f32_e32 v142, v142
	v_exp_f32_e32 v143, v143
	v_exp_f32_e32 v144, v144
	v_exp_f32_e32 v145, v145
	v_exp_f32_e32 v146, v146
	v_exp_f32_e32 v147, v147
	v_exp_f32_e32 v148, v148
	v_exp_f32_e32 v149, v149
	v_exp_f32_e32 v150, v150
	v_exp_f32_e32 v151, v151
	v_exp_f32_e32 v152, v152
	v_exp_f32_e32 v153, v153
	v_exp_f32_e32 v154, v154
	v_exp_f32_e32 v155, v155
	v_pk_fma_f32 v[140:141], v[140:141], s[8:9], s[8:9] op_sel_hi:[1,0,0]
	v_pk_fma_f32 v[142:143], v[142:143], s[8:9], s[8:9] op_sel_hi:[1,0,0]
	v_pk_fma_f32 v[144:145], v[144:145], s[8:9], s[8:9] op_sel_hi:[1,0,0]
	v_pk_fma_f32 v[146:147], v[146:147], s[8:9], s[8:9] op_sel_hi:[1,0,0]
	v_pk_fma_f32 v[148:149], v[148:149], s[8:9], s[8:9] op_sel_hi:[1,0,0]
	v_pk_fma_f32 v[150:151], v[150:151], s[8:9], s[8:9] op_sel_hi:[1,0,0]
	v_pk_fma_f32 v[152:153], v[152:153], s[8:9], s[8:9] op_sel_hi:[1,0,0]
	v_pk_fma_f32 v[154:155], v[154:155], s[8:9], s[8:9] op_sel_hi:[1,0,0]
	v_rcp_f32_e32 v140, v140
	v_rcp_f32_e32 v141, v141
	v_rcp_f32_e32 v142, v142
	v_rcp_f32_e32 v143, v143
	v_rcp_f32_e32 v144, v144
	v_rcp_f32_e32 v145, v145
	v_rcp_f32_e32 v146, v146
	v_rcp_f32_e32 v147, v147
	v_rcp_f32_e32 v148, v148
	v_rcp_f32_e32 v149, v149
	v_rcp_f32_e32 v150, v150
	v_rcp_f32_e32 v151, v151
	v_rcp_f32_e32 v152, v152
	v_rcp_f32_e32 v153, v153
;     __device__ __forceinline__ void operator()(const f32x4 (&acc)[2][2][4][2], const Unit& u, int wr, int wc, int fr, int fq) const {
;     ...
;                     for (int m = 0; m < 4; ++m) { unsigned char* rowp = gb8 + (size_t)(row0 + ai * HALF + m * 16) * 1024; const float nrf = -1.4426950408889634f * rsr[ai * HALF + m * 16];
; #pragma unroll
;                         for (int bj = 0; bj < 2; ++bj) { u32x2 w; w.x = 0u; w.y = 0u;
; #pragma unroll
;                             for (int e = 0; e < 4; ++e) { const float x0 = acc[ai][bj][m][0][e], x1 = acc[ai][bj][m][1][e];
;                                 const float r0 = 255.0f * __builtin_amdgcn_rcpf(1.0f + __builtin_amdgcn_exp2f(nrf * x0)), r1 = 255.0f * __builtin_amdgcn_rcpf(1.0f + __builtin_amdgcn_exp2f(nrf * x1));
;                                 w.x |= (unsigned)(r0 + 0.5f) << (8 * e); w.y |= (unsigned)(r1 + 0.5f) << (8 * e); }
;                             *(u32x2*)(rowp + bj * HALF) = w; }
	v_rcp_f32_e32 v154, v154
	v_rcp_f32_e32 v155, v155
	s_mov_b64 s[0:1], 0x24000
	v_lshl_add_u64 v[136:137], v[134:135], 0, s[0:1]
	v_cvt_rpi_i32_f32_sdwa v156, v140 dst_sel:BYTE_0 dst_unused:UNUSED_PAD src0_sel:DWORD
	v_cvt_rpi_i32_f32_sdwa v157, v144 dst_sel:BYTE_0 dst_unused:UNUSED_PAD src0_sel:DWORD
	v_cvt_rpi_i32_f32_sdwa v158, v148 dst_sel:BYTE_0 dst_unused:UNUSED_PAD src0_sel:DWORD
	v_cvt_rpi_i32_f32_sdwa v159, v152 dst_sel:BYTE_0 dst_unused:UNUSED_PAD src0_sel:DWORD
	v_cvt_rpi_i32_f32_sdwa v156, v141 dst_sel:BYTE_1 dst_unused:UNUSED_PRESERVE src0_sel:DWORD
	v_cvt_rpi_i32_f32_sdwa v157, v145 dst_sel:BYTE_1 dst_unused:UNUSED_PRESERVE src0_sel:DWORD
	v_cvt_rpi_i32_f32_sdwa v158, v149 dst_sel:BYTE_1 dst_unused:UNUSED_PRESERVE src0_sel:DWORD
	v_cvt_rpi_i32_f32_sdwa v159, v153 dst_sel:BYTE_1 dst_unused:UNUSED_PRESERVE src0_sel:DWORD
	v_cvt_rpi_i32_f32_sdwa v156, v142 dst_sel:BYTE_2 dst_unused:UNUSED_PRESERVE src0_sel:DWORD
	v_cvt_rpi_i32_f32_sdwa v157, v146 dst_sel:BYTE_2 dst_unused:UNUSED_PRESERVE src0_sel:DWORD
	v_cvt_rpi_i32_f32_sdwa v158, v150 dst_sel:BYTE_2 dst_unused:UNUSED_PRESERVE src0_sel:DWORD
	v_cvt_rpi_i32_f32_sdwa v159, v154 dst_sel:BYTE_2 dst_unused:UNUSED_PRESERVE src0_sel:DWORD
	v_cvt_rpi_i32_f32_sdwa v156, v143 dst_sel:BYTE_3 dst_unused:UNUSED_PRESERVE src0_sel:DWORD
	v_cvt_rpi_i32_f32_sdwa v157, v147 dst_sel:BYTE_3 dst_unused:UNUSED_PRESERVE src0_sel:DWORD
	v_cvt_rpi_i32_f32_sdwa v158, v151 dst_sel:BYTE_3 dst_unused:UNUSED_PRESERVE src0_sel:DWORD
	v_cvt_rpi_i32_f32_sdwa v159, v155 dst_sel:BYTE_3 dst_unused:UNUSED_PRESERVE src0_sel:DWORD
	s_nop 0
	global_store_dwordx2 v[136:137], v[156:157], off
	global_store_dwordx2 v[136:137], v[158:159], off offset:128
	s_nop 1
	s_waitcnt lgkmcnt(0)
	v_mov_b32_e32 v160, v161
	ds_read_b32 v161, v205 offset:704
	v_mul_f32_e32 v160, 0xbfb8aa3b, v160
	v_pk_mul_f32 v[140:141], v[32:33], v[160:161] op_sel_hi:[1,0]
	v_pk_mul_f32 v[142:143], v[34:35], v[160:161] op_sel_hi:[1,0]
	v_pk_mul_f32 v[144:145], v[28:29], v[160:161] op_sel_hi:[1,0]
	v_pk_mul_f32 v[146:147], v[30:31], v[160:161] op_sel_hi:[1,0]
	v_pk_mul_f32 v[148:149], v[24:25], v[160:161] op_sel_hi:[1,0]
	v_pk_mul_f32 v[150:151], v[26:27], v[160:161] op_sel_hi:[1,0]
	v_pk_mul_f32 v[152:153], v[20:21], v[160:161] op_sel_hi:[1,0]
	v_pk_mul_f32 v[154:155], v[22:23], v[160:161] op_sel_hi:[1,0]
	v_exp_f32_e32 v140, v140
	v_exp_f32_e32 v141, v141
	v_exp_f32_e32 v142, v142
	v_exp_f32_e32 v143, v143
	v_exp_f32_e32 v144, v144
	v_exp_f32_e32 v145, v145
	v_exp_f32_e32 v146, v146
	v_exp_f32_e32 v147, v147
	v_exp_f32_e32 v148, v148
	v_exp_f32_e32 v149, v149
	v_exp_f32_e32 v150, v150
	v_exp_f32_e32 v151, v151
	v_exp_f32_e32 v152, v152
	v_exp_f32_e32 v153, v153
	v_exp_f32_e32 v154, v154
	v_exp_f32_e32 v155, v155
	v_pk_fma_f32 v[140:141], v[140:141], s[8:9], s[8:9] op_sel_hi:[1,0,0]
	v_pk_fma_f32 v[142:143], v[142:143], s[8:9], s[8:9] op_sel_hi:[1,0,0]
	v_pk_fma_f32 v[144:145], v[144:145], s[8:9], s[8:9] op_sel_hi:[1,0,0]
	v_pk_fma_f32 v[146:147], v[146:147], s[8:9], s[8:9] op_sel_hi:[1,0,0]
	v_pk_fma_f32 v[148:149], v[148:149], s[8:9], s[8:9] op_sel_hi:[1,0,0]
	v_pk_fma_f32 v[150:151], v[150:151], s[8:9], s[8:9] op_sel_hi:[1,0,0]
	v_pk_fma_f32 v[152:153], v[152:153], s[8:9], s[8:9] op_sel_hi:[1,0,0]
	v_pk_fma_f32 v[154:155], v[154:155], s[8:9], s[8:9] op_sel_hi:[1,0,0]
	v_rcp_f32_e32 v140, v140
	v_rcp_f32_e32 v141, v141
	v_rcp_f32_e32 v142, v142
	v_rcp_f32_e32 v143, v143
	v_rcp_f32_e32 v144, v144
	v_rcp_f32_e32 v145, v145
	v_rcp_f32_e32 v146, v146
	v_rcp_f32_e32 v147, v147
	v_rcp_f32_e32 v148, v148
	v_rcp_f32_e32 v149, v149
	v_rcp_f32_e32 v150, v150
	v_rcp_f32_e32 v151, v151
	v_rcp_f32_e32 v152, v152
	v_rcp_f32_e32 v153, v153
	v_rcp_f32_e32 v154, v154
	v_rcp_f32_e32 v155, v155
	s_mov_b64 s[0:1], 0x28000
	v_lshl_add_u64 v[136:137], v[134:135], 0, s[0:1]
	v_cvt_rpi_i32_f32_sdwa v156, v140 dst_sel:BYTE_0 dst_unused:UNUSED_PAD src0_sel:DWORD
	v_cvt_rpi_i32_f32_sdwa v157, v144 dst_sel:BYTE_0 dst_unused:UNUSED_PAD src0_sel:DWORD
	v_cvt_rpi_i32_f32_sdwa v158, v148 dst_sel:BYTE_0 dst_unused:UNUSED_PAD src0_sel:DWORD
	v_cvt_rpi_i32_f32_sdwa v159, v152 dst_sel:BYTE_0 dst_unused:UNUSED_PAD src0_sel:DWORD
	v_cvt_rpi_i32_f32_sdwa v156, v141 dst_sel:BYTE_1 dst_unused:UNUSED_PRESERVE src0_sel:DWORD
	v_cvt_rpi_i32_f32_sdwa v157, v145 dst_sel:BYTE_1 dst_unused:UNUSED_PRESERVE src0_sel:DWORD
	v_cvt_rpi_i32_f32_sdwa v158, v149 dst_sel:BYTE_1 dst_unused:UNUSED_PRESERVE src0_sel:DWORD
	v_cvt_rpi_i32_f32_sdwa v159, v153 dst_sel:BYTE_1 dst_unused:UNUSED_PRESERVE src0_sel:DWORD
	v_cvt_rpi_i32_f32_sdwa v156, v142 dst_sel:BYTE_2 dst_unused:UNUSED_PRESERVE src0_sel:DWORD
	v_cvt_rpi_i32_f32_sdwa v157, v146 dst_sel:BYTE_2 dst_unused:UNUSED_PRESERVE src0_sel:DWORD
	v_cvt_rpi_i32_f32_sdwa v158, v150 dst_sel:BYTE_2 dst_unused:UNUSED_PRESERVE src0_sel:DWORD
	v_cvt_rpi_i32_f32_sdwa v159, v154 dst_sel:BYTE_2 dst_unused:UNUSED_PRESERVE src0_sel:DWORD
	v_cvt_rpi_i32_f32_sdwa v156, v143 dst_sel:BYTE_3 dst_unused:UNUSED_PRESERVE src0_sel:DWORD
	v_cvt_rpi_i32_f32_sdwa v157, v147 dst_sel:BYTE_3 dst_unused:UNUSED_PRESERVE src0_sel:DWORD
	v_cvt_rpi_i32_f32_sdwa v158, v151 dst_sel:BYTE_3 dst_unused:UNUSED_PRESERVE src0_sel:DWORD
	v_cvt_rpi_i32_f32_sdwa v159, v155 dst_sel:BYTE_3 dst_unused:UNUSED_PRESERVE src0_sel:DWORD
	s_nop 0
	global_store_dwordx2 v[136:137], v[156:157], off
	global_store_dwordx2 v[136:137], v[158:159], off offset:128
	s_nop 1
	s_waitcnt lgkmcnt(0)
;     __device__ __forceinline__ void operator()(const f32x4 (&acc)[2][2][4][2], const Unit& u, int wr, int wc, int fr, int fq) const {
;     ...
;             bf16_t* base = (bf16_t*)(wsb + (pn < 2 ? WS_U : (pn < 4 ? WS_VG : WS_VA))); const int ldc = 512, pc = pn < 2 ? pn : (pn < 4 ? pn - 2 : pn - 8), act = pn < 4 ? 1 : 0;
;             float* stat = (pn == 2 || pn == 3) ? (float*)(wsb + WS_STAT) + ((pn - 2) * 4 + wc) * 2 : nullptr;
;             if (pn < 10) store_tile8(acc, rsr, base, ldc, row0, pc * 256 + cl, act, u.half != 0, stat, fq);
;     ...
;                     for (int m = 0; m < 4; ++m) { unsigned char* rowp = gb8 + (size_t)(row0 + ai * HALF + m * 16) * 1024; const float nrf = -1.4426950408889634f * rsr[ai * HALF + m * 16];
; #pragma unroll
;                         for (int bj = 0; bj < 2; ++bj) { u32x2 w; w.x = 0u; w.y = 0u;
; #pragma unroll
;                             for (int e = 0; e < 4; ++e) { const float x0 = acc[ai][bj][m][0][e], x1 = acc[ai][bj][m][1][e];
;                                 const float r0 = 255.0f * __builtin_amdgcn_rcpf(1.0f + __builtin_amdgcn_exp2f(nrf * x0)), r1 = 255.0f * __builtin_amdgcn_rcpf(1.0f + __builtin_amdgcn_exp2f(nrf * x1));
;                                 w.x |= (unsigned)(r0 + 0.5f) << (8 * e); w.y |= (unsigned)(r1 + 0.5f) << (8 * e); }
;                             *(u32x2*)(rowp + bj * HALF) = w; }
	v_mov_b32_e32 v160, v161
	v_mul_f32_e32 v160, 0xbfb8aa3b, v160
	v_pk_mul_f32 v[140:141], v[16:17], v[160:161] op_sel_hi:[1,0]
	v_pk_mul_f32 v[142:143], v[18:19], v[160:161] op_sel_hi:[1,0]
	v_pk_mul_f32 v[144:145], v[12:13], v[160:161] op_sel_hi:[1,0]
	v_pk_mul_f32 v[146:147], v[14:15], v[160:161] op_sel_hi:[1,0]
	v_pk_mul_f32 v[148:149], v[8:9], v[160:161] op_sel_hi:[1,0]
	v_pk_mul_f32 v[150:151], v[10:11], v[160:161] op_sel_hi:[1,0]
	v_pk_mul_f32 v[152:153], v[4:5], v[160:161] op_sel_hi:[1,0]
	v_pk_mul_f32 v[154:155], v[6:7], v[160:161] op_sel_hi:[1,0]
	v_exp_f32_e32 v140, v140
	v_exp_f32_e32 v141, v141
	v_exp_f32_e32 v142, v142
	v_exp_f32_e32 v143, v143
	v_exp_f32_e32 v144, v144
	v_exp_f32_e32 v145, v145
	v_exp_f32_e32 v146, v146
	v_exp_f32_e32 v147, v147
	v_exp_f32_e32 v148, v148
	v_exp_f32_e32 v149, v149
	v_exp_f32_e32 v150, v150
	v_exp_f32_e32 v151, v151
	v_exp_f32_e32 v152, v152
	v_exp_f32_e32 v153, v153
	v_exp_f32_e32 v154, v154
	v_exp_f32_e32 v155, v155
	v_pk_fma_f32 v[140:141], v[140:141], s[8:9], s[8:9] op_sel_hi:[1,0,0]
	v_pk_fma_f32 v[142:143], v[142:143], s[8:9], s[8:9] op_sel_hi:[1,0,0]
	v_pk_fma_f32 v[144:145], v[144:145], s[8:9], s[8:9] op_sel_hi:[1,0,0]
	v_pk_fma_f32 v[146:147], v[146:147], s[8:9], s[8:9] op_sel_hi:[1,0,0]
	v_pk_fma_f32 v[148:149], v[148:149], s[8:9], s[8:9] op_sel_hi:[1,0,0]
	v_pk_fma_f32 v[150:151], v[150:151], s[8:9], s[8:9] op_sel_hi:[1,0,0]
	v_pk_fma_f32 v[152:153], v[152:153], s[8:9], s[8:9] op_sel_hi:[1,0,0]
	v_pk_fma_f32 v[154:155], v[154:155], s[8:9], s[8:9] op_sel_hi:[1,0,0]
	v_rcp_f32_e32 v140, v140
	v_rcp_f32_e32 v141, v141
	v_rcp_f32_e32 v142, v142
	v_rcp_f32_e32 v143, v143
	v_rcp_f32_e32 v144, v144
	v_rcp_f32_e32 v145, v145
	v_rcp_f32_e32 v146, v146
	v_rcp_f32_e32 v147, v147
	v_rcp_f32_e32 v148, v148
	v_rcp_f32_e32 v149, v149
	v_rcp_f32_e32 v150, v150
	v_rcp_f32_e32 v151, v151
	v_rcp_f32_e32 v152, v152
	v_rcp_f32_e32 v153, v153
	v_rcp_f32_e32 v154, v154
	v_rcp_f32_e32 v155, v155
	s_mov_b64 s[0:1], 0x2c000
	v_lshl_add_u64 v[136:137], v[134:135], 0, s[0:1]
	v_cvt_rpi_i32_f32_sdwa v156, v140 dst_sel:BYTE_0 dst_unused:UNUSED_PAD src0_sel:DWORD
	v_cvt_rpi_i32_f32_sdwa v157, v144 dst_sel:BYTE_0 dst_unused:UNUSED_PAD src0_sel:DWORD
	v_cvt_rpi_i32_f32_sdwa v158, v148 dst_sel:BYTE_0 dst_unused:UNUSED_PAD src0_sel:DWORD
	v_cvt_rpi_i32_f32_sdwa v159, v152 dst_sel:BYTE_0 dst_unused:UNUSED_PAD src0_sel:DWORD
	v_cvt_rpi_i32_f32_sdwa v156, v141 dst_sel:BYTE_1 dst_unused:UNUSED_PRESERVE src0_sel:DWORD
	v_cvt_rpi_i32_f32_sdwa v157, v145 dst_sel:BYTE_1 dst_unused:UNUSED_PRESERVE src0_sel:DWORD
	v_cvt_rpi_i32_f32_sdwa v158, v149 dst_sel:BYTE_1 dst_unused:UNUSED_PRESERVE src0_sel:DWORD
	v_cvt_rpi_i32_f32_sdwa v159, v153 dst_sel:BYTE_1 dst_unused:UNUSED_PRESERVE src0_sel:DWORD
	v_cvt_rpi_i32_f32_sdwa v156, v142 dst_sel:BYTE_2 dst_unused:UNUSED_PRESERVE src0_sel:DWORD
	v_cvt_rpi_i32_f32_sdwa v157, v146 dst_sel:BYTE_2 dst_unused:UNUSED_PRESERVE src0_sel:DWORD
	v_cvt_rpi_i32_f32_sdwa v158, v150 dst_sel:BYTE_2 dst_unused:UNUSED_PRESERVE src0_sel:DWORD
	v_cvt_rpi_i32_f32_sdwa v159, v154 dst_sel:BYTE_2 dst_unused:UNUSED_PRESERVE src0_sel:DWORD
	v_cvt_rpi_i32_f32_sdwa v156, v143 dst_sel:BYTE_3 dst_unused:UNUSED_PRESERVE src0_sel:DWORD
	v_cvt_rpi_i32_f32_sdwa v157, v147 dst_sel:BYTE_3 dst_unused:UNUSED_PRESERVE src0_sel:DWORD
	v_cvt_rpi_i32_f32_sdwa v158, v151 dst_sel:BYTE_3 dst_unused:UNUSED_PRESERVE src0_sel:DWORD
	v_cvt_rpi_i32_f32_sdwa v159, v155 dst_sel:BYTE_3 dst_unused:UNUSED_PRESERVE src0_sel:DWORD
	s_nop 0
	global_store_dwordx2 v[136:137], v[156:157], off
	global_store_dwordx2 v[136:137], v[158:159], off offset:128
	s_nop 1
	s_mov_b64 s[0:1], 0
.LBB0_401:
	s_andn2_b64 vcc, exec, s[0:1]
	s_cbranch_vccnz .LBB0_537
	ds_read_b32 v156, v205
	s_mov_b32 s0, 0xe000000
	s_cmp_lt_i32 s70, 4
	s_cselect_b32 s0, 0xc000000, s0
	s_cmp_lt_i32 s70, 2
	s_cselect_b32 s0, 0xa000000, s0
	s_and_b32 s1, s70, 1
	s_lshl_b32 s1, s1, 9
	s_add_i32 s0, s0, s1
	s_add_u32 s0, s16, s0
	s_addc_u32 s1, s17, 0
	v_ashrrev_i32_e32 v133, 31, v132
	v_lshlrev_b64 v[134:135], 10, v[132:133]
	v_lshl_add_u64 v[136:137], v[172:173], 1, s[0:1]
	v_lshl_add_u64 v[134:135], v[136:137], 0, v[134:135]
	s_lshl_b32 s8, s70, 3
	s_add_i32 s8, s74, s8
	s_ashr_i32 s9, s8, 31
	s_lshl_b64 s[8:9], s[8:9], 2
	s_add_u32 s38, s75, s8
	s_addc_u32 s39, s76, s9
	v_lshlrev_b64 v[138:139], 6, v[132:133]
	v_lshl_add_u64 v[138:139], v[138:139], 0, s[38:39]
	s_cmp_lt_i32 s70, 2
	s_cbranch_scc1 .Lt8_gelu
	s_cmp_lt_i32 s70, 4
	s_cbranch_scc1 .Lt8_gstat
; __device__ __forceinline__ u32x4 pack8(const f32x4 a, const f32x4 b) { u32x4 w; w.x = cvt_pk_bf16(a[0], a[1]); w.y = cvt_pk_bf16(a[2], a[3]); w.z = cvt_pk_bf16(b[0], b[1]); w.w = cvt_pk_bf16(b[2], b[3]); return w; }
;     ...
;         for (int m = 0; m < 4; ++m) { bf16_t* rowp = base + (size_t)(row0 + ai * HALF + m * 16) * ldc + col0; float ls1 = 0.f, ls2 = 0.f; const float rf = rsr[ai * HALF + m * 16];
; #pragma unroll
;             for (int bj = 0; bj < 2; ++bj) { f32x4 v0 = acc[ai][bj][m][0] * rf, v1 = acc[ai][bj][m][1] * rf;
;                 if (act != 0) {
; #pragma unroll
;                     for (int e = 0; e < 4; ++e) { const float x0 = v0[e], x1 = v1[e];
;                         const float r0 = __builtin_amdgcn_rcpf(1.0f + __builtin_amdgcn_exp2f(x0 * (c0 + c1 * x0 * x0))), r1 = __builtin_amdgcn_rcpf(1.0f + __builtin_amdgcn_exp2f(x1 * (c0 + c1 * x1 * x1)));
;                         v0[e] = act == 1 ? x0 * r0 : r0; v1[e] = act == 1 ? x1 * r1 : r1; } }
;                 if (stat) {
; #pragma unroll
;                     for (int e = 0; e < 4; ++e) { ls1 += v0[e] + v1[e]; ls2 += v0[e] * v0[e] + v1[e] * v1[e]; } }
;                 *(u32x4*)(rowp + bj * HALF) = pack8(v0, v1); }
	s_waitcnt lgkmcnt(0)
	ds_read_b32 v157, v205 offset:64
	v_pk_mul_f32 v[128:129], v[128:129], v[156:157] op_sel_hi:[1,0]
	v_pk_mul_f32 v[130:131], v[130:131], v[156:157] op_sel_hi:[1,0]
	v_pk_mul_f32 v[124:125], v[124:125], v[156:157] op_sel_hi:[1,0]
	v_pk_mul_f32 v[126:127], v[126:127], v[156:157] op_sel_hi:[1,0]
	v_pk_mul_f32 v[120:121], v[120:121], v[156:157] op_sel_hi:[1,0]
	v_pk_mul_f32 v[122:123], v[122:123], v[156:157] op_sel_hi:[1,0]
	v_pk_mul_f32 v[116:117], v[116:117], v[156:157] op_sel_hi:[1,0]
	v_pk_mul_f32 v[118:119], v[118:119], v[156:157] op_sel_hi:[1,0]
	v_cvt_pk_bf16_f32 v128, v128, v129
	v_cvt_pk_bf16_f32 v129, v130, v131
	v_cvt_pk_bf16_f32 v130, v124, v125
	v_cvt_pk_bf16_f32 v131, v126, v127
	global_store_dwordx4 v[134:135], v[128:131], off
	v_cvt_pk_bf16_f32 v120, v120, v121
	v_cvt_pk_bf16_f32 v121, v122, v123
	v_cvt_pk_bf16_f32 v122, v116, v117
	v_cvt_pk_bf16_f32 v123, v118, v119
	global_store_dwordx4 v[134:135], v[120:123], off offset:256
	s_waitcnt lgkmcnt(0)
	v_mov_b32_e32 v156, v157
	ds_read_b32 v157, v205 offset:128
	v_pk_mul_f32 v[112:113], v[112:113], v[156:157] op_sel_hi:[1,0]
	v_pk_mul_f32 v[114:115], v[114:115], v[156:157] op_sel_hi:[1,0]
	v_pk_mul_f32 v[108:109], v[108:109], v[156:157] op_sel_hi:[1,0]
	v_pk_mul_f32 v[110:111], v[110:111], v[156:157] op_sel_hi:[1,0]
	v_pk_mul_f32 v[104:105], v[104:105], v[156:157] op_sel_hi:[1,0]
	v_pk_mul_f32 v[106:107], v[106:107], v[156:157] op_sel_hi:[1,0]
	v_pk_mul_f32 v[100:101], v[100:101], v[156:157] op_sel_hi:[1,0]
	v_pk_mul_f32 v[102:103], v[102:103], v[156:157] op_sel_hi:[1,0]
	s_mov_b64 s[0:1], 0x4000
	v_lshl_add_u64 v[136:137], v[134:135], 0, s[0:1]
	v_cvt_pk_bf16_f32 v112, v112, v113
	v_cvt_pk_bf16_f32 v113, v114, v115
	v_cvt_pk_bf16_f32 v114, v108, v109
	v_cvt_pk_bf16_f32 v115, v110, v111
	global_store_dwordx4 v[136:137], v[112:115], off
	v_cvt_pk_bf16_f32 v104, v104, v105
	v_cvt_pk_bf16_f32 v105, v106, v107
	v_cvt_pk_bf16_f32 v106, v100, v101
	v_cvt_pk_bf16_f32 v107, v102, v103
	global_store_dwordx4 v[136:137], v[104:107], off offset:256
	s_waitcnt lgkmcnt(0)
	v_mov_b32_e32 v156, v157
	ds_read_b32 v157, v205 offset:192
	v_pk_mul_f32 v[96:97], v[96:97], v[156:157] op_sel_hi:[1,0]
	v_pk_mul_f32 v[98:99], v[98:99], v[156:157] op_sel_hi:[1,0]
	v_pk_mul_f32 v[92:93], v[92:93], v[156:157] op_sel_hi:[1,0]
	v_pk_mul_f32 v[94:95], v[94:95], v[156:157] op_sel_hi:[1,0]
	v_pk_mul_f32 v[88:89], v[88:89], v[156:157] op_sel_hi:[1,0]
	v_pk_mul_f32 v[90:91], v[90:91], v[156:157] op_sel_hi:[1,0]
	v_pk_mul_f32 v[84:85], v[84:85], v[156:157] op_sel_hi:[1,0]
	v_pk_mul_f32 v[86:87], v[86:87], v[156:157] op_sel_hi:[1,0]
	s_mov_b64 s[0:1], 0x8000
	v_lshl_add_u64 v[136:137], v[134:135], 0, s[0:1]
	v_cvt_pk_bf16_f32 v96, v96, v97
	v_cvt_pk_bf16_f32 v97, v98, v99
	v_cvt_pk_bf16_f32 v98, v92, v93
	v_cvt_pk_bf16_f32 v99, v94, v95
	global_store_dwordx4 v[136:137], v[96:99], off
	v_cvt_pk_bf16_f32 v88, v88, v89
	v_cvt_pk_bf16_f32 v89, v90, v91
	v_cvt_pk_bf16_f32 v90, v84, v85
	v_cvt_pk_bf16_f32 v91, v86, v87
	global_store_dwordx4 v[136:137], v[88:91], off offset:256
	s_waitcnt lgkmcnt(0)
	v_mov_b32_e32 v156, v157
	ds_read_b32 v157, v205 offset:512
	v_pk_mul_f32 v[80:81], v[80:81], v[156:157] op_sel_hi:[1,0]
	v_pk_mul_f32 v[82:83], v[82:83], v[156:157] op_sel_hi:[1,0]
	v_pk_mul_f32 v[76:77], v[76:77], v[156:157] op_sel_hi:[1,0]
	v_pk_mul_f32 v[78:79], v[78:79], v[156:157] op_sel_hi:[1,0]
	v_pk_mul_f32 v[72:73], v[72:73], v[156:157] op_sel_hi:[1,0]
	v_pk_mul_f32 v[74:75], v[74:75], v[156:157] op_sel_hi:[1,0]
	v_pk_mul_f32 v[68:69], v[68:69], v[156:157] op_sel_hi:[1,0]
	v_pk_mul_f32 v[70:71], v[70:71], v[156:157] op_sel_hi:[1,0]
	s_mov_b64 s[0:1], 0xc000
	v_lshl_add_u64 v[136:137], v[134:135], 0, s[0:1]
	v_cvt_pk_bf16_f32 v80, v80, v81
	v_cvt_pk_bf16_f32 v81, v82, v83
	v_cvt_pk_bf16_f32 v82, v76, v77
	v_cvt_pk_bf16_f32 v83, v78, v79
	global_store_dwordx4 v[136:137], v[80:83], off
	v_cvt_pk_bf16_f32 v72, v72, v73
	v_cvt_pk_bf16_f32 v73, v74, v75
	v_cvt_pk_bf16_f32 v74, v68, v69
	v_cvt_pk_bf16_f32 v75, v70, v71
	global_store_dwordx4 v[136:137], v[72:75], off offset:256
	s_waitcnt lgkmcnt(0)
	v_mov_b32_e32 v156, v157
	ds_read_b32 v157, v205 offset:576
	v_pk_mul_f32 v[64:65], v[64:65], v[156:157] op_sel_hi:[1,0]
	v_pk_mul_f32 v[66:67], v[66:67], v[156:157] op_sel_hi:[1,0]
	v_pk_mul_f32 v[60:61], v[60:61], v[156:157] op_sel_hi:[1,0]
	v_pk_mul_f32 v[62:63], v[62:63], v[156:157] op_sel_hi:[1,0]
	v_pk_mul_f32 v[56:57], v[56:57], v[156:157] op_sel_hi:[1,0]
	v_pk_mul_f32 v[58:59], v[58:59], v[156:157] op_sel_hi:[1,0]
	v_pk_mul_f32 v[52:53], v[52:53], v[156:157] op_sel_hi:[1,0]
	v_pk_mul_f32 v[54:55], v[54:55], v[156:157] op_sel_hi:[1,0]
	s_mov_b64 s[0:1], 0x20000
	v_lshl_add_u64 v[136:137], v[134:135], 0, s[0:1]
	v_cvt_pk_bf16_f32 v64, v64, v65
	v_cvt_pk_bf16_f32 v65, v66, v67
	v_cvt_pk_bf16_f32 v66, v60, v61
	v_cvt_pk_bf16_f32 v67, v62, v63
	global_store_dwordx4 v[136:137], v[64:67], off
	v_cvt_pk_bf16_f32 v56, v56, v57
	v_cvt_pk_bf16_f32 v57, v58, v59
	v_cvt_pk_bf16_f32 v58, v52, v53
	v_cvt_pk_bf16_f32 v59, v54, v55
	global_store_dwordx4 v[136:137], v[56:59], off offset:256
	s_waitcnt lgkmcnt(0)
	v_mov_b32_e32 v156, v157
	ds_read_b32 v157, v205 offset:640
	v_pk_mul_f32 v[48:49], v[48:49], v[156:157] op_sel_hi:[1,0]
	v_pk_mul_f32 v[50:51], v[50:51], v[156:157] op_sel_hi:[1,0]
	v_pk_mul_f32 v[44:45], v[44:45], v[156:157] op_sel_hi:[1,0]
	v_pk_mul_f32 v[46:47], v[46:47], v[156:157] op_sel_hi:[1,0]
	v_pk_mul_f32 v[40:41], v[40:41], v[156:157] op_sel_hi:[1,0]
	v_pk_mul_f32 v[42:43], v[42:43], v[156:157] op_sel_hi:[1,0]
	v_pk_mul_f32 v[36:37], v[36:37], v[156:157] op_sel_hi:[1,0]
	v_pk_mul_f32 v[38:39], v[38:39], v[156:157] op_sel_hi:[1,0]
	s_mov_b64 s[0:1], 0x24000
	v_lshl_add_u64 v[136:137], v[134:135], 0, s[0:1]
	v_cvt_pk_bf16_f32 v48, v48, v49
	v_cvt_pk_bf16_f32 v49, v50, v51
	v_cvt_pk_bf16_f32 v50, v44, v45
	v_cvt_pk_bf16_f32 v51, v46, v47
	global_store_dwordx4 v[136:137], v[48:51], off
	v_cvt_pk_bf16_f32 v40, v40, v41
	v_cvt_pk_bf16_f32 v41, v42, v43
	v_cvt_pk_bf16_f32 v42, v36, v37
	v_cvt_pk_bf16_f32 v43, v38, v39
	global_store_dwordx4 v[136:137], v[40:43], off offset:256
	s_waitcnt lgkmcnt(0)
; __device__ __forceinline__ u32x4 pack8(const f32x4 a, const f32x4 b) { u32x4 w; w.x = cvt_pk_bf16(a[0], a[1]); w.y = cvt_pk_bf16(a[2], a[3]); w.z = cvt_pk_bf16(b[0], b[1]); w.w = cvt_pk_bf16(b[2], b[3]); return w; }
; __device__ __forceinline__ float gelu_t(float x) { const float z = x * (-2.302208198f - 0.10294324f * x * x); return x * __builtin_amdgcn_rcpf(1.0f + __builtin_amdgcn_exp2f(z)); }
;     ...
;         for (int m = 0; m < 4; ++m) { bf16_t* rowp = base + (size_t)(row0 + ai * HALF + m * 16) * ldc + col0; float ls1 = 0.f, ls2 = 0.f; const float rf = rsr[ai * HALF + m * 16];
; #pragma unroll
;             for (int bj = 0; bj < 2; ++bj) { f32x4 v0 = acc[ai][bj][m][0] * rf, v1 = acc[ai][bj][m][1] * rf;
;                 if (act != 0) {
; #pragma unroll
;                     for (int e = 0; e < 4; ++e) { const float x0 = v0[e], x1 = v1[e];
;                         const float r0 = __builtin_amdgcn_rcpf(1.0f + __builtin_amdgcn_exp2f(x0 * (c0 + c1 * x0 * x0))), r1 = __builtin_amdgcn_rcpf(1.0f + __builtin_amdgcn_exp2f(x1 * (c0 + c1 * x1 * x1)));
;                         v0[e] = act == 1 ? x0 * r0 : r0; v1[e] = act == 1 ? x1 * r1 : r1; } }
;                 if (stat) {
; #pragma unroll
;                     for (int e = 0; e < 4; ++e) { ls1 += v0[e] + v1[e]; ls2 += v0[e] * v0[e] + v1[e] * v1[e]; } }
;                 *(u32x4*)(rowp + bj * HALF) = pack8(v0, v1); }
	v_mov_b32_e32 v156, v157
	ds_read_b32 v157, v205 offset:704
	v_pk_mul_f32 v[32:33], v[32:33], v[156:157] op_sel_hi:[1,0]
	v_pk_mul_f32 v[34:35], v[34:35], v[156:157] op_sel_hi:[1,0]
	v_pk_mul_f32 v[28:29], v[28:29], v[156:157] op_sel_hi:[1,0]
	v_pk_mul_f32 v[30:31], v[30:31], v[156:157] op_sel_hi:[1,0]
	v_pk_mul_f32 v[24:25], v[24:25], v[156:157] op_sel_hi:[1,0]
	v_pk_mul_f32 v[26:27], v[26:27], v[156:157] op_sel_hi:[1,0]
	v_pk_mul_f32 v[20:21], v[20:21], v[156:157] op_sel_hi:[1,0]
	v_pk_mul_f32 v[22:23], v[22:23], v[156:157] op_sel_hi:[1,0]
	s_mov_b64 s[0:1], 0x28000
	v_lshl_add_u64 v[136:137], v[134:135], 0, s[0:1]
	v_cvt_pk_bf16_f32 v32, v32, v33
	v_cvt_pk_bf16_f32 v33, v34, v35
	v_cvt_pk_bf16_f32 v34, v28, v29
	v_cvt_pk_bf16_f32 v35, v30, v31
	global_store_dwordx4 v[136:137], v[32:35], off
	v_cvt_pk_bf16_f32 v24, v24, v25
	v_cvt_pk_bf16_f32 v25, v26, v27
	v_cvt_pk_bf16_f32 v26, v20, v21
	v_cvt_pk_bf16_f32 v27, v22, v23
	global_store_dwordx4 v[136:137], v[24:27], off offset:256
	s_waitcnt lgkmcnt(0)
	v_mov_b32_e32 v156, v157
	v_pk_mul_f32 v[16:17], v[16:17], v[156:157] op_sel_hi:[1,0]
	v_pk_mul_f32 v[18:19], v[18:19], v[156:157] op_sel_hi:[1,0]
	v_pk_mul_f32 v[12:13], v[12:13], v[156:157] op_sel_hi:[1,0]
	v_pk_mul_f32 v[14:15], v[14:15], v[156:157] op_sel_hi:[1,0]
	v_pk_mul_f32 v[8:9], v[8:9], v[156:157] op_sel_hi:[1,0]
	v_pk_mul_f32 v[10:11], v[10:11], v[156:157] op_sel_hi:[1,0]
	v_pk_mul_f32 v[4:5], v[4:5], v[156:157] op_sel_hi:[1,0]
	v_pk_mul_f32 v[6:7], v[6:7], v[156:157] op_sel_hi:[1,0]
	s_mov_b64 s[0:1], 0x2c000
	v_lshl_add_u64 v[136:137], v[134:135], 0, s[0:1]
	v_cvt_pk_bf16_f32 v16, v16, v17
	v_cvt_pk_bf16_f32 v17, v18, v19
	v_cvt_pk_bf16_f32 v18, v12, v13
	v_cvt_pk_bf16_f32 v19, v14, v15
	global_store_dwordx4 v[136:137], v[16:19], off
	v_cvt_pk_bf16_f32 v8, v8, v9
	v_cvt_pk_bf16_f32 v9, v10, v11
	v_cvt_pk_bf16_f32 v10, v4, v5
	v_cvt_pk_bf16_f32 v11, v6, v7
	global_store_dwordx4 v[136:137], v[8:11], off offset:256
	s_branch .Lt8_end
.Lt8_gelu:
	s_waitcnt lgkmcnt(0)
	ds_read_b32 v157, v205 offset:64
	v_mul_f32_e32 v188, v156, v156
	v_mul_f32_e32 v186, 0xc0135761, v156
	v_rcp_f32_e32 v190, v156
	v_mul_f32_e32 v188, v188, v156
	v_mul_f32_e32 v188, 0xbdd2d3e8, v188
	v_pk_mul_f32 v[140:141], v[128:129], v[128:129]
	v_pk_mul_f32 v[142:143], v[130:131], v[130:131]
	v_pk_mul_f32 v[144:145], v[124:125], v[124:125]
	v_pk_mul_f32 v[146:147], v[126:127], v[126:127]
	v_pk_mul_f32 v[148:149], v[120:121], v[120:121]
	v_pk_mul_f32 v[150:151], v[122:123], v[122:123]
	v_pk_mul_f32 v[152:153], v[116:117], v[116:117]
	v_pk_mul_f32 v[154:155], v[118:119], v[118:119]
	v_pk_fma_f32 v[140:141], v[140:141], v[188:189], v[186:187] op_sel_hi:[1,0,0]
	v_pk_fma_f32 v[142:143], v[142:143], v[188:189], v[186:187] op_sel_hi:[1,0,0]
	v_pk_fma_f32 v[144:145], v[144:145], v[188:189], v[186:187] op_sel_hi:[1,0,0]
	v_pk_fma_f32 v[146:147], v[146:147], v[188:189], v[186:187] op_sel_hi:[1,0,0]
	v_pk_fma_f32 v[148:149], v[148:149], v[188:189], v[186:187] op_sel_hi:[1,0,0]
	v_pk_fma_f32 v[150:151], v[150:151], v[188:189], v[186:187] op_sel_hi:[1,0,0]
	v_pk_fma_f32 v[152:153], v[152:153], v[188:189], v[186:187] op_sel_hi:[1,0,0]
	v_pk_fma_f32 v[154:155], v[154:155], v[188:189], v[186:187] op_sel_hi:[1,0,0]
	v_pk_mul_f32 v[140:141], v[128:129], v[140:141]
	v_pk_mul_f32 v[142:143], v[130:131], v[142:143]
	v_pk_mul_f32 v[144:145], v[124:125], v[144:145]
	v_pk_mul_f32 v[146:147], v[126:127], v[146:147]
	v_pk_mul_f32 v[148:149], v[120:121], v[148:149]
	v_pk_mul_f32 v[150:151], v[122:123], v[150:151]
	v_pk_mul_f32 v[152:153], v[116:117], v[152:153]
	v_pk_mul_f32 v[154:155], v[118:119], v[154:155]
	v_exp_f32_e32 v140, v140
	v_exp_f32_e32 v141, v141
	v_exp_f32_e32 v142, v142
	v_exp_f32_e32 v143, v143
	v_exp_f32_e32 v144, v144
	v_exp_f32_e32 v145, v145
	v_exp_f32_e32 v146, v146
	v_exp_f32_e32 v147, v147
	v_exp_f32_e32 v148, v148
	v_exp_f32_e32 v149, v149
	v_exp_f32_e32 v150, v150
	v_exp_f32_e32 v151, v151
	v_exp_f32_e32 v152, v152
	v_exp_f32_e32 v153, v153
	v_exp_f32_e32 v154, v154
	v_exp_f32_e32 v155, v155
	v_pk_fma_f32 v[140:141], v[140:141], v[190:191], v[190:191] op_sel_hi:[1,0,0]
	v_pk_fma_f32 v[142:143], v[142:143], v[190:191], v[190:191] op_sel_hi:[1,0,0]
	v_pk_fma_f32 v[144:145], v[144:145], v[190:191], v[190:191] op_sel_hi:[1,0,0]
	v_pk_fma_f32 v[146:147], v[146:147], v[190:191], v[190:191] op_sel_hi:[1,0,0]
	v_pk_fma_f32 v[148:149], v[148:149], v[190:191], v[190:191] op_sel_hi:[1,0,0]
	v_pk_fma_f32 v[150:151], v[150:151], v[190:191], v[190:191] op_sel_hi:[1,0,0]
	v_pk_fma_f32 v[152:153], v[152:153], v[190:191], v[190:191] op_sel_hi:[1,0,0]
	v_pk_fma_f32 v[154:155], v[154:155], v[190:191], v[190:191] op_sel_hi:[1,0,0]
	v_rcp_f32_e32 v140, v140
	v_rcp_f32_e32 v141, v141
	v_rcp_f32_e32 v142, v142
	v_rcp_f32_e32 v143, v143
	v_rcp_f32_e32 v144, v144
	v_rcp_f32_e32 v145, v145
	v_rcp_f32_e32 v146, v146
	v_rcp_f32_e32 v147, v147
	v_rcp_f32_e32 v148, v148
	v_rcp_f32_e32 v149, v149
	v_rcp_f32_e32 v150, v150
	v_rcp_f32_e32 v151, v151
	v_rcp_f32_e32 v152, v152
	v_rcp_f32_e32 v153, v153
	v_rcp_f32_e32 v154, v154
	v_rcp_f32_e32 v155, v155
	v_pk_mul_f32 v[128:129], v[128:129], v[140:141]
	v_pk_mul_f32 v[130:131], v[130:131], v[142:143]
	v_pk_mul_f32 v[124:125], v[124:125], v[144:145]
	v_pk_mul_f32 v[126:127], v[126:127], v[146:147]
	v_pk_mul_f32 v[120:121], v[120:121], v[148:149]
	v_pk_mul_f32 v[122:123], v[122:123], v[150:151]
	v_pk_mul_f32 v[116:117], v[116:117], v[152:153]
	v_pk_mul_f32 v[118:119], v[118:119], v[154:155]
	v_cvt_pk_bf16_f32 v128, v128, v129
	v_cvt_pk_bf16_f32 v129, v130, v131
	v_cvt_pk_bf16_f32 v130, v124, v125
	v_cvt_pk_bf16_f32 v131, v126, v127
	global_store_dwordx4 v[134:135], v[128:131], off
	v_cvt_pk_bf16_f32 v120, v120, v121
	v_cvt_pk_bf16_f32 v121, v122, v123
	v_cvt_pk_bf16_f32 v122, v116, v117
	v_cvt_pk_bf16_f32 v123, v118, v119
	global_store_dwordx4 v[134:135], v[120:123], off offset:256
	s_waitcnt lgkmcnt(0)
; __device__ __forceinline__ u32x4 pack8(const f32x4 a, const f32x4 b) { u32x4 w; w.x = cvt_pk_bf16(a[0], a[1]); w.y = cvt_pk_bf16(a[2], a[3]); w.z = cvt_pk_bf16(b[0], b[1]); w.w = cvt_pk_bf16(b[2], b[3]); return w; }
; __device__ __forceinline__ float gelu_t(float x) { const float z = x * (-2.302208198f - 0.10294324f * x * x); return x * __builtin_amdgcn_rcpf(1.0f + __builtin_amdgcn_exp2f(z)); }
;     ...
;         for (int m = 0; m < 4; ++m) { bf16_t* rowp = base + (size_t)(row0 + ai * HALF + m * 16) * ldc + col0; float ls1 = 0.f, ls2 = 0.f; const float rf = rsr[ai * HALF + m * 16];
; #pragma unroll
;             for (int bj = 0; bj < 2; ++bj) { f32x4 v0 = acc[ai][bj][m][0] * rf, v1 = acc[ai][bj][m][1] * rf;
;                 if (act != 0) {
; #pragma unroll
;                     for (int e = 0; e < 4; ++e) { const float x0 = v0[e], x1 = v1[e];
;                         const float r0 = __builtin_amdgcn_rcpf(1.0f + __builtin_amdgcn_exp2f(x0 * (c0 + c1 * x0 * x0))), r1 = __builtin_amdgcn_rcpf(1.0f + __builtin_amdgcn_exp2f(x1 * (c0 + c1 * x1 * x1)));
;                         v0[e] = act == 1 ? x0 * r0 : r0; v1[e] = act == 1 ? x1 * r1 : r1; } }
;                 if (stat) {
; #pragma unroll
;                     for (int e = 0; e < 4; ++e) { ls1 += v0[e] + v1[e]; ls2 += v0[e] * v0[e] + v1[e] * v1[e]; } }
;                 *(u32x4*)(rowp + bj * HALF) = pack8(v0, v1); }
	v_mov_b32_e32 v156, v157
	ds_read_b32 v157, v205 offset:128
	v_mul_f32_e32 v188, v156, v156
	v_mul_f32_e32 v186, 0xc0135761, v156
	v_rcp_f32_e32 v190, v156
	v_mul_f32_e32 v188, v188, v156
	v_mul_f32_e32 v188, 0xbdd2d3e8, v188
	v_pk_mul_f32 v[140:141], v[112:113], v[112:113]
	v_pk_mul_f32 v[142:143], v[114:115], v[114:115]
	v_pk_mul_f32 v[144:145], v[108:109], v[108:109]
	v_pk_mul_f32 v[146:147], v[110:111], v[110:111]
	v_pk_mul_f32 v[148:149], v[104:105], v[104:105]
	v_pk_mul_f32 v[150:151], v[106:107], v[106:107]
	v_pk_mul_f32 v[152:153], v[100:101], v[100:101]
	v_pk_mul_f32 v[154:155], v[102:103], v[102:103]
	v_pk_fma_f32 v[140:141], v[140:141], v[188:189], v[186:187] op_sel_hi:[1,0,0]
	v_pk_fma_f32 v[142:143], v[142:143], v[188:189], v[186:187] op_sel_hi:[1,0,0]
	v_pk_fma_f32 v[144:145], v[144:145], v[188:189], v[186:187] op_sel_hi:[1,0,0]
	v_pk_fma_f32 v[146:147], v[146:147], v[188:189], v[186:187] op_sel_hi:[1,0,0]
	v_pk_fma_f32 v[148:149], v[148:149], v[188:189], v[186:187] op_sel_hi:[1,0,0]
	v_pk_fma_f32 v[150:151], v[150:151], v[188:189], v[186:187] op_sel_hi:[1,0,0]
	v_pk_fma_f32 v[152:153], v[152:153], v[188:189], v[186:187] op_sel_hi:[1,0,0]
	v_pk_fma_f32 v[154:155], v[154:155], v[188:189], v[186:187] op_sel_hi:[1,0,0]
	v_pk_mul_f32 v[140:141], v[112:113], v[140:141]
	v_pk_mul_f32 v[142:143], v[114:115], v[142:143]
	v_pk_mul_f32 v[144:145], v[108:109], v[144:145]
	v_pk_mul_f32 v[146:147], v[110:111], v[146:147]
	v_pk_mul_f32 v[148:149], v[104:105], v[148:149]
	v_pk_mul_f32 v[150:151], v[106:107], v[150:151]
	v_pk_mul_f32 v[152:153], v[100:101], v[152:153]
	v_pk_mul_f32 v[154:155], v[102:103], v[154:155]
	v_exp_f32_e32 v140, v140
	v_exp_f32_e32 v141, v141
	v_exp_f32_e32 v142, v142
	v_exp_f32_e32 v143, v143
	v_exp_f32_e32 v144, v144
	v_exp_f32_e32 v145, v145
	v_exp_f32_e32 v146, v146
	v_exp_f32_e32 v147, v147
	v_exp_f32_e32 v148, v148
	v_exp_f32_e32 v149, v149
	v_exp_f32_e32 v150, v150
	v_exp_f32_e32 v151, v151
	v_exp_f32_e32 v152, v152
	v_exp_f32_e32 v153, v153
	v_exp_f32_e32 v154, v154
	v_exp_f32_e32 v155, v155
	v_pk_fma_f32 v[140:141], v[140:141], v[190:191], v[190:191] op_sel_hi:[1,0,0]
	v_pk_fma_f32 v[142:143], v[142:143], v[190:191], v[190:191] op_sel_hi:[1,0,0]
	v_pk_fma_f32 v[144:145], v[144:145], v[190:191], v[190:191] op_sel_hi:[1,0,0]
	v_pk_fma_f32 v[146:147], v[146:147], v[190:191], v[190:191] op_sel_hi:[1,0,0]
	v_pk_fma_f32 v[148:149], v[148:149], v[190:191], v[190:191] op_sel_hi:[1,0,0]
	v_pk_fma_f32 v[150:151], v[150:151], v[190:191], v[190:191] op_sel_hi:[1,0,0]
	v_pk_fma_f32 v[152:153], v[152:153], v[190:191], v[190:191] op_sel_hi:[1,0,0]
	v_pk_fma_f32 v[154:155], v[154:155], v[190:191], v[190:191] op_sel_hi:[1,0,0]
	v_rcp_f32_e32 v140, v140
	v_rcp_f32_e32 v141, v141
	v_rcp_f32_e32 v142, v142
	v_rcp_f32_e32 v143, v143
	v_rcp_f32_e32 v144, v144
	v_rcp_f32_e32 v145, v145
	v_rcp_f32_e32 v146, v146
	v_rcp_f32_e32 v147, v147
	v_rcp_f32_e32 v148, v148
	v_rcp_f32_e32 v149, v149
	v_rcp_f32_e32 v150, v150
	v_rcp_f32_e32 v151, v151
	v_rcp_f32_e32 v152, v152
	v_rcp_f32_e32 v153, v153
	v_rcp_f32_e32 v154, v154
	v_rcp_f32_e32 v155, v155
	v_pk_mul_f32 v[112:113], v[112:113], v[140:141]
	v_pk_mul_f32 v[114:115], v[114:115], v[142:143]
	v_pk_mul_f32 v[108:109], v[108:109], v[144:145]
	v_pk_mul_f32 v[110:111], v[110:111], v[146:147]
	v_pk_mul_f32 v[104:105], v[104:105], v[148:149]
	v_pk_mul_f32 v[106:107], v[106:107], v[150:151]
	v_pk_mul_f32 v[100:101], v[100:101], v[152:153]
	v_pk_mul_f32 v[102:103], v[102:103], v[154:155]
	s_mov_b64 s[0:1], 0x4000
	v_lshl_add_u64 v[136:137], v[134:135], 0, s[0:1]
	v_cvt_pk_bf16_f32 v112, v112, v113
	v_cvt_pk_bf16_f32 v113, v114, v115
	v_cvt_pk_bf16_f32 v114, v108, v109
	v_cvt_pk_bf16_f32 v115, v110, v111
	global_store_dwordx4 v[136:137], v[112:115], off
	v_cvt_pk_bf16_f32 v104, v104, v105
	v_cvt_pk_bf16_f32 v105, v106, v107
	v_cvt_pk_bf16_f32 v106, v100, v101
	v_cvt_pk_bf16_f32 v107, v102, v103
	global_store_dwordx4 v[136:137], v[104:107], off offset:256
	s_waitcnt lgkmcnt(0)
	v_mov_b32_e32 v156, v157
	ds_read_b32 v157, v205 offset:192
	v_mul_f32_e32 v188, v156, v156
	v_mul_f32_e32 v186, 0xc0135761, v156
	v_rcp_f32_e32 v190, v156
	v_mul_f32_e32 v188, v188, v156
	v_mul_f32_e32 v188, 0xbdd2d3e8, v188
	v_pk_mul_f32 v[140:141], v[96:97], v[96:97]
	v_pk_mul_f32 v[142:143], v[98:99], v[98:99]
	v_pk_mul_f32 v[144:145], v[92:93], v[92:93]
	v_pk_mul_f32 v[146:147], v[94:95], v[94:95]
	v_pk_mul_f32 v[148:149], v[88:89], v[88:89]
	v_pk_mul_f32 v[150:151], v[90:91], v[90:91]
	v_pk_mul_f32 v[152:153], v[84:85], v[84:85]
	v_pk_mul_f32 v[154:155], v[86:87], v[86:87]
	v_pk_fma_f32 v[140:141], v[140:141], v[188:189], v[186:187] op_sel_hi:[1,0,0]
	v_pk_fma_f32 v[142:143], v[142:143], v[188:189], v[186:187] op_sel_hi:[1,0,0]
	v_pk_fma_f32 v[144:145], v[144:145], v[188:189], v[186:187] op_sel_hi:[1,0,0]
	v_pk_fma_f32 v[146:147], v[146:147], v[188:189], v[186:187] op_sel_hi:[1,0,0]
	v_pk_fma_f32 v[148:149], v[148:149], v[188:189], v[186:187] op_sel_hi:[1,0,0]
	v_pk_fma_f32 v[150:151], v[150:151], v[188:189], v[186:187] op_sel_hi:[1,0,0]
	v_pk_fma_f32 v[152:153], v[152:153], v[188:189], v[186:187] op_sel_hi:[1,0,0]
	v_pk_fma_f32 v[154:155], v[154:155], v[188:189], v[186:187] op_sel_hi:[1,0,0]
	v_pk_mul_f32 v[140:141], v[96:97], v[140:141]
	v_pk_mul_f32 v[142:143], v[98:99], v[142:143]
	v_pk_mul_f32 v[144:145], v[92:93], v[144:145]
	v_pk_mul_f32 v[146:147], v[94:95], v[146:147]
	v_pk_mul_f32 v[148:149], v[88:89], v[148:149]
	v_pk_mul_f32 v[150:151], v[90:91], v[150:151]
	v_pk_mul_f32 v[152:153], v[84:85], v[152:153]
	v_pk_mul_f32 v[154:155], v[86:87], v[154:155]
	v_exp_f32_e32 v140, v140
	v_exp_f32_e32 v141, v141
; __device__ __forceinline__ u32x4 pack8(const f32x4 a, const f32x4 b) { u32x4 w; w.x = cvt_pk_bf16(a[0], a[1]); w.y = cvt_pk_bf16(a[2], a[3]); w.z = cvt_pk_bf16(b[0], b[1]); w.w = cvt_pk_bf16(b[2], b[3]); return w; }
; __device__ __forceinline__ float gelu_t(float x) { const float z = x * (-2.302208198f - 0.10294324f * x * x); return x * __builtin_amdgcn_rcpf(1.0f + __builtin_amdgcn_exp2f(z)); }
;     ...
;         for (int m = 0; m < 4; ++m) { bf16_t* rowp = base + (size_t)(row0 + ai * HALF + m * 16) * ldc + col0; float ls1 = 0.f, ls2 = 0.f; const float rf = rsr[ai * HALF + m * 16];
; #pragma unroll
;             for (int bj = 0; bj < 2; ++bj) { f32x4 v0 = acc[ai][bj][m][0] * rf, v1 = acc[ai][bj][m][1] * rf;
;                 if (act != 0) {
; #pragma unroll
;                     for (int e = 0; e < 4; ++e) { const float x0 = v0[e], x1 = v1[e];
;                         const float r0 = __builtin_amdgcn_rcpf(1.0f + __builtin_amdgcn_exp2f(x0 * (c0 + c1 * x0 * x0))), r1 = __builtin_amdgcn_rcpf(1.0f + __builtin_amdgcn_exp2f(x1 * (c0 + c1 * x1 * x1)));
;                         v0[e] = act == 1 ? x0 * r0 : r0; v1[e] = act == 1 ? x1 * r1 : r1; } }
;                 if (stat) {
; #pragma unroll
;                     for (int e = 0; e < 4; ++e) { ls1 += v0[e] + v1[e]; ls2 += v0[e] * v0[e] + v1[e] * v1[e]; } }
;                 *(u32x4*)(rowp + bj * HALF) = pack8(v0, v1); }
	v_exp_f32_e32 v142, v142
	v_exp_f32_e32 v143, v143
	v_exp_f32_e32 v144, v144
	v_exp_f32_e32 v145, v145
	v_exp_f32_e32 v146, v146
	v_exp_f32_e32 v147, v147
	v_exp_f32_e32 v148, v148
	v_exp_f32_e32 v149, v149
	v_exp_f32_e32 v150, v150
	v_exp_f32_e32 v151, v151
	v_exp_f32_e32 v152, v152
	v_exp_f32_e32 v153, v153
	v_exp_f32_e32 v154, v154
	v_exp_f32_e32 v155, v155
	v_pk_fma_f32 v[140:141], v[140:141], v[190:191], v[190:191] op_sel_hi:[1,0,0]
	v_pk_fma_f32 v[142:143], v[142:143], v[190:191], v[190:191] op_sel_hi:[1,0,0]
	v_pk_fma_f32 v[144:145], v[144:145], v[190:191], v[190:191] op_sel_hi:[1,0,0]
	v_pk_fma_f32 v[146:147], v[146:147], v[190:191], v[190:191] op_sel_hi:[1,0,0]
	v_pk_fma_f32 v[148:149], v[148:149], v[190:191], v[190:191] op_sel_hi:[1,0,0]
	v_pk_fma_f32 v[150:151], v[150:151], v[190:191], v[190:191] op_sel_hi:[1,0,0]
	v_pk_fma_f32 v[152:153], v[152:153], v[190:191], v[190:191] op_sel_hi:[1,0,0]
	v_pk_fma_f32 v[154:155], v[154:155], v[190:191], v[190:191] op_sel_hi:[1,0,0]
	v_rcp_f32_e32 v140, v140
	v_rcp_f32_e32 v141, v141
	v_rcp_f32_e32 v142, v142
	v_rcp_f32_e32 v143, v143
	v_rcp_f32_e32 v144, v144
	v_rcp_f32_e32 v145, v145
	v_rcp_f32_e32 v146, v146
	v_rcp_f32_e32 v147, v147
	v_rcp_f32_e32 v148, v148
	v_rcp_f32_e32 v149, v149
	v_rcp_f32_e32 v150, v150
	v_rcp_f32_e32 v151, v151
	v_rcp_f32_e32 v152, v152
	v_rcp_f32_e32 v153, v153
	v_rcp_f32_e32 v154, v154
	v_rcp_f32_e32 v155, v155
	v_pk_mul_f32 v[96:97], v[96:97], v[140:141]
	v_pk_mul_f32 v[98:99], v[98:99], v[142:143]
	v_pk_mul_f32 v[92:93], v[92:93], v[144:145]
	v_pk_mul_f32 v[94:95], v[94:95], v[146:147]
	v_pk_mul_f32 v[88:89], v[88:89], v[148:149]
	v_pk_mul_f32 v[90:91], v[90:91], v[150:151]
	v_pk_mul_f32 v[84:85], v[84:85], v[152:153]
	v_pk_mul_f32 v[86:87], v[86:87], v[154:155]
	s_mov_b64 s[0:1], 0x8000
	v_lshl_add_u64 v[136:137], v[134:135], 0, s[0:1]
	v_cvt_pk_bf16_f32 v96, v96, v97
	v_cvt_pk_bf16_f32 v97, v98, v99
	v_cvt_pk_bf16_f32 v98, v92, v93
	v_cvt_pk_bf16_f32 v99, v94, v95
	global_store_dwordx4 v[136:137], v[96:99], off
	v_cvt_pk_bf16_f32 v88, v88, v89
	v_cvt_pk_bf16_f32 v89, v90, v91
	v_cvt_pk_bf16_f32 v90, v84, v85
	v_cvt_pk_bf16_f32 v91, v86, v87
	global_store_dwordx4 v[136:137], v[88:91], off offset:256
	s_waitcnt lgkmcnt(0)
	v_mov_b32_e32 v156, v157
	ds_read_b32 v157, v205 offset:512
	v_mul_f32_e32 v188, v156, v156
	v_mul_f32_e32 v186, 0xc0135761, v156
	v_rcp_f32_e32 v190, v156
	v_mul_f32_e32 v188, v188, v156
	v_mul_f32_e32 v188, 0xbdd2d3e8, v188
	v_pk_mul_f32 v[140:141], v[80:81], v[80:81]
	v_pk_mul_f32 v[142:143], v[82:83], v[82:83]
	v_pk_mul_f32 v[144:145], v[76:77], v[76:77]
	v_pk_mul_f32 v[146:147], v[78:79], v[78:79]
	v_pk_mul_f32 v[148:149], v[72:73], v[72:73]
	v_pk_mul_f32 v[150:151], v[74:75], v[74:75]
	v_pk_mul_f32 v[152:153], v[68:69], v[68:69]
	v_pk_mul_f32 v[154:155], v[70:71], v[70:71]
	v_pk_fma_f32 v[140:141], v[140:141], v[188:189], v[186:187] op_sel_hi:[1,0,0]
	v_pk_fma_f32 v[142:143], v[142:143], v[188:189], v[186:187] op_sel_hi:[1,0,0]
	v_pk_fma_f32 v[144:145], v[144:145], v[188:189], v[186:187] op_sel_hi:[1,0,0]
	v_pk_fma_f32 v[146:147], v[146:147], v[188:189], v[186:187] op_sel_hi:[1,0,0]
	v_pk_fma_f32 v[148:149], v[148:149], v[188:189], v[186:187] op_sel_hi:[1,0,0]
	v_pk_fma_f32 v[150:151], v[150:151], v[188:189], v[186:187] op_sel_hi:[1,0,0]
	v_pk_fma_f32 v[152:153], v[152:153], v[188:189], v[186:187] op_sel_hi:[1,0,0]
	v_pk_fma_f32 v[154:155], v[154:155], v[188:189], v[186:187] op_sel_hi:[1,0,0]
	v_pk_mul_f32 v[140:141], v[80:81], v[140:141]
	v_pk_mul_f32 v[142:143], v[82:83], v[142:143]
	v_pk_mul_f32 v[144:145], v[76:77], v[144:145]
	v_pk_mul_f32 v[146:147], v[78:79], v[146:147]
	v_pk_mul_f32 v[148:149], v[72:73], v[148:149]
	v_pk_mul_f32 v[150:151], v[74:75], v[150:151]
	v_pk_mul_f32 v[152:153], v[68:69], v[152:153]
	v_pk_mul_f32 v[154:155], v[70:71], v[154:155]
	v_exp_f32_e32 v140, v140
	v_exp_f32_e32 v141, v141
	v_exp_f32_e32 v142, v142
	v_exp_f32_e32 v143, v143
	v_exp_f32_e32 v144, v144
	v_exp_f32_e32 v145, v145
	v_exp_f32_e32 v146, v146
	v_exp_f32_e32 v147, v147
	v_exp_f32_e32 v148, v148
	v_exp_f32_e32 v149, v149
	v_exp_f32_e32 v150, v150
	v_exp_f32_e32 v151, v151
	v_exp_f32_e32 v152, v152
	v_exp_f32_e32 v153, v153
	v_exp_f32_e32 v154, v154
	v_exp_f32_e32 v155, v155
	v_pk_fma_f32 v[140:141], v[140:141], v[190:191], v[190:191] op_sel_hi:[1,0,0]
	v_pk_fma_f32 v[142:143], v[142:143], v[190:191], v[190:191] op_sel_hi:[1,0,0]
	v_pk_fma_f32 v[144:145], v[144:145], v[190:191], v[190:191] op_sel_hi:[1,0,0]
	v_pk_fma_f32 v[146:147], v[146:147], v[190:191], v[190:191] op_sel_hi:[1,0,0]
	v_pk_fma_f32 v[148:149], v[148:149], v[190:191], v[190:191] op_sel_hi:[1,0,0]
	v_pk_fma_f32 v[150:151], v[150:151], v[190:191], v[190:191] op_sel_hi:[1,0,0]
	v_pk_fma_f32 v[152:153], v[152:153], v[190:191], v[190:191] op_sel_hi:[1,0,0]
	v_pk_fma_f32 v[154:155], v[154:155], v[190:191], v[190:191] op_sel_hi:[1,0,0]
	v_rcp_f32_e32 v140, v140
	v_rcp_f32_e32 v141, v141
	v_rcp_f32_e32 v142, v142
	v_rcp_f32_e32 v143, v143
	v_rcp_f32_e32 v144, v144
	v_rcp_f32_e32 v145, v145
	v_rcp_f32_e32 v146, v146
	v_rcp_f32_e32 v147, v147
	v_rcp_f32_e32 v148, v148
	v_rcp_f32_e32 v149, v149
	v_rcp_f32_e32 v150, v150
	v_rcp_f32_e32 v151, v151
	v_rcp_f32_e32 v152, v152
	v_rcp_f32_e32 v153, v153
	v_rcp_f32_e32 v154, v154
	v_rcp_f32_e32 v155, v155
	v_pk_mul_f32 v[80:81], v[80:81], v[140:141]
	v_pk_mul_f32 v[82:83], v[82:83], v[142:143]
	v_pk_mul_f32 v[76:77], v[76:77], v[144:145]
	v_pk_mul_f32 v[78:79], v[78:79], v[146:147]
	v_pk_mul_f32 v[72:73], v[72:73], v[148:149]
	v_pk_mul_f32 v[74:75], v[74:75], v[150:151]
	v_pk_mul_f32 v[68:69], v[68:69], v[152:153]
	v_pk_mul_f32 v[70:71], v[70:71], v[154:155]
	s_mov_b64 s[0:1], 0xc000
	v_lshl_add_u64 v[136:137], v[134:135], 0, s[0:1]
	v_cvt_pk_bf16_f32 v80, v80, v81
	v_cvt_pk_bf16_f32 v81, v82, v83
	v_cvt_pk_bf16_f32 v82, v76, v77
	v_cvt_pk_bf16_f32 v83, v78, v79
	global_store_dwordx4 v[136:137], v[80:83], off
	v_cvt_pk_bf16_f32 v72, v72, v73
	v_cvt_pk_bf16_f32 v73, v74, v75
	v_cvt_pk_bf16_f32 v74, v68, v69
	v_cvt_pk_bf16_f32 v75, v70, v71
	global_store_dwordx4 v[136:137], v[72:75], off offset:256
	s_waitcnt lgkmcnt(0)
; __device__ __forceinline__ u32x4 pack8(const f32x4 a, const f32x4 b) { u32x4 w; w.x = cvt_pk_bf16(a[0], a[1]); w.y = cvt_pk_bf16(a[2], a[3]); w.z = cvt_pk_bf16(b[0], b[1]); w.w = cvt_pk_bf16(b[2], b[3]); return w; }
; __device__ __forceinline__ float gelu_t(float x) { const float z = x * (-2.302208198f - 0.10294324f * x * x); return x * __builtin_amdgcn_rcpf(1.0f + __builtin_amdgcn_exp2f(z)); }
;     ...
;         for (int m = 0; m < 4; ++m) { bf16_t* rowp = base + (size_t)(row0 + ai * HALF + m * 16) * ldc + col0; float ls1 = 0.f, ls2 = 0.f; const float rf = rsr[ai * HALF + m * 16];
; #pragma unroll
;             for (int bj = 0; bj < 2; ++bj) { f32x4 v0 = acc[ai][bj][m][0] * rf, v1 = acc[ai][bj][m][1] * rf;
;                 if (act != 0) {
; #pragma unroll
;                     for (int e = 0; e < 4; ++e) { const float x0 = v0[e], x1 = v1[e];
;                         const float r0 = __builtin_amdgcn_rcpf(1.0f + __builtin_amdgcn_exp2f(x0 * (c0 + c1 * x0 * x0))), r1 = __builtin_amdgcn_rcpf(1.0f + __builtin_amdgcn_exp2f(x1 * (c0 + c1 * x1 * x1)));
;                         v0[e] = act == 1 ? x0 * r0 : r0; v1[e] = act == 1 ? x1 * r1 : r1; } }
;                 if (stat) {
; #pragma unroll
;                     for (int e = 0; e < 4; ++e) { ls1 += v0[e] + v1[e]; ls2 += v0[e] * v0[e] + v1[e] * v1[e]; } }
;                 *(u32x4*)(rowp + bj * HALF) = pack8(v0, v1); }
	v_mov_b32_e32 v156, v157
	ds_read_b32 v157, v205 offset:576
	v_mul_f32_e32 v188, v156, v156
	v_mul_f32_e32 v186, 0xc0135761, v156
	v_rcp_f32_e32 v190, v156
	v_mul_f32_e32 v188, v188, v156
	v_mul_f32_e32 v188, 0xbdd2d3e8, v188
	v_pk_mul_f32 v[140:141], v[64:65], v[64:65]
	v_pk_mul_f32 v[142:143], v[66:67], v[66:67]
	v_pk_mul_f32 v[144:145], v[60:61], v[60:61]
	v_pk_mul_f32 v[146:147], v[62:63], v[62:63]
	v_pk_mul_f32 v[148:149], v[56:57], v[56:57]
	v_pk_mul_f32 v[150:151], v[58:59], v[58:59]
	v_pk_mul_f32 v[152:153], v[52:53], v[52:53]
	v_pk_mul_f32 v[154:155], v[54:55], v[54:55]
	v_pk_fma_f32 v[140:141], v[140:141], v[188:189], v[186:187] op_sel_hi:[1,0,0]
	v_pk_fma_f32 v[142:143], v[142:143], v[188:189], v[186:187] op_sel_hi:[1,0,0]
	v_pk_fma_f32 v[144:145], v[144:145], v[188:189], v[186:187] op_sel_hi:[1,0,0]
	v_pk_fma_f32 v[146:147], v[146:147], v[188:189], v[186:187] op_sel_hi:[1,0,0]
	v_pk_fma_f32 v[148:149], v[148:149], v[188:189], v[186:187] op_sel_hi:[1,0,0]
	v_pk_fma_f32 v[150:151], v[150:151], v[188:189], v[186:187] op_sel_hi:[1,0,0]
	v_pk_fma_f32 v[152:153], v[152:153], v[188:189], v[186:187] op_sel_hi:[1,0,0]
	v_pk_fma_f32 v[154:155], v[154:155], v[188:189], v[186:187] op_sel_hi:[1,0,0]
	v_pk_mul_f32 v[140:141], v[64:65], v[140:141]
	v_pk_mul_f32 v[142:143], v[66:67], v[142:143]
	v_pk_mul_f32 v[144:145], v[60:61], v[144:145]
	v_pk_mul_f32 v[146:147], v[62:63], v[146:147]
	v_pk_mul_f32 v[148:149], v[56:57], v[148:149]
	v_pk_mul_f32 v[150:151], v[58:59], v[150:151]
	v_pk_mul_f32 v[152:153], v[52:53], v[152:153]
	v_pk_mul_f32 v[154:155], v[54:55], v[154:155]
	v_exp_f32_e32 v140, v140
	v_exp_f32_e32 v141, v141
	v_exp_f32_e32 v142, v142
	v_exp_f32_e32 v143, v143
	v_exp_f32_e32 v144, v144
	v_exp_f32_e32 v145, v145
	v_exp_f32_e32 v146, v146
	v_exp_f32_e32 v147, v147
	v_exp_f32_e32 v148, v148
	v_exp_f32_e32 v149, v149
	v_exp_f32_e32 v150, v150
	v_exp_f32_e32 v151, v151
	v_exp_f32_e32 v152, v152
	v_exp_f32_e32 v153, v153
	v_exp_f32_e32 v154, v154
	v_exp_f32_e32 v155, v155
	v_pk_fma_f32 v[140:141], v[140:141], v[190:191], v[190:191] op_sel_hi:[1,0,0]
	v_pk_fma_f32 v[142:143], v[142:143], v[190:191], v[190:191] op_sel_hi:[1,0,0]
	v_pk_fma_f32 v[144:145], v[144:145], v[190:191], v[190:191] op_sel_hi:[1,0,0]
	v_pk_fma_f32 v[146:147], v[146:147], v[190:191], v[190:191] op_sel_hi:[1,0,0]
	v_pk_fma_f32 v[148:149], v[148:149], v[190:191], v[190:191] op_sel_hi:[1,0,0]
	v_pk_fma_f32 v[150:151], v[150:151], v[190:191], v[190:191] op_sel_hi:[1,0,0]
	v_pk_fma_f32 v[152:153], v[152:153], v[190:191], v[190:191] op_sel_hi:[1,0,0]
	v_pk_fma_f32 v[154:155], v[154:155], v[190:191], v[190:191] op_sel_hi:[1,0,0]
	v_rcp_f32_e32 v140, v140
	v_rcp_f32_e32 v141, v141
	v_rcp_f32_e32 v142, v142
	v_rcp_f32_e32 v143, v143
	v_rcp_f32_e32 v144, v144
	v_rcp_f32_e32 v145, v145
	v_rcp_f32_e32 v146, v146
	v_rcp_f32_e32 v147, v147
	v_rcp_f32_e32 v148, v148
	v_rcp_f32_e32 v149, v149
	v_rcp_f32_e32 v150, v150
	v_rcp_f32_e32 v151, v151
	v_rcp_f32_e32 v152, v152
	v_rcp_f32_e32 v153, v153
	v_rcp_f32_e32 v154, v154
	v_rcp_f32_e32 v155, v155
	v_pk_mul_f32 v[64:65], v[64:65], v[140:141]
	v_pk_mul_f32 v[66:67], v[66:67], v[142:143]
	v_pk_mul_f32 v[60:61], v[60:61], v[144:145]
	v_pk_mul_f32 v[62:63], v[62:63], v[146:147]
	v_pk_mul_f32 v[56:57], v[56:57], v[148:149]
	v_pk_mul_f32 v[58:59], v[58:59], v[150:151]
	v_pk_mul_f32 v[52:53], v[52:53], v[152:153]
	v_pk_mul_f32 v[54:55], v[54:55], v[154:155]
	s_mov_b64 s[0:1], 0x20000
	v_lshl_add_u64 v[136:137], v[134:135], 0, s[0:1]
	v_cvt_pk_bf16_f32 v64, v64, v65
	v_cvt_pk_bf16_f32 v65, v66, v67
	v_cvt_pk_bf16_f32 v66, v60, v61
	v_cvt_pk_bf16_f32 v67, v62, v63
	global_store_dwordx4 v[136:137], v[64:67], off
	v_cvt_pk_bf16_f32 v56, v56, v57
	v_cvt_pk_bf16_f32 v57, v58, v59
	v_cvt_pk_bf16_f32 v58, v52, v53
	v_cvt_pk_bf16_f32 v59, v54, v55
	global_store_dwordx4 v[136:137], v[56:59], off offset:256
	s_waitcnt lgkmcnt(0)
	v_mov_b32_e32 v156, v157
	ds_read_b32 v157, v205 offset:640
	v_mul_f32_e32 v188, v156, v156
	v_mul_f32_e32 v186, 0xc0135761, v156
	v_rcp_f32_e32 v190, v156
	v_mul_f32_e32 v188, v188, v156
	v_mul_f32_e32 v188, 0xbdd2d3e8, v188
	v_pk_mul_f32 v[140:141], v[48:49], v[48:49]
	v_pk_mul_f32 v[142:143], v[50:51], v[50:51]
	v_pk_mul_f32 v[144:145], v[44:45], v[44:45]
	v_pk_mul_f32 v[146:147], v[46:47], v[46:47]
	v_pk_mul_f32 v[148:149], v[40:41], v[40:41]
	v_pk_mul_f32 v[150:151], v[42:43], v[42:43]
	v_pk_mul_f32 v[152:153], v[36:37], v[36:37]
	v_pk_mul_f32 v[154:155], v[38:39], v[38:39]
	v_pk_fma_f32 v[140:141], v[140:141], v[188:189], v[186:187] op_sel_hi:[1,0,0]
	v_pk_fma_f32 v[142:143], v[142:143], v[188:189], v[186:187] op_sel_hi:[1,0,0]
	v_pk_fma_f32 v[144:145], v[144:145], v[188:189], v[186:187] op_sel_hi:[1,0,0]
	v_pk_fma_f32 v[146:147], v[146:147], v[188:189], v[186:187] op_sel_hi:[1,0,0]
	v_pk_fma_f32 v[148:149], v[148:149], v[188:189], v[186:187] op_sel_hi:[1,0,0]
	v_pk_fma_f32 v[150:151], v[150:151], v[188:189], v[186:187] op_sel_hi:[1,0,0]
	v_pk_fma_f32 v[152:153], v[152:153], v[188:189], v[186:187] op_sel_hi:[1,0,0]
	v_pk_fma_f32 v[154:155], v[154:155], v[188:189], v[186:187] op_sel_hi:[1,0,0]
	v_pk_mul_f32 v[140:141], v[48:49], v[140:141]
	v_pk_mul_f32 v[142:143], v[50:51], v[142:143]
	v_pk_mul_f32 v[144:145], v[44:45], v[144:145]
	v_pk_mul_f32 v[146:147], v[46:47], v[146:147]
	v_pk_mul_f32 v[148:149], v[40:41], v[148:149]
	v_pk_mul_f32 v[150:151], v[42:43], v[150:151]
	v_pk_mul_f32 v[152:153], v[36:37], v[152:153]
	v_pk_mul_f32 v[154:155], v[38:39], v[154:155]
	v_exp_f32_e32 v140, v140
	v_exp_f32_e32 v141, v141
	v_exp_f32_e32 v142, v142
	v_exp_f32_e32 v143, v143
	v_exp_f32_e32 v144, v144
	v_exp_f32_e32 v145, v145
; __device__ __forceinline__ u32x4 pack8(const f32x4 a, const f32x4 b) { u32x4 w; w.x = cvt_pk_bf16(a[0], a[1]); w.y = cvt_pk_bf16(a[2], a[3]); w.z = cvt_pk_bf16(b[0], b[1]); w.w = cvt_pk_bf16(b[2], b[3]); return w; }
; __device__ __forceinline__ float gelu_t(float x) { const float z = x * (-2.302208198f - 0.10294324f * x * x); return x * __builtin_amdgcn_rcpf(1.0f + __builtin_amdgcn_exp2f(z)); }
;     ...
;         for (int m = 0; m < 4; ++m) { bf16_t* rowp = base + (size_t)(row0 + ai * HALF + m * 16) * ldc + col0; float ls1 = 0.f, ls2 = 0.f; const float rf = rsr[ai * HALF + m * 16];
; #pragma unroll
;             for (int bj = 0; bj < 2; ++bj) { f32x4 v0 = acc[ai][bj][m][0] * rf, v1 = acc[ai][bj][m][1] * rf;
;                 if (act != 0) {
; #pragma unroll
;                     for (int e = 0; e < 4; ++e) { const float x0 = v0[e], x1 = v1[e];
;                         const float r0 = __builtin_amdgcn_rcpf(1.0f + __builtin_amdgcn_exp2f(x0 * (c0 + c1 * x0 * x0))), r1 = __builtin_amdgcn_rcpf(1.0f + __builtin_amdgcn_exp2f(x1 * (c0 + c1 * x1 * x1)));
;                         v0[e] = act == 1 ? x0 * r0 : r0; v1[e] = act == 1 ? x1 * r1 : r1; } }
;                 if (stat) {
; #pragma unroll
;                     for (int e = 0; e < 4; ++e) { ls1 += v0[e] + v1[e]; ls2 += v0[e] * v0[e] + v1[e] * v1[e]; } }
;                 *(u32x4*)(rowp + bj * HALF) = pack8(v0, v1); }
	v_exp_f32_e32 v146, v146
	v_exp_f32_e32 v147, v147
	v_exp_f32_e32 v148, v148
	v_exp_f32_e32 v149, v149
	v_exp_f32_e32 v150, v150
	v_exp_f32_e32 v151, v151
	v_exp_f32_e32 v152, v152
	v_exp_f32_e32 v153, v153
	v_exp_f32_e32 v154, v154
	v_exp_f32_e32 v155, v155
	v_pk_fma_f32 v[140:141], v[140:141], v[190:191], v[190:191] op_sel_hi:[1,0,0]
	v_pk_fma_f32 v[142:143], v[142:143], v[190:191], v[190:191] op_sel_hi:[1,0,0]
	v_pk_fma_f32 v[144:145], v[144:145], v[190:191], v[190:191] op_sel_hi:[1,0,0]
	v_pk_fma_f32 v[146:147], v[146:147], v[190:191], v[190:191] op_sel_hi:[1,0,0]
	v_pk_fma_f32 v[148:149], v[148:149], v[190:191], v[190:191] op_sel_hi:[1,0,0]
	v_pk_fma_f32 v[150:151], v[150:151], v[190:191], v[190:191] op_sel_hi:[1,0,0]
	v_pk_fma_f32 v[152:153], v[152:153], v[190:191], v[190:191] op_sel_hi:[1,0,0]
	v_pk_fma_f32 v[154:155], v[154:155], v[190:191], v[190:191] op_sel_hi:[1,0,0]
	v_rcp_f32_e32 v140, v140
	v_rcp_f32_e32 v141, v141
	v_rcp_f32_e32 v142, v142
	v_rcp_f32_e32 v143, v143
	v_rcp_f32_e32 v144, v144
	v_rcp_f32_e32 v145, v145
	v_rcp_f32_e32 v146, v146
	v_rcp_f32_e32 v147, v147
	v_rcp_f32_e32 v148, v148
	v_rcp_f32_e32 v149, v149
	v_rcp_f32_e32 v150, v150
	v_rcp_f32_e32 v151, v151
	v_rcp_f32_e32 v152, v152
	v_rcp_f32_e32 v153, v153
	v_rcp_f32_e32 v154, v154
	v_rcp_f32_e32 v155, v155
	v_pk_mul_f32 v[48:49], v[48:49], v[140:141]
	v_pk_mul_f32 v[50:51], v[50:51], v[142:143]
	v_pk_mul_f32 v[44:45], v[44:45], v[144:145]
	v_pk_mul_f32 v[46:47], v[46:47], v[146:147]
	v_pk_mul_f32 v[40:41], v[40:41], v[148:149]
	v_pk_mul_f32 v[42:43], v[42:43], v[150:151]
	v_pk_mul_f32 v[36:37], v[36:37], v[152:153]
	v_pk_mul_f32 v[38:39], v[38:39], v[154:155]
	s_mov_b64 s[0:1], 0x24000
	v_lshl_add_u64 v[136:137], v[134:135], 0, s[0:1]
	v_cvt_pk_bf16_f32 v48, v48, v49
	v_cvt_pk_bf16_f32 v49, v50, v51
	v_cvt_pk_bf16_f32 v50, v44, v45
	v_cvt_pk_bf16_f32 v51, v46, v47
	global_store_dwordx4 v[136:137], v[48:51], off
	v_cvt_pk_bf16_f32 v40, v40, v41
	v_cvt_pk_bf16_f32 v41, v42, v43
	v_cvt_pk_bf16_f32 v42, v36, v37
	v_cvt_pk_bf16_f32 v43, v38, v39
	global_store_dwordx4 v[136:137], v[40:43], off offset:256
	s_waitcnt lgkmcnt(0)
	v_mov_b32_e32 v156, v157
	ds_read_b32 v157, v205 offset:704
	v_mul_f32_e32 v188, v156, v156
	v_mul_f32_e32 v186, 0xc0135761, v156
	v_rcp_f32_e32 v190, v156
	v_mul_f32_e32 v188, v188, v156
	v_mul_f32_e32 v188, 0xbdd2d3e8, v188
	v_pk_mul_f32 v[140:141], v[32:33], v[32:33]
	v_pk_mul_f32 v[142:143], v[34:35], v[34:35]
	v_pk_mul_f32 v[144:145], v[28:29], v[28:29]
	v_pk_mul_f32 v[146:147], v[30:31], v[30:31]
	v_pk_mul_f32 v[148:149], v[24:25], v[24:25]
	v_pk_mul_f32 v[150:151], v[26:27], v[26:27]
	v_pk_mul_f32 v[152:153], v[20:21], v[20:21]
	v_pk_mul_f32 v[154:155], v[22:23], v[22:23]
	v_pk_fma_f32 v[140:141], v[140:141], v[188:189], v[186:187] op_sel_hi:[1,0,0]
	v_pk_fma_f32 v[142:143], v[142:143], v[188:189], v[186:187] op_sel_hi:[1,0,0]
	v_pk_fma_f32 v[144:145], v[144:145], v[188:189], v[186:187] op_sel_hi:[1,0,0]
	v_pk_fma_f32 v[146:147], v[146:147], v[188:189], v[186:187] op_sel_hi:[1,0,0]
	v_pk_fma_f32 v[148:149], v[148:149], v[188:189], v[186:187] op_sel_hi:[1,0,0]
	v_pk_fma_f32 v[150:151], v[150:151], v[188:189], v[186:187] op_sel_hi:[1,0,0]
	v_pk_fma_f32 v[152:153], v[152:153], v[188:189], v[186:187] op_sel_hi:[1,0,0]
	v_pk_fma_f32 v[154:155], v[154:155], v[188:189], v[186:187] op_sel_hi:[1,0,0]
	v_pk_mul_f32 v[140:141], v[32:33], v[140:141]
	v_pk_mul_f32 v[142:143], v[34:35], v[142:143]
	v_pk_mul_f32 v[144:145], v[28:29], v[144:145]
	v_pk_mul_f32 v[146:147], v[30:31], v[146:147]
	v_pk_mul_f32 v[148:149], v[24:25], v[148:149]
	v_pk_mul_f32 v[150:151], v[26:27], v[150:151]
	v_pk_mul_f32 v[152:153], v[20:21], v[152:153]
	v_pk_mul_f32 v[154:155], v[22:23], v[154:155]
	v_exp_f32_e32 v140, v140
	v_exp_f32_e32 v141, v141
	v_exp_f32_e32 v142, v142
	v_exp_f32_e32 v143, v143
	v_exp_f32_e32 v144, v144
	v_exp_f32_e32 v145, v145
	v_exp_f32_e32 v146, v146
	v_exp_f32_e32 v147, v147
	v_exp_f32_e32 v148, v148
	v_exp_f32_e32 v149, v149
	v_exp_f32_e32 v150, v150
	v_exp_f32_e32 v151, v151
	v_exp_f32_e32 v152, v152
	v_exp_f32_e32 v153, v153
	v_exp_f32_e32 v154, v154
	v_exp_f32_e32 v155, v155
	v_pk_fma_f32 v[140:141], v[140:141], v[190:191], v[190:191] op_sel_hi:[1,0,0]
	v_pk_fma_f32 v[142:143], v[142:143], v[190:191], v[190:191] op_sel_hi:[1,0,0]
	v_pk_fma_f32 v[144:145], v[144:145], v[190:191], v[190:191] op_sel_hi:[1,0,0]
	v_pk_fma_f32 v[146:147], v[146:147], v[190:191], v[190:191] op_sel_hi:[1,0,0]
	v_pk_fma_f32 v[148:149], v[148:149], v[190:191], v[190:191] op_sel_hi:[1,0,0]
	v_pk_fma_f32 v[150:151], v[150:151], v[190:191], v[190:191] op_sel_hi:[1,0,0]
	v_pk_fma_f32 v[152:153], v[152:153], v[190:191], v[190:191] op_sel_hi:[1,0,0]
	v_pk_fma_f32 v[154:155], v[154:155], v[190:191], v[190:191] op_sel_hi:[1,0,0]
	v_rcp_f32_e32 v140, v140
	v_rcp_f32_e32 v141, v141
	v_rcp_f32_e32 v142, v142
	v_rcp_f32_e32 v143, v143
	v_rcp_f32_e32 v144, v144
	v_rcp_f32_e32 v145, v145
	v_rcp_f32_e32 v146, v146
	v_rcp_f32_e32 v147, v147
	v_rcp_f32_e32 v148, v148
	v_rcp_f32_e32 v149, v149
	v_rcp_f32_e32 v150, v150
	v_rcp_f32_e32 v151, v151
	v_rcp_f32_e32 v152, v152
	v_rcp_f32_e32 v153, v153
	v_rcp_f32_e32 v154, v154
	v_rcp_f32_e32 v155, v155
	v_pk_mul_f32 v[32:33], v[32:33], v[140:141]
	v_pk_mul_f32 v[34:35], v[34:35], v[142:143]
	v_pk_mul_f32 v[28:29], v[28:29], v[144:145]
	v_pk_mul_f32 v[30:31], v[30:31], v[146:147]
	v_pk_mul_f32 v[24:25], v[24:25], v[148:149]
	v_pk_mul_f32 v[26:27], v[26:27], v[150:151]
	v_pk_mul_f32 v[20:21], v[20:21], v[152:153]
	v_pk_mul_f32 v[22:23], v[22:23], v[154:155]
	s_mov_b64 s[0:1], 0x28000
	v_lshl_add_u64 v[136:137], v[134:135], 0, s[0:1]
	v_cvt_pk_bf16_f32 v32, v32, v33
	v_cvt_pk_bf16_f32 v33, v34, v35
	v_cvt_pk_bf16_f32 v34, v28, v29
	v_cvt_pk_bf16_f32 v35, v30, v31
	global_store_dwordx4 v[136:137], v[32:35], off
	v_cvt_pk_bf16_f32 v24, v24, v25
	v_cvt_pk_bf16_f32 v25, v26, v27
	v_cvt_pk_bf16_f32 v26, v20, v21
	v_cvt_pk_bf16_f32 v27, v22, v23
	global_store_dwordx4 v[136:137], v[24:27], off offset:256
	s_waitcnt lgkmcnt(0)
; __device__ __forceinline__ u32x4 pack8(const f32x4 a, const f32x4 b) { u32x4 w; w.x = cvt_pk_bf16(a[0], a[1]); w.y = cvt_pk_bf16(a[2], a[3]); w.z = cvt_pk_bf16(b[0], b[1]); w.w = cvt_pk_bf16(b[2], b[3]); return w; }
; __device__ __forceinline__ float gelu_t(float x) { const float z = x * (-2.302208198f - 0.10294324f * x * x); return x * __builtin_amdgcn_rcpf(1.0f + __builtin_amdgcn_exp2f(z)); }
;     ...
;         for (int m = 0; m < 4; ++m) { bf16_t* rowp = base + (size_t)(row0 + ai * HALF + m * 16) * ldc + col0; float ls1 = 0.f, ls2 = 0.f; const float rf = rsr[ai * HALF + m * 16];
; #pragma unroll
;             for (int bj = 0; bj < 2; ++bj) { f32x4 v0 = acc[ai][bj][m][0] * rf, v1 = acc[ai][bj][m][1] * rf;
;                 if (act != 0) {
; #pragma unroll
;                     for (int e = 0; e < 4; ++e) { const float x0 = v0[e], x1 = v1[e];
;                         const float r0 = __builtin_amdgcn_rcpf(1.0f + __builtin_amdgcn_exp2f(x0 * (c0 + c1 * x0 * x0))), r1 = __builtin_amdgcn_rcpf(1.0f + __builtin_amdgcn_exp2f(x1 * (c0 + c1 * x1 * x1)));
;                         v0[e] = act == 1 ? x0 * r0 : r0; v1[e] = act == 1 ? x1 * r1 : r1; } }
;                 if (stat) {
; #pragma unroll
;                     for (int e = 0; e < 4; ++e) { ls1 += v0[e] + v1[e]; ls2 += v0[e] * v0[e] + v1[e] * v1[e]; } }
;                 *(u32x4*)(rowp + bj * HALF) = pack8(v0, v1); }
	v_mov_b32_e32 v156, v157
	v_mul_f32_e32 v188, v156, v156
	v_mul_f32_e32 v186, 0xc0135761, v156
	v_rcp_f32_e32 v190, v156
	v_mul_f32_e32 v188, v188, v156
	v_mul_f32_e32 v188, 0xbdd2d3e8, v188
	v_pk_mul_f32 v[140:141], v[16:17], v[16:17]
	v_pk_mul_f32 v[142:143], v[18:19], v[18:19]
	v_pk_mul_f32 v[144:145], v[12:13], v[12:13]
	v_pk_mul_f32 v[146:147], v[14:15], v[14:15]
	v_pk_mul_f32 v[148:149], v[8:9], v[8:9]
	v_pk_mul_f32 v[150:151], v[10:11], v[10:11]
	v_pk_mul_f32 v[152:153], v[4:5], v[4:5]
	v_pk_mul_f32 v[154:155], v[6:7], v[6:7]
	v_pk_fma_f32 v[140:141], v[140:141], v[188:189], v[186:187] op_sel_hi:[1,0,0]
	v_pk_fma_f32 v[142:143], v[142:143], v[188:189], v[186:187] op_sel_hi:[1,0,0]
	v_pk_fma_f32 v[144:145], v[144:145], v[188:189], v[186:187] op_sel_hi:[1,0,0]
	v_pk_fma_f32 v[146:147], v[146:147], v[188:189], v[186:187] op_sel_hi:[1,0,0]
	v_pk_fma_f32 v[148:149], v[148:149], v[188:189], v[186:187] op_sel_hi:[1,0,0]
	v_pk_fma_f32 v[150:151], v[150:151], v[188:189], v[186:187] op_sel_hi:[1,0,0]
	v_pk_fma_f32 v[152:153], v[152:153], v[188:189], v[186:187] op_sel_hi:[1,0,0]
	v_pk_fma_f32 v[154:155], v[154:155], v[188:189], v[186:187] op_sel_hi:[1,0,0]
	v_pk_mul_f32 v[140:141], v[16:17], v[140:141]
	v_pk_mul_f32 v[142:143], v[18:19], v[142:143]
	v_pk_mul_f32 v[144:145], v[12:13], v[144:145]
	v_pk_mul_f32 v[146:147], v[14:15], v[146:147]
	v_pk_mul_f32 v[148:149], v[8:9], v[148:149]
	v_pk_mul_f32 v[150:151], v[10:11], v[150:151]
	v_pk_mul_f32 v[152:153], v[4:5], v[152:153]
	v_pk_mul_f32 v[154:155], v[6:7], v[154:155]
	v_exp_f32_e32 v140, v140
	v_exp_f32_e32 v141, v141
	v_exp_f32_e32 v142, v142
	v_exp_f32_e32 v143, v143
	v_exp_f32_e32 v144, v144
	v_exp_f32_e32 v145, v145
	v_exp_f32_e32 v146, v146
	v_exp_f32_e32 v147, v147
	v_exp_f32_e32 v148, v148
	v_exp_f32_e32 v149, v149
	v_exp_f32_e32 v150, v150
	v_exp_f32_e32 v151, v151
	v_exp_f32_e32 v152, v152
	v_exp_f32_e32 v153, v153
	v_exp_f32_e32 v154, v154
	v_exp_f32_e32 v155, v155
	v_pk_fma_f32 v[140:141], v[140:141], v[190:191], v[190:191] op_sel_hi:[1,0,0]
	v_pk_fma_f32 v[142:143], v[142:143], v[190:191], v[190:191] op_sel_hi:[1,0,0]
	v_pk_fma_f32 v[144:145], v[144:145], v[190:191], v[190:191] op_sel_hi:[1,0,0]
	v_pk_fma_f32 v[146:147], v[146:147], v[190:191], v[190:191] op_sel_hi:[1,0,0]
	v_pk_fma_f32 v[148:149], v[148:149], v[190:191], v[190:191] op_sel_hi:[1,0,0]
	v_pk_fma_f32 v[150:151], v[150:151], v[190:191], v[190:191] op_sel_hi:[1,0,0]
	v_pk_fma_f32 v[152:153], v[152:153], v[190:191], v[190:191] op_sel_hi:[1,0,0]
	v_pk_fma_f32 v[154:155], v[154:155], v[190:191], v[190:191] op_sel_hi:[1,0,0]
	v_rcp_f32_e32 v140, v140
	v_rcp_f32_e32 v141, v141
	v_rcp_f32_e32 v142, v142
	v_rcp_f32_e32 v143, v143
	v_rcp_f32_e32 v144, v144
	v_rcp_f32_e32 v145, v145
	v_rcp_f32_e32 v146, v146
	v_rcp_f32_e32 v147, v147
	v_rcp_f32_e32 v148, v148
	v_rcp_f32_e32 v149, v149
	v_rcp_f32_e32 v150, v150
	v_rcp_f32_e32 v151, v151
	v_rcp_f32_e32 v152, v152
	v_rcp_f32_e32 v153, v153
	v_rcp_f32_e32 v154, v154
	v_rcp_f32_e32 v155, v155
	v_pk_mul_f32 v[16:17], v[16:17], v[140:141]
	v_pk_mul_f32 v[18:19], v[18:19], v[142:143]
	v_pk_mul_f32 v[12:13], v[12:13], v[144:145]
	v_pk_mul_f32 v[14:15], v[14:15], v[146:147]
	v_pk_mul_f32 v[8:9], v[8:9], v[148:149]
	v_pk_mul_f32 v[10:11], v[10:11], v[150:151]
	v_pk_mul_f32 v[4:5], v[4:5], v[152:153]
	v_pk_mul_f32 v[6:7], v[6:7], v[154:155]
	s_mov_b64 s[0:1], 0x2c000
	v_lshl_add_u64 v[136:137], v[134:135], 0, s[0:1]
	v_cvt_pk_bf16_f32 v16, v16, v17
	v_cvt_pk_bf16_f32 v17, v18, v19
	v_cvt_pk_bf16_f32 v18, v12, v13
	v_cvt_pk_bf16_f32 v19, v14, v15
	global_store_dwordx4 v[136:137], v[16:19], off
	v_cvt_pk_bf16_f32 v8, v8, v9
	v_cvt_pk_bf16_f32 v9, v10, v11
	v_cvt_pk_bf16_f32 v10, v4, v5
	v_cvt_pk_bf16_f32 v11, v6, v7
	global_store_dwordx4 v[136:137], v[8:11], off offset:256
	s_branch .Lt8_end
.Lt8_gstat:
	s_waitcnt lgkmcnt(0)
	ds_read_b32 v157, v205 offset:64
	v_mul_f32_e32 v188, v156, v156
	v_mul_f32_e32 v186, 0xc0135761, v156
	v_rcp_f32_e32 v190, v156
	v_mul_f32_e32 v188, v188, v156
	v_mul_f32_e32 v188, 0xbdd2d3e8, v188
	v_pk_mul_f32 v[140:141], v[128:129], v[128:129]
	v_pk_mul_f32 v[142:143], v[130:131], v[130:131]
	v_pk_mul_f32 v[144:145], v[124:125], v[124:125]
	v_pk_mul_f32 v[146:147], v[126:127], v[126:127]
	v_pk_mul_f32 v[148:149], v[120:121], v[120:121]
	v_pk_mul_f32 v[150:151], v[122:123], v[122:123]
	v_pk_mul_f32 v[152:153], v[116:117], v[116:117]
	v_pk_mul_f32 v[154:155], v[118:119], v[118:119]
	v_pk_fma_f32 v[140:141], v[140:141], v[188:189], v[186:187] op_sel_hi:[1,0,0]
	v_pk_fma_f32 v[142:143], v[142:143], v[188:189], v[186:187] op_sel_hi:[1,0,0]
	v_pk_fma_f32 v[144:145], v[144:145], v[188:189], v[186:187] op_sel_hi:[1,0,0]
	v_pk_fma_f32 v[146:147], v[146:147], v[188:189], v[186:187] op_sel_hi:[1,0,0]
	v_pk_fma_f32 v[148:149], v[148:149], v[188:189], v[186:187] op_sel_hi:[1,0,0]
	v_pk_fma_f32 v[150:151], v[150:151], v[188:189], v[186:187] op_sel_hi:[1,0,0]
	v_pk_fma_f32 v[152:153], v[152:153], v[188:189], v[186:187] op_sel_hi:[1,0,0]
	v_pk_fma_f32 v[154:155], v[154:155], v[188:189], v[186:187] op_sel_hi:[1,0,0]
	v_pk_mul_f32 v[140:141], v[128:129], v[140:141]
	v_pk_mul_f32 v[142:143], v[130:131], v[142:143]
	v_pk_mul_f32 v[144:145], v[124:125], v[144:145]
	v_pk_mul_f32 v[146:147], v[126:127], v[146:147]
	v_pk_mul_f32 v[148:149], v[120:121], v[148:149]
	v_pk_mul_f32 v[150:151], v[122:123], v[150:151]
	v_pk_mul_f32 v[152:153], v[116:117], v[152:153]
	v_pk_mul_f32 v[154:155], v[118:119], v[154:155]
	v_exp_f32_e32 v140, v140
	v_exp_f32_e32 v141, v141
	v_exp_f32_e32 v142, v142
	v_exp_f32_e32 v143, v143
	v_exp_f32_e32 v144, v144
	v_exp_f32_e32 v145, v145
	v_exp_f32_e32 v146, v146
; __device__ __forceinline__ u32x4 pack8(const f32x4 a, const f32x4 b) { u32x4 w; w.x = cvt_pk_bf16(a[0], a[1]); w.y = cvt_pk_bf16(a[2], a[3]); w.z = cvt_pk_bf16(b[0], b[1]); w.w = cvt_pk_bf16(b[2], b[3]); return w; }
;     ...
;                     for (int e = 0; e < 4; ++e) { const float x0 = v0[e], x1 = v1[e];
;                         const float r0 = __builtin_amdgcn_rcpf(1.0f + __builtin_amdgcn_exp2f(x0 * (c0 + c1 * x0 * x0))), r1 = __builtin_amdgcn_rcpf(1.0f + __builtin_amdgcn_exp2f(x1 * (c0 + c1 * x1 * x1)));
;                         v0[e] = act == 1 ? x0 * r0 : r0; v1[e] = act == 1 ? x1 * r1 : r1; } }
;                 if (stat) {
; #pragma unroll
;                     for (int e = 0; e < 4; ++e) { ls1 += v0[e] + v1[e]; ls2 += v0[e] * v0[e] + v1[e] * v1[e]; } }
;                 *(u32x4*)(rowp + bj * HALF) = pack8(v0, v1); }
;             if (stat) { ls1 = xor_add<16>(ls1); ls1 = xor_add<32>(ls1); ls2 = xor_add<16>(ls2); ls2 = xor_add<32>(ls2);
;                 if (fq == 0) { f32x2 st2; st2.x = ls1; st2.y = ls2; *(f32x2*)(stat + (size_t)(row0 + ai * HALF + m * 16) * 16) = st2; } }
;             asm volatile("" ::: "memory"); } }
	v_exp_f32_e32 v147, v147
	v_exp_f32_e32 v148, v148
	v_exp_f32_e32 v149, v149
	v_exp_f32_e32 v150, v150
	v_exp_f32_e32 v151, v151
	v_exp_f32_e32 v152, v152
	v_exp_f32_e32 v153, v153
	v_exp_f32_e32 v154, v154
	v_exp_f32_e32 v155, v155
	v_pk_fma_f32 v[140:141], v[140:141], v[190:191], v[190:191] op_sel_hi:[1,0,0]
	v_pk_fma_f32 v[142:143], v[142:143], v[190:191], v[190:191] op_sel_hi:[1,0,0]
	v_pk_fma_f32 v[144:145], v[144:145], v[190:191], v[190:191] op_sel_hi:[1,0,0]
	v_pk_fma_f32 v[146:147], v[146:147], v[190:191], v[190:191] op_sel_hi:[1,0,0]
	v_pk_fma_f32 v[148:149], v[148:149], v[190:191], v[190:191] op_sel_hi:[1,0,0]
	v_pk_fma_f32 v[150:151], v[150:151], v[190:191], v[190:191] op_sel_hi:[1,0,0]
	v_pk_fma_f32 v[152:153], v[152:153], v[190:191], v[190:191] op_sel_hi:[1,0,0]
	v_pk_fma_f32 v[154:155], v[154:155], v[190:191], v[190:191] op_sel_hi:[1,0,0]
	v_rcp_f32_e32 v140, v140
	v_rcp_f32_e32 v141, v141
	v_rcp_f32_e32 v142, v142
	v_rcp_f32_e32 v143, v143
	v_rcp_f32_e32 v144, v144
	v_rcp_f32_e32 v145, v145
	v_rcp_f32_e32 v146, v146
	v_rcp_f32_e32 v147, v147
	v_rcp_f32_e32 v148, v148
	v_rcp_f32_e32 v149, v149
	v_rcp_f32_e32 v150, v150
	v_rcp_f32_e32 v151, v151
	v_rcp_f32_e32 v152, v152
	v_rcp_f32_e32 v153, v153
	v_rcp_f32_e32 v154, v154
	v_rcp_f32_e32 v155, v155
	v_pk_mul_f32 v[128:129], v[128:129], v[140:141]
	v_pk_mul_f32 v[130:131], v[130:131], v[142:143]
	v_pk_mul_f32 v[124:125], v[124:125], v[144:145]
	v_pk_mul_f32 v[126:127], v[126:127], v[146:147]
	v_pk_mul_f32 v[120:121], v[120:121], v[148:149]
	v_pk_mul_f32 v[122:123], v[122:123], v[150:151]
	v_pk_mul_f32 v[116:117], v[116:117], v[152:153]
	v_pk_mul_f32 v[118:119], v[118:119], v[154:155]
	v_pk_add_f32 v[192:193], v[128:129], v[130:131]
	v_pk_mul_f32 v[194:195], v[128:129], v[128:129]
	v_pk_fma_f32 v[194:195], v[130:131], v[130:131], v[194:195]
	v_pk_add_f32 v[192:193], v[192:193], v[124:125]
	v_pk_fma_f32 v[194:195], v[124:125], v[124:125], v[194:195]
	v_pk_add_f32 v[192:193], v[192:193], v[126:127]
	v_pk_fma_f32 v[194:195], v[126:127], v[126:127], v[194:195]
	v_pk_add_f32 v[192:193], v[192:193], v[120:121]
	v_pk_fma_f32 v[194:195], v[120:121], v[120:121], v[194:195]
	v_pk_add_f32 v[192:193], v[192:193], v[122:123]
	v_pk_fma_f32 v[194:195], v[122:123], v[122:123], v[194:195]
	v_pk_add_f32 v[192:193], v[192:193], v[116:117]
	v_pk_fma_f32 v[194:195], v[116:117], v[116:117], v[194:195]
	v_pk_add_f32 v[192:193], v[192:193], v[118:119]
	v_pk_fma_f32 v[194:195], v[118:119], v[118:119], v[194:195]
	v_add_f32_e32 v162, v192, v193
	v_add_f32_e32 v163, v194, v195
	ds_swizzle_b32 v161, v162 offset:swizzle(SWAP,16)
	ds_swizzle_b32 v182, v163 offset:swizzle(SWAP,16)
	v_cvt_pk_bf16_f32 v128, v128, v129
	v_cvt_pk_bf16_f32 v129, v130, v131
	v_cvt_pk_bf16_f32 v130, v124, v125
	v_cvt_pk_bf16_f32 v131, v126, v127
	global_store_dwordx4 v[134:135], v[128:131], off
	v_cvt_pk_bf16_f32 v120, v120, v121
	v_cvt_pk_bf16_f32 v121, v122, v123
	v_cvt_pk_bf16_f32 v122, v116, v117
	v_cvt_pk_bf16_f32 v123, v118, v119
	global_store_dwordx4 v[134:135], v[120:123], off offset:256
	s_waitcnt lgkmcnt(0)
	v_add_f32_e32 v162, v162, v161
	v_add_f32_e32 v163, v163, v182
	v_mov_b32_e32 v183, v162
	v_mov_b32_e32 v184, v163
	s_mov_b64 s[0:1], 0x0
	v_lshl_add_u64 v[140:141], v[138:139], 0, s[0:1]
	v_permlane32_swap_b32_e32 v162, v183
	v_permlane32_swap_b32_e32 v163, v184
	s_mov_b64 s[8:9], exec
	s_and_b64 exec, exec, s[4:5]
	v_add_f32_e32 v162, v162, v183
	v_add_f32_e32 v163, v163, v184
	global_store_dwordx2 v[140:141], v[162:163], off
	s_mov_b64 exec, s[8:9]
	s_nop 1
	s_waitcnt lgkmcnt(0)
	v_mov_b32_e32 v156, v157
	ds_read_b32 v157, v205 offset:128
	v_mul_f32_e32 v188, v156, v156
	v_mul_f32_e32 v186, 0xc0135761, v156
	v_rcp_f32_e32 v190, v156
	v_mul_f32_e32 v188, v188, v156
	v_mul_f32_e32 v188, 0xbdd2d3e8, v188
	v_pk_mul_f32 v[140:141], v[112:113], v[112:113]
	v_pk_mul_f32 v[142:143], v[114:115], v[114:115]
	v_pk_mul_f32 v[144:145], v[108:109], v[108:109]
	v_pk_mul_f32 v[146:147], v[110:111], v[110:111]
	v_pk_mul_f32 v[148:149], v[104:105], v[104:105]
	v_pk_mul_f32 v[150:151], v[106:107], v[106:107]
	v_pk_mul_f32 v[152:153], v[100:101], v[100:101]
	v_pk_mul_f32 v[154:155], v[102:103], v[102:103]
	v_pk_fma_f32 v[140:141], v[140:141], v[188:189], v[186:187] op_sel_hi:[1,0,0]
	v_pk_fma_f32 v[142:143], v[142:143], v[188:189], v[186:187] op_sel_hi:[1,0,0]
	v_pk_fma_f32 v[144:145], v[144:145], v[188:189], v[186:187] op_sel_hi:[1,0,0]
	v_pk_fma_f32 v[146:147], v[146:147], v[188:189], v[186:187] op_sel_hi:[1,0,0]
	v_pk_fma_f32 v[148:149], v[148:149], v[188:189], v[186:187] op_sel_hi:[1,0,0]
	v_pk_fma_f32 v[150:151], v[150:151], v[188:189], v[186:187] op_sel_hi:[1,0,0]
	v_pk_fma_f32 v[152:153], v[152:153], v[188:189], v[186:187] op_sel_hi:[1,0,0]
	v_pk_fma_f32 v[154:155], v[154:155], v[188:189], v[186:187] op_sel_hi:[1,0,0]
	v_pk_mul_f32 v[140:141], v[112:113], v[140:141]
	v_pk_mul_f32 v[142:143], v[114:115], v[142:143]
	v_pk_mul_f32 v[144:145], v[108:109], v[144:145]
	v_pk_mul_f32 v[146:147], v[110:111], v[146:147]
	v_pk_mul_f32 v[148:149], v[104:105], v[148:149]
	v_pk_mul_f32 v[150:151], v[106:107], v[150:151]
	v_pk_mul_f32 v[152:153], v[100:101], v[152:153]
	v_pk_mul_f32 v[154:155], v[102:103], v[154:155]
	v_exp_f32_e32 v140, v140
	v_exp_f32_e32 v141, v141
	v_exp_f32_e32 v142, v142
	v_exp_f32_e32 v143, v143
	v_exp_f32_e32 v144, v144
	v_exp_f32_e32 v145, v145
	v_exp_f32_e32 v146, v146
	v_exp_f32_e32 v147, v147
	v_exp_f32_e32 v148, v148
	v_exp_f32_e32 v149, v149
	v_exp_f32_e32 v150, v150
	v_exp_f32_e32 v151, v151
	v_exp_f32_e32 v152, v152
	v_exp_f32_e32 v153, v153
	v_exp_f32_e32 v154, v154
	v_exp_f32_e32 v155, v155
; __device__ __forceinline__ u32x4 pack8(const f32x4 a, const f32x4 b) { u32x4 w; w.x = cvt_pk_bf16(a[0], a[1]); w.y = cvt_pk_bf16(a[2], a[3]); w.z = cvt_pk_bf16(b[0], b[1]); w.w = cvt_pk_bf16(b[2], b[3]); return w; }
;     ...
;         for (int m = 0; m < 4; ++m) { bf16_t* rowp = base + (size_t)(row0 + ai * HALF + m * 16) * ldc + col0; float ls1 = 0.f, ls2 = 0.f; const float rf = rsr[ai * HALF + m * 16];
; #pragma unroll
;             for (int bj = 0; bj < 2; ++bj) { f32x4 v0 = acc[ai][bj][m][0] * rf, v1 = acc[ai][bj][m][1] * rf;
;                 if (act != 0) {
; #pragma unroll
;                     for (int e = 0; e < 4; ++e) { const float x0 = v0[e], x1 = v1[e];
;                         const float r0 = __builtin_amdgcn_rcpf(1.0f + __builtin_amdgcn_exp2f(x0 * (c0 + c1 * x0 * x0))), r1 = __builtin_amdgcn_rcpf(1.0f + __builtin_amdgcn_exp2f(x1 * (c0 + c1 * x1 * x1)));
;                         v0[e] = act == 1 ? x0 * r0 : r0; v1[e] = act == 1 ? x1 * r1 : r1; } }
;                 if (stat) {
; #pragma unroll
;                     for (int e = 0; e < 4; ++e) { ls1 += v0[e] + v1[e]; ls2 += v0[e] * v0[e] + v1[e] * v1[e]; } }
;                 *(u32x4*)(rowp + bj * HALF) = pack8(v0, v1); }
;             if (stat) { ls1 = xor_add<16>(ls1); ls1 = xor_add<32>(ls1); ls2 = xor_add<16>(ls2); ls2 = xor_add<32>(ls2);
;                 if (fq == 0) { f32x2 st2; st2.x = ls1; st2.y = ls2; *(f32x2*)(stat + (size_t)(row0 + ai * HALF + m * 16) * 16) = st2; } }
	v_pk_fma_f32 v[140:141], v[140:141], v[190:191], v[190:191] op_sel_hi:[1,0,0]
	v_pk_fma_f32 v[142:143], v[142:143], v[190:191], v[190:191] op_sel_hi:[1,0,0]
	v_pk_fma_f32 v[144:145], v[144:145], v[190:191], v[190:191] op_sel_hi:[1,0,0]
	v_pk_fma_f32 v[146:147], v[146:147], v[190:191], v[190:191] op_sel_hi:[1,0,0]
	v_pk_fma_f32 v[148:149], v[148:149], v[190:191], v[190:191] op_sel_hi:[1,0,0]
	v_pk_fma_f32 v[150:151], v[150:151], v[190:191], v[190:191] op_sel_hi:[1,0,0]
	v_pk_fma_f32 v[152:153], v[152:153], v[190:191], v[190:191] op_sel_hi:[1,0,0]
	v_pk_fma_f32 v[154:155], v[154:155], v[190:191], v[190:191] op_sel_hi:[1,0,0]
	v_rcp_f32_e32 v140, v140
	v_rcp_f32_e32 v141, v141
	v_rcp_f32_e32 v142, v142
	v_rcp_f32_e32 v143, v143
	v_rcp_f32_e32 v144, v144
	v_rcp_f32_e32 v145, v145
	v_rcp_f32_e32 v146, v146
	v_rcp_f32_e32 v147, v147
	v_rcp_f32_e32 v148, v148
	v_rcp_f32_e32 v149, v149
	v_rcp_f32_e32 v150, v150
	v_rcp_f32_e32 v151, v151
	v_rcp_f32_e32 v152, v152
	v_rcp_f32_e32 v153, v153
	v_rcp_f32_e32 v154, v154
	v_rcp_f32_e32 v155, v155
	v_pk_mul_f32 v[112:113], v[112:113], v[140:141]
	v_pk_mul_f32 v[114:115], v[114:115], v[142:143]
	v_pk_mul_f32 v[108:109], v[108:109], v[144:145]
	v_pk_mul_f32 v[110:111], v[110:111], v[146:147]
	v_pk_mul_f32 v[104:105], v[104:105], v[148:149]
	v_pk_mul_f32 v[106:107], v[106:107], v[150:151]
	v_pk_mul_f32 v[100:101], v[100:101], v[152:153]
	v_pk_mul_f32 v[102:103], v[102:103], v[154:155]
	s_mov_b64 s[0:1], 0x4000
	v_lshl_add_u64 v[136:137], v[134:135], 0, s[0:1]
	v_pk_add_f32 v[192:193], v[112:113], v[114:115]
	v_pk_mul_f32 v[194:195], v[112:113], v[112:113]
	v_pk_fma_f32 v[194:195], v[114:115], v[114:115], v[194:195]
	v_pk_add_f32 v[192:193], v[192:193], v[108:109]
	v_pk_fma_f32 v[194:195], v[108:109], v[108:109], v[194:195]
	v_pk_add_f32 v[192:193], v[192:193], v[110:111]
	v_pk_fma_f32 v[194:195], v[110:111], v[110:111], v[194:195]
	v_pk_add_f32 v[192:193], v[192:193], v[104:105]
	v_pk_fma_f32 v[194:195], v[104:105], v[104:105], v[194:195]
	v_pk_add_f32 v[192:193], v[192:193], v[106:107]
	v_pk_fma_f32 v[194:195], v[106:107], v[106:107], v[194:195]
	v_pk_add_f32 v[192:193], v[192:193], v[100:101]
	v_pk_fma_f32 v[194:195], v[100:101], v[100:101], v[194:195]
	v_pk_add_f32 v[192:193], v[192:193], v[102:103]
	v_pk_fma_f32 v[194:195], v[102:103], v[102:103], v[194:195]
	v_add_f32_e32 v162, v192, v193
	v_add_f32_e32 v163, v194, v195
	ds_swizzle_b32 v161, v162 offset:swizzle(SWAP,16)
	ds_swizzle_b32 v182, v163 offset:swizzle(SWAP,16)
	v_cvt_pk_bf16_f32 v112, v112, v113
	v_cvt_pk_bf16_f32 v113, v114, v115
	v_cvt_pk_bf16_f32 v114, v108, v109
	v_cvt_pk_bf16_f32 v115, v110, v111
	global_store_dwordx4 v[136:137], v[112:115], off
	v_cvt_pk_bf16_f32 v104, v104, v105
	v_cvt_pk_bf16_f32 v105, v106, v107
	v_cvt_pk_bf16_f32 v106, v100, v101
	v_cvt_pk_bf16_f32 v107, v102, v103
	global_store_dwordx4 v[136:137], v[104:107], off offset:256
	s_waitcnt lgkmcnt(0)
	v_add_f32_e32 v162, v162, v161
	v_add_f32_e32 v163, v163, v182
	v_mov_b32_e32 v183, v162
	v_mov_b32_e32 v184, v163
	s_mov_b64 s[0:1], 0x400
	v_lshl_add_u64 v[140:141], v[138:139], 0, s[0:1]
	v_permlane32_swap_b32_e32 v162, v183
	v_permlane32_swap_b32_e32 v163, v184
	s_mov_b64 s[8:9], exec
	s_and_b64 exec, exec, s[4:5]
	v_add_f32_e32 v162, v162, v183
	v_add_f32_e32 v163, v163, v184
	global_store_dwordx2 v[140:141], v[162:163], off
	s_mov_b64 exec, s[8:9]
	s_nop 1
	s_waitcnt lgkmcnt(0)
	v_mov_b32_e32 v156, v157
	ds_read_b32 v157, v205 offset:192
	v_mul_f32_e32 v188, v156, v156
	v_mul_f32_e32 v186, 0xc0135761, v156
	v_rcp_f32_e32 v190, v156
	v_mul_f32_e32 v188, v188, v156
	v_mul_f32_e32 v188, 0xbdd2d3e8, v188
	v_pk_mul_f32 v[140:141], v[96:97], v[96:97]
	v_pk_mul_f32 v[142:143], v[98:99], v[98:99]
	v_pk_mul_f32 v[144:145], v[92:93], v[92:93]
	v_pk_mul_f32 v[146:147], v[94:95], v[94:95]
	v_pk_mul_f32 v[148:149], v[88:89], v[88:89]
	v_pk_mul_f32 v[150:151], v[90:91], v[90:91]
	v_pk_mul_f32 v[152:153], v[84:85], v[84:85]
	v_pk_mul_f32 v[154:155], v[86:87], v[86:87]
	v_pk_fma_f32 v[140:141], v[140:141], v[188:189], v[186:187] op_sel_hi:[1,0,0]
	v_pk_fma_f32 v[142:143], v[142:143], v[188:189], v[186:187] op_sel_hi:[1,0,0]
	v_pk_fma_f32 v[144:145], v[144:145], v[188:189], v[186:187] op_sel_hi:[1,0,0]
	v_pk_fma_f32 v[146:147], v[146:147], v[188:189], v[186:187] op_sel_hi:[1,0,0]
	v_pk_fma_f32 v[148:149], v[148:149], v[188:189], v[186:187] op_sel_hi:[1,0,0]
	v_pk_fma_f32 v[150:151], v[150:151], v[188:189], v[186:187] op_sel_hi:[1,0,0]
	v_pk_fma_f32 v[152:153], v[152:153], v[188:189], v[186:187] op_sel_hi:[1,0,0]
	v_pk_fma_f32 v[154:155], v[154:155], v[188:189], v[186:187] op_sel_hi:[1,0,0]
	v_pk_mul_f32 v[140:141], v[96:97], v[140:141]
	v_pk_mul_f32 v[142:143], v[98:99], v[142:143]
	v_pk_mul_f32 v[144:145], v[92:93], v[144:145]
	v_pk_mul_f32 v[146:147], v[94:95], v[146:147]
	v_pk_mul_f32 v[148:149], v[88:89], v[148:149]
	v_pk_mul_f32 v[150:151], v[90:91], v[150:151]
	v_pk_mul_f32 v[152:153], v[84:85], v[152:153]
	v_pk_mul_f32 v[154:155], v[86:87], v[154:155]
	v_exp_f32_e32 v140, v140
	v_exp_f32_e32 v141, v141
	v_exp_f32_e32 v142, v142
	v_exp_f32_e32 v143, v143
	v_exp_f32_e32 v144, v144
	v_exp_f32_e32 v145, v145
	v_exp_f32_e32 v146, v146
	v_exp_f32_e32 v147, v147
	v_exp_f32_e32 v148, v148
	v_exp_f32_e32 v149, v149
	v_exp_f32_e32 v150, v150
	v_exp_f32_e32 v151, v151
	v_exp_f32_e32 v152, v152
	v_exp_f32_e32 v153, v153
	v_exp_f32_e32 v154, v154
	v_exp_f32_e32 v155, v155
	v_pk_fma_f32 v[140:141], v[140:141], v[190:191], v[190:191] op_sel_hi:[1,0,0]
	v_pk_fma_f32 v[142:143], v[142:143], v[190:191], v[190:191] op_sel_hi:[1,0,0]
	v_pk_fma_f32 v[144:145], v[144:145], v[190:191], v[190:191] op_sel_hi:[1,0,0]
; __device__ __forceinline__ u32x4 pack8(const f32x4 a, const f32x4 b) { u32x4 w; w.x = cvt_pk_bf16(a[0], a[1]); w.y = cvt_pk_bf16(a[2], a[3]); w.z = cvt_pk_bf16(b[0], b[1]); w.w = cvt_pk_bf16(b[2], b[3]); return w; }
;     ...
;         for (int m = 0; m < 4; ++m) { bf16_t* rowp = base + (size_t)(row0 + ai * HALF + m * 16) * ldc + col0; float ls1 = 0.f, ls2 = 0.f; const float rf = rsr[ai * HALF + m * 16];
; #pragma unroll
;             for (int bj = 0; bj < 2; ++bj) { f32x4 v0 = acc[ai][bj][m][0] * rf, v1 = acc[ai][bj][m][1] * rf;
;                 if (act != 0) {
; #pragma unroll
;                     for (int e = 0; e < 4; ++e) { const float x0 = v0[e], x1 = v1[e];
;                         const float r0 = __builtin_amdgcn_rcpf(1.0f + __builtin_amdgcn_exp2f(x0 * (c0 + c1 * x0 * x0))), r1 = __builtin_amdgcn_rcpf(1.0f + __builtin_amdgcn_exp2f(x1 * (c0 + c1 * x1 * x1)));
;                         v0[e] = act == 1 ? x0 * r0 : r0; v1[e] = act == 1 ? x1 * r1 : r1; } }
;                 if (stat) {
; #pragma unroll
;                     for (int e = 0; e < 4; ++e) { ls1 += v0[e] + v1[e]; ls2 += v0[e] * v0[e] + v1[e] * v1[e]; } }
;                 *(u32x4*)(rowp + bj * HALF) = pack8(v0, v1); }
;             if (stat) { ls1 = xor_add<16>(ls1); ls1 = xor_add<32>(ls1); ls2 = xor_add<16>(ls2); ls2 = xor_add<32>(ls2);
;                 if (fq == 0) { f32x2 st2; st2.x = ls1; st2.y = ls2; *(f32x2*)(stat + (size_t)(row0 + ai * HALF + m * 16) * 16) = st2; } }
	v_pk_fma_f32 v[146:147], v[146:147], v[190:191], v[190:191] op_sel_hi:[1,0,0]
	v_pk_fma_f32 v[148:149], v[148:149], v[190:191], v[190:191] op_sel_hi:[1,0,0]
	v_pk_fma_f32 v[150:151], v[150:151], v[190:191], v[190:191] op_sel_hi:[1,0,0]
	v_pk_fma_f32 v[152:153], v[152:153], v[190:191], v[190:191] op_sel_hi:[1,0,0]
	v_pk_fma_f32 v[154:155], v[154:155], v[190:191], v[190:191] op_sel_hi:[1,0,0]
	v_rcp_f32_e32 v140, v140
	v_rcp_f32_e32 v141, v141
	v_rcp_f32_e32 v142, v142
	v_rcp_f32_e32 v143, v143
	v_rcp_f32_e32 v144, v144
	v_rcp_f32_e32 v145, v145
	v_rcp_f32_e32 v146, v146
	v_rcp_f32_e32 v147, v147
	v_rcp_f32_e32 v148, v148
	v_rcp_f32_e32 v149, v149
	v_rcp_f32_e32 v150, v150
	v_rcp_f32_e32 v151, v151
	v_rcp_f32_e32 v152, v152
	v_rcp_f32_e32 v153, v153
	v_rcp_f32_e32 v154, v154
	v_rcp_f32_e32 v155, v155
	v_pk_mul_f32 v[96:97], v[96:97], v[140:141]
	v_pk_mul_f32 v[98:99], v[98:99], v[142:143]
	v_pk_mul_f32 v[92:93], v[92:93], v[144:145]
	v_pk_mul_f32 v[94:95], v[94:95], v[146:147]
	v_pk_mul_f32 v[88:89], v[88:89], v[148:149]
	v_pk_mul_f32 v[90:91], v[90:91], v[150:151]
	v_pk_mul_f32 v[84:85], v[84:85], v[152:153]
	v_pk_mul_f32 v[86:87], v[86:87], v[154:155]
	s_mov_b64 s[0:1], 0x8000
	v_lshl_add_u64 v[136:137], v[134:135], 0, s[0:1]
	v_pk_add_f32 v[192:193], v[96:97], v[98:99]
	v_pk_mul_f32 v[194:195], v[96:97], v[96:97]
	v_pk_fma_f32 v[194:195], v[98:99], v[98:99], v[194:195]
	v_pk_add_f32 v[192:193], v[192:193], v[92:93]
	v_pk_fma_f32 v[194:195], v[92:93], v[92:93], v[194:195]
	v_pk_add_f32 v[192:193], v[192:193], v[94:95]
	v_pk_fma_f32 v[194:195], v[94:95], v[94:95], v[194:195]
	v_pk_add_f32 v[192:193], v[192:193], v[88:89]
	v_pk_fma_f32 v[194:195], v[88:89], v[88:89], v[194:195]
	v_pk_add_f32 v[192:193], v[192:193], v[90:91]
	v_pk_fma_f32 v[194:195], v[90:91], v[90:91], v[194:195]
	v_pk_add_f32 v[192:193], v[192:193], v[84:85]
	v_pk_fma_f32 v[194:195], v[84:85], v[84:85], v[194:195]
	v_pk_add_f32 v[192:193], v[192:193], v[86:87]
	v_pk_fma_f32 v[194:195], v[86:87], v[86:87], v[194:195]
	v_add_f32_e32 v162, v192, v193
	v_add_f32_e32 v163, v194, v195
	ds_swizzle_b32 v161, v162 offset:swizzle(SWAP,16)
	ds_swizzle_b32 v182, v163 offset:swizzle(SWAP,16)
	v_cvt_pk_bf16_f32 v96, v96, v97
	v_cvt_pk_bf16_f32 v97, v98, v99
	v_cvt_pk_bf16_f32 v98, v92, v93
	v_cvt_pk_bf16_f32 v99, v94, v95
	global_store_dwordx4 v[136:137], v[96:99], off
	v_cvt_pk_bf16_f32 v88, v88, v89
	v_cvt_pk_bf16_f32 v89, v90, v91
	v_cvt_pk_bf16_f32 v90, v84, v85
	v_cvt_pk_bf16_f32 v91, v86, v87
	global_store_dwordx4 v[136:137], v[88:91], off offset:256
	s_waitcnt lgkmcnt(0)
	v_add_f32_e32 v162, v162, v161
	v_add_f32_e32 v163, v163, v182
	v_mov_b32_e32 v183, v162
	v_mov_b32_e32 v184, v163
	s_mov_b64 s[0:1], 0x800
	v_lshl_add_u64 v[140:141], v[138:139], 0, s[0:1]
	v_permlane32_swap_b32_e32 v162, v183
	v_permlane32_swap_b32_e32 v163, v184
	s_mov_b64 s[8:9], exec
	s_and_b64 exec, exec, s[4:5]
	v_add_f32_e32 v162, v162, v183
	v_add_f32_e32 v163, v163, v184
	global_store_dwordx2 v[140:141], v[162:163], off
	s_mov_b64 exec, s[8:9]
	s_nop 1
	s_waitcnt lgkmcnt(0)
	v_mov_b32_e32 v156, v157
	ds_read_b32 v157, v205 offset:512
	v_mul_f32_e32 v188, v156, v156
	v_mul_f32_e32 v186, 0xc0135761, v156
	v_rcp_f32_e32 v190, v156
	v_mul_f32_e32 v188, v188, v156
	v_mul_f32_e32 v188, 0xbdd2d3e8, v188
	v_pk_mul_f32 v[140:141], v[80:81], v[80:81]
	v_pk_mul_f32 v[142:143], v[82:83], v[82:83]
	v_pk_mul_f32 v[144:145], v[76:77], v[76:77]
	v_pk_mul_f32 v[146:147], v[78:79], v[78:79]
	v_pk_mul_f32 v[148:149], v[72:73], v[72:73]
	v_pk_mul_f32 v[150:151], v[74:75], v[74:75]
	v_pk_mul_f32 v[152:153], v[68:69], v[68:69]
	v_pk_mul_f32 v[154:155], v[70:71], v[70:71]
	v_pk_fma_f32 v[140:141], v[140:141], v[188:189], v[186:187] op_sel_hi:[1,0,0]
	v_pk_fma_f32 v[142:143], v[142:143], v[188:189], v[186:187] op_sel_hi:[1,0,0]
	v_pk_fma_f32 v[144:145], v[144:145], v[188:189], v[186:187] op_sel_hi:[1,0,0]
	v_pk_fma_f32 v[146:147], v[146:147], v[188:189], v[186:187] op_sel_hi:[1,0,0]
	v_pk_fma_f32 v[148:149], v[148:149], v[188:189], v[186:187] op_sel_hi:[1,0,0]
	v_pk_fma_f32 v[150:151], v[150:151], v[188:189], v[186:187] op_sel_hi:[1,0,0]
	v_pk_fma_f32 v[152:153], v[152:153], v[188:189], v[186:187] op_sel_hi:[1,0,0]
	v_pk_fma_f32 v[154:155], v[154:155], v[188:189], v[186:187] op_sel_hi:[1,0,0]
	v_pk_mul_f32 v[140:141], v[80:81], v[140:141]
	v_pk_mul_f32 v[142:143], v[82:83], v[142:143]
	v_pk_mul_f32 v[144:145], v[76:77], v[144:145]
	v_pk_mul_f32 v[146:147], v[78:79], v[146:147]
	v_pk_mul_f32 v[148:149], v[72:73], v[148:149]
	v_pk_mul_f32 v[150:151], v[74:75], v[150:151]
	v_pk_mul_f32 v[152:153], v[68:69], v[152:153]
	v_pk_mul_f32 v[154:155], v[70:71], v[154:155]
	v_exp_f32_e32 v140, v140
	v_exp_f32_e32 v141, v141
	v_exp_f32_e32 v142, v142
	v_exp_f32_e32 v143, v143
	v_exp_f32_e32 v144, v144
	v_exp_f32_e32 v145, v145
	v_exp_f32_e32 v146, v146
	v_exp_f32_e32 v147, v147
	v_exp_f32_e32 v148, v148
	v_exp_f32_e32 v149, v149
	v_exp_f32_e32 v150, v150
	v_exp_f32_e32 v151, v151
	v_exp_f32_e32 v152, v152
	v_exp_f32_e32 v153, v153
	v_exp_f32_e32 v154, v154
	v_exp_f32_e32 v155, v155
	v_pk_fma_f32 v[140:141], v[140:141], v[190:191], v[190:191] op_sel_hi:[1,0,0]
	v_pk_fma_f32 v[142:143], v[142:143], v[190:191], v[190:191] op_sel_hi:[1,0,0]
	v_pk_fma_f32 v[144:145], v[144:145], v[190:191], v[190:191] op_sel_hi:[1,0,0]
	v_pk_fma_f32 v[146:147], v[146:147], v[190:191], v[190:191] op_sel_hi:[1,0,0]
	v_pk_fma_f32 v[148:149], v[148:149], v[190:191], v[190:191] op_sel_hi:[1,0,0]
	v_pk_fma_f32 v[150:151], v[150:151], v[190:191], v[190:191] op_sel_hi:[1,0,0]
	v_pk_fma_f32 v[152:153], v[152:153], v[190:191], v[190:191] op_sel_hi:[1,0,0]
; __device__ __forceinline__ u32x4 pack8(const f32x4 a, const f32x4 b) { u32x4 w; w.x = cvt_pk_bf16(a[0], a[1]); w.y = cvt_pk_bf16(a[2], a[3]); w.z = cvt_pk_bf16(b[0], b[1]); w.w = cvt_pk_bf16(b[2], b[3]); return w; }
;     ...
;         for (int m = 0; m < 4; ++m) { bf16_t* rowp = base + (size_t)(row0 + ai * HALF + m * 16) * ldc + col0; float ls1 = 0.f, ls2 = 0.f; const float rf = rsr[ai * HALF + m * 16];
; #pragma unroll
;             for (int bj = 0; bj < 2; ++bj) { f32x4 v0 = acc[ai][bj][m][0] * rf, v1 = acc[ai][bj][m][1] * rf;
;                 if (act != 0) {
; #pragma unroll
;                     for (int e = 0; e < 4; ++e) { const float x0 = v0[e], x1 = v1[e];
;                         const float r0 = __builtin_amdgcn_rcpf(1.0f + __builtin_amdgcn_exp2f(x0 * (c0 + c1 * x0 * x0))), r1 = __builtin_amdgcn_rcpf(1.0f + __builtin_amdgcn_exp2f(x1 * (c0 + c1 * x1 * x1)));
;                         v0[e] = act == 1 ? x0 * r0 : r0; v1[e] = act == 1 ? x1 * r1 : r1; } }
;                 if (stat) {
; #pragma unroll
;                     for (int e = 0; e < 4; ++e) { ls1 += v0[e] + v1[e]; ls2 += v0[e] * v0[e] + v1[e] * v1[e]; } }
;                 *(u32x4*)(rowp + bj * HALF) = pack8(v0, v1); }
;             if (stat) { ls1 = xor_add<16>(ls1); ls1 = xor_add<32>(ls1); ls2 = xor_add<16>(ls2); ls2 = xor_add<32>(ls2);
;                 if (fq == 0) { f32x2 st2; st2.x = ls1; st2.y = ls2; *(f32x2*)(stat + (size_t)(row0 + ai * HALF + m * 16) * 16) = st2; } }
	v_pk_fma_f32 v[154:155], v[154:155], v[190:191], v[190:191] op_sel_hi:[1,0,0]
	v_rcp_f32_e32 v140, v140
	v_rcp_f32_e32 v141, v141
	v_rcp_f32_e32 v142, v142
	v_rcp_f32_e32 v143, v143
	v_rcp_f32_e32 v144, v144
	v_rcp_f32_e32 v145, v145
	v_rcp_f32_e32 v146, v146
	v_rcp_f32_e32 v147, v147
	v_rcp_f32_e32 v148, v148
	v_rcp_f32_e32 v149, v149
	v_rcp_f32_e32 v150, v150
	v_rcp_f32_e32 v151, v151
	v_rcp_f32_e32 v152, v152
	v_rcp_f32_e32 v153, v153
	v_rcp_f32_e32 v154, v154
	v_rcp_f32_e32 v155, v155
	v_pk_mul_f32 v[80:81], v[80:81], v[140:141]
	v_pk_mul_f32 v[82:83], v[82:83], v[142:143]
	v_pk_mul_f32 v[76:77], v[76:77], v[144:145]
	v_pk_mul_f32 v[78:79], v[78:79], v[146:147]
	v_pk_mul_f32 v[72:73], v[72:73], v[148:149]
	v_pk_mul_f32 v[74:75], v[74:75], v[150:151]
	v_pk_mul_f32 v[68:69], v[68:69], v[152:153]
	v_pk_mul_f32 v[70:71], v[70:71], v[154:155]
	s_mov_b64 s[0:1], 0xc000
	v_lshl_add_u64 v[136:137], v[134:135], 0, s[0:1]
	v_pk_add_f32 v[192:193], v[80:81], v[82:83]
	v_pk_mul_f32 v[194:195], v[80:81], v[80:81]
	v_pk_fma_f32 v[194:195], v[82:83], v[82:83], v[194:195]
	v_pk_add_f32 v[192:193], v[192:193], v[76:77]
	v_pk_fma_f32 v[194:195], v[76:77], v[76:77], v[194:195]
	v_pk_add_f32 v[192:193], v[192:193], v[78:79]
	v_pk_fma_f32 v[194:195], v[78:79], v[78:79], v[194:195]
	v_pk_add_f32 v[192:193], v[192:193], v[72:73]
	v_pk_fma_f32 v[194:195], v[72:73], v[72:73], v[194:195]
	v_pk_add_f32 v[192:193], v[192:193], v[74:75]
	v_pk_fma_f32 v[194:195], v[74:75], v[74:75], v[194:195]
	v_pk_add_f32 v[192:193], v[192:193], v[68:69]
	v_pk_fma_f32 v[194:195], v[68:69], v[68:69], v[194:195]
	v_pk_add_f32 v[192:193], v[192:193], v[70:71]
	v_pk_fma_f32 v[194:195], v[70:71], v[70:71], v[194:195]
	v_add_f32_e32 v162, v192, v193
	v_add_f32_e32 v163, v194, v195
	ds_swizzle_b32 v161, v162 offset:swizzle(SWAP,16)
	ds_swizzle_b32 v182, v163 offset:swizzle(SWAP,16)
	v_cvt_pk_bf16_f32 v80, v80, v81
	v_cvt_pk_bf16_f32 v81, v82, v83
	v_cvt_pk_bf16_f32 v82, v76, v77
	v_cvt_pk_bf16_f32 v83, v78, v79
	global_store_dwordx4 v[136:137], v[80:83], off
	v_cvt_pk_bf16_f32 v72, v72, v73
	v_cvt_pk_bf16_f32 v73, v74, v75
	v_cvt_pk_bf16_f32 v74, v68, v69
	v_cvt_pk_bf16_f32 v75, v70, v71
	global_store_dwordx4 v[136:137], v[72:75], off offset:256
	s_waitcnt lgkmcnt(0)
	v_add_f32_e32 v162, v162, v161
	v_add_f32_e32 v163, v163, v182
	v_mov_b32_e32 v183, v162
	v_mov_b32_e32 v184, v163
	s_mov_b64 s[0:1], 0xc00
	v_lshl_add_u64 v[140:141], v[138:139], 0, s[0:1]
	v_permlane32_swap_b32_e32 v162, v183
	v_permlane32_swap_b32_e32 v163, v184
	s_mov_b64 s[8:9], exec
	s_and_b64 exec, exec, s[4:5]
	v_add_f32_e32 v162, v162, v183
	v_add_f32_e32 v163, v163, v184
	global_store_dwordx2 v[140:141], v[162:163], off
	s_mov_b64 exec, s[8:9]
	s_nop 1
	s_waitcnt lgkmcnt(0)
	v_mov_b32_e32 v156, v157
	ds_read_b32 v157, v205 offset:576
	v_mul_f32_e32 v188, v156, v156
	v_mul_f32_e32 v186, 0xc0135761, v156
	v_rcp_f32_e32 v190, v156
	v_mul_f32_e32 v188, v188, v156
	v_mul_f32_e32 v188, 0xbdd2d3e8, v188
	v_pk_mul_f32 v[140:141], v[64:65], v[64:65]
	v_pk_mul_f32 v[142:143], v[66:67], v[66:67]
	v_pk_mul_f32 v[144:145], v[60:61], v[60:61]
	v_pk_mul_f32 v[146:147], v[62:63], v[62:63]
	v_pk_mul_f32 v[148:149], v[56:57], v[56:57]
	v_pk_mul_f32 v[150:151], v[58:59], v[58:59]
	v_pk_mul_f32 v[152:153], v[52:53], v[52:53]
	v_pk_mul_f32 v[154:155], v[54:55], v[54:55]
	v_pk_fma_f32 v[140:141], v[140:141], v[188:189], v[186:187] op_sel_hi:[1,0,0]
	v_pk_fma_f32 v[142:143], v[142:143], v[188:189], v[186:187] op_sel_hi:[1,0,0]
	v_pk_fma_f32 v[144:145], v[144:145], v[188:189], v[186:187] op_sel_hi:[1,0,0]
	v_pk_fma_f32 v[146:147], v[146:147], v[188:189], v[186:187] op_sel_hi:[1,0,0]
	v_pk_fma_f32 v[148:149], v[148:149], v[188:189], v[186:187] op_sel_hi:[1,0,0]
	v_pk_fma_f32 v[150:151], v[150:151], v[188:189], v[186:187] op_sel_hi:[1,0,0]
	v_pk_fma_f32 v[152:153], v[152:153], v[188:189], v[186:187] op_sel_hi:[1,0,0]
	v_pk_fma_f32 v[154:155], v[154:155], v[188:189], v[186:187] op_sel_hi:[1,0,0]
	v_pk_mul_f32 v[140:141], v[64:65], v[140:141]
	v_pk_mul_f32 v[142:143], v[66:67], v[142:143]
	v_pk_mul_f32 v[144:145], v[60:61], v[144:145]
	v_pk_mul_f32 v[146:147], v[62:63], v[146:147]
	v_pk_mul_f32 v[148:149], v[56:57], v[148:149]
	v_pk_mul_f32 v[150:151], v[58:59], v[150:151]
	v_pk_mul_f32 v[152:153], v[52:53], v[152:153]
	v_pk_mul_f32 v[154:155], v[54:55], v[154:155]
	v_exp_f32_e32 v140, v140
	v_exp_f32_e32 v141, v141
	v_exp_f32_e32 v142, v142
	v_exp_f32_e32 v143, v143
	v_exp_f32_e32 v144, v144
	v_exp_f32_e32 v145, v145
	v_exp_f32_e32 v146, v146
	v_exp_f32_e32 v147, v147
	v_exp_f32_e32 v148, v148
	v_exp_f32_e32 v149, v149
	v_exp_f32_e32 v150, v150
	v_exp_f32_e32 v151, v151
	v_exp_f32_e32 v152, v152
	v_exp_f32_e32 v153, v153
	v_exp_f32_e32 v154, v154
	v_exp_f32_e32 v155, v155
	v_pk_fma_f32 v[140:141], v[140:141], v[190:191], v[190:191] op_sel_hi:[1,0,0]
	v_pk_fma_f32 v[142:143], v[142:143], v[190:191], v[190:191] op_sel_hi:[1,0,0]
	v_pk_fma_f32 v[144:145], v[144:145], v[190:191], v[190:191] op_sel_hi:[1,0,0]
	v_pk_fma_f32 v[146:147], v[146:147], v[190:191], v[190:191] op_sel_hi:[1,0,0]
	v_pk_fma_f32 v[148:149], v[148:149], v[190:191], v[190:191] op_sel_hi:[1,0,0]
	v_pk_fma_f32 v[150:151], v[150:151], v[190:191], v[190:191] op_sel_hi:[1,0,0]
	v_pk_fma_f32 v[152:153], v[152:153], v[190:191], v[190:191] op_sel_hi:[1,0,0]
	v_pk_fma_f32 v[154:155], v[154:155], v[190:191], v[190:191] op_sel_hi:[1,0,0]
	v_rcp_f32_e32 v140, v140
	v_rcp_f32_e32 v141, v141
	v_rcp_f32_e32 v142, v142
	v_rcp_f32_e32 v143, v143
	v_rcp_f32_e32 v144, v144
	v_rcp_f32_e32 v145, v145
	v_rcp_f32_e32 v146, v146
	v_rcp_f32_e32 v147, v147
	v_rcp_f32_e32 v148, v148
; __device__ __forceinline__ u32x4 pack8(const f32x4 a, const f32x4 b) { u32x4 w; w.x = cvt_pk_bf16(a[0], a[1]); w.y = cvt_pk_bf16(a[2], a[3]); w.z = cvt_pk_bf16(b[0], b[1]); w.w = cvt_pk_bf16(b[2], b[3]); return w; }
;     ...
;         for (int m = 0; m < 4; ++m) { bf16_t* rowp = base + (size_t)(row0 + ai * HALF + m * 16) * ldc + col0; float ls1 = 0.f, ls2 = 0.f; const float rf = rsr[ai * HALF + m * 16];
; #pragma unroll
;             for (int bj = 0; bj < 2; ++bj) { f32x4 v0 = acc[ai][bj][m][0] * rf, v1 = acc[ai][bj][m][1] * rf;
;                 if (act != 0) {
; #pragma unroll
;                     for (int e = 0; e < 4; ++e) { const float x0 = v0[e], x1 = v1[e];
;                         const float r0 = __builtin_amdgcn_rcpf(1.0f + __builtin_amdgcn_exp2f(x0 * (c0 + c1 * x0 * x0))), r1 = __builtin_amdgcn_rcpf(1.0f + __builtin_amdgcn_exp2f(x1 * (c0 + c1 * x1 * x1)));
;                         v0[e] = act == 1 ? x0 * r0 : r0; v1[e] = act == 1 ? x1 * r1 : r1; } }
;                 if (stat) {
; #pragma unroll
;                     for (int e = 0; e < 4; ++e) { ls1 += v0[e] + v1[e]; ls2 += v0[e] * v0[e] + v1[e] * v1[e]; } }
;                 *(u32x4*)(rowp + bj * HALF) = pack8(v0, v1); }
;             if (stat) { ls1 = xor_add<16>(ls1); ls1 = xor_add<32>(ls1); ls2 = xor_add<16>(ls2); ls2 = xor_add<32>(ls2);
;                 if (fq == 0) { f32x2 st2; st2.x = ls1; st2.y = ls2; *(f32x2*)(stat + (size_t)(row0 + ai * HALF + m * 16) * 16) = st2; } }
	v_rcp_f32_e32 v149, v149
	v_rcp_f32_e32 v150, v150
	v_rcp_f32_e32 v151, v151
	v_rcp_f32_e32 v152, v152
	v_rcp_f32_e32 v153, v153
	v_rcp_f32_e32 v154, v154
	v_rcp_f32_e32 v155, v155
	v_pk_mul_f32 v[64:65], v[64:65], v[140:141]
	v_pk_mul_f32 v[66:67], v[66:67], v[142:143]
	v_pk_mul_f32 v[60:61], v[60:61], v[144:145]
	v_pk_mul_f32 v[62:63], v[62:63], v[146:147]
	v_pk_mul_f32 v[56:57], v[56:57], v[148:149]
	v_pk_mul_f32 v[58:59], v[58:59], v[150:151]
	v_pk_mul_f32 v[52:53], v[52:53], v[152:153]
	v_pk_mul_f32 v[54:55], v[54:55], v[154:155]
	s_mov_b64 s[0:1], 0x20000
	v_lshl_add_u64 v[136:137], v[134:135], 0, s[0:1]
	v_pk_add_f32 v[192:193], v[64:65], v[66:67]
	v_pk_mul_f32 v[194:195], v[64:65], v[64:65]
	v_pk_fma_f32 v[194:195], v[66:67], v[66:67], v[194:195]
	v_pk_add_f32 v[192:193], v[192:193], v[60:61]
	v_pk_fma_f32 v[194:195], v[60:61], v[60:61], v[194:195]
	v_pk_add_f32 v[192:193], v[192:193], v[62:63]
	v_pk_fma_f32 v[194:195], v[62:63], v[62:63], v[194:195]
	v_pk_add_f32 v[192:193], v[192:193], v[56:57]
	v_pk_fma_f32 v[194:195], v[56:57], v[56:57], v[194:195]
	v_pk_add_f32 v[192:193], v[192:193], v[58:59]
	v_pk_fma_f32 v[194:195], v[58:59], v[58:59], v[194:195]
	v_pk_add_f32 v[192:193], v[192:193], v[52:53]
	v_pk_fma_f32 v[194:195], v[52:53], v[52:53], v[194:195]
	v_pk_add_f32 v[192:193], v[192:193], v[54:55]
	v_pk_fma_f32 v[194:195], v[54:55], v[54:55], v[194:195]
	v_add_f32_e32 v162, v192, v193
	v_add_f32_e32 v163, v194, v195
	ds_swizzle_b32 v161, v162 offset:swizzle(SWAP,16)
	ds_swizzle_b32 v182, v163 offset:swizzle(SWAP,16)
	v_cvt_pk_bf16_f32 v64, v64, v65
	v_cvt_pk_bf16_f32 v65, v66, v67
	v_cvt_pk_bf16_f32 v66, v60, v61
	v_cvt_pk_bf16_f32 v67, v62, v63
	global_store_dwordx4 v[136:137], v[64:67], off
	v_cvt_pk_bf16_f32 v56, v56, v57
	v_cvt_pk_bf16_f32 v57, v58, v59
	v_cvt_pk_bf16_f32 v58, v52, v53
	v_cvt_pk_bf16_f32 v59, v54, v55
	global_store_dwordx4 v[136:137], v[56:59], off offset:256
	s_waitcnt lgkmcnt(0)
	v_add_f32_e32 v162, v162, v161
	v_add_f32_e32 v163, v163, v182
	v_mov_b32_e32 v183, v162
	v_mov_b32_e32 v184, v163
	s_mov_b64 s[0:1], 0x2000
	v_lshl_add_u64 v[140:141], v[138:139], 0, s[0:1]
	v_permlane32_swap_b32_e32 v162, v183
	v_permlane32_swap_b32_e32 v163, v184
	s_mov_b64 s[8:9], exec
	s_and_b64 exec, exec, s[4:5]
	v_add_f32_e32 v162, v162, v183
	v_add_f32_e32 v163, v163, v184
	global_store_dwordx2 v[140:141], v[162:163], off
	s_mov_b64 exec, s[8:9]
	s_nop 1
	s_waitcnt lgkmcnt(0)
	v_mov_b32_e32 v156, v157
	ds_read_b32 v157, v205 offset:640
	v_mul_f32_e32 v188, v156, v156
	v_mul_f32_e32 v186, 0xc0135761, v156
	v_rcp_f32_e32 v190, v156
	v_mul_f32_e32 v188, v188, v156
	v_mul_f32_e32 v188, 0xbdd2d3e8, v188
	v_pk_mul_f32 v[140:141], v[48:49], v[48:49]
	v_pk_mul_f32 v[142:143], v[50:51], v[50:51]
	v_pk_mul_f32 v[144:145], v[44:45], v[44:45]
	v_pk_mul_f32 v[146:147], v[46:47], v[46:47]
	v_pk_mul_f32 v[148:149], v[40:41], v[40:41]
	v_pk_mul_f32 v[150:151], v[42:43], v[42:43]
	v_pk_mul_f32 v[152:153], v[36:37], v[36:37]
	v_pk_mul_f32 v[154:155], v[38:39], v[38:39]
	v_pk_fma_f32 v[140:141], v[140:141], v[188:189], v[186:187] op_sel_hi:[1,0,0]
	v_pk_fma_f32 v[142:143], v[142:143], v[188:189], v[186:187] op_sel_hi:[1,0,0]
	v_pk_fma_f32 v[144:145], v[144:145], v[188:189], v[186:187] op_sel_hi:[1,0,0]
	v_pk_fma_f32 v[146:147], v[146:147], v[188:189], v[186:187] op_sel_hi:[1,0,0]
	v_pk_fma_f32 v[148:149], v[148:149], v[188:189], v[186:187] op_sel_hi:[1,0,0]
	v_pk_fma_f32 v[150:151], v[150:151], v[188:189], v[186:187] op_sel_hi:[1,0,0]
	v_pk_fma_f32 v[152:153], v[152:153], v[188:189], v[186:187] op_sel_hi:[1,0,0]
	v_pk_fma_f32 v[154:155], v[154:155], v[188:189], v[186:187] op_sel_hi:[1,0,0]
	v_pk_mul_f32 v[140:141], v[48:49], v[140:141]
	v_pk_mul_f32 v[142:143], v[50:51], v[142:143]
	v_pk_mul_f32 v[144:145], v[44:45], v[144:145]
	v_pk_mul_f32 v[146:147], v[46:47], v[146:147]
	v_pk_mul_f32 v[148:149], v[40:41], v[148:149]
	v_pk_mul_f32 v[150:151], v[42:43], v[150:151]
	v_pk_mul_f32 v[152:153], v[36:37], v[152:153]
	v_pk_mul_f32 v[154:155], v[38:39], v[154:155]
	v_exp_f32_e32 v140, v140
	v_exp_f32_e32 v141, v141
	v_exp_f32_e32 v142, v142
	v_exp_f32_e32 v143, v143
	v_exp_f32_e32 v144, v144
	v_exp_f32_e32 v145, v145
	v_exp_f32_e32 v146, v146
	v_exp_f32_e32 v147, v147
	v_exp_f32_e32 v148, v148
	v_exp_f32_e32 v149, v149
	v_exp_f32_e32 v150, v150
	v_exp_f32_e32 v151, v151
	v_exp_f32_e32 v152, v152
	v_exp_f32_e32 v153, v153
	v_exp_f32_e32 v154, v154
	v_exp_f32_e32 v155, v155
	v_pk_fma_f32 v[140:141], v[140:141], v[190:191], v[190:191] op_sel_hi:[1,0,0]
	v_pk_fma_f32 v[142:143], v[142:143], v[190:191], v[190:191] op_sel_hi:[1,0,0]
	v_pk_fma_f32 v[144:145], v[144:145], v[190:191], v[190:191] op_sel_hi:[1,0,0]
	v_pk_fma_f32 v[146:147], v[146:147], v[190:191], v[190:191] op_sel_hi:[1,0,0]
	v_pk_fma_f32 v[148:149], v[148:149], v[190:191], v[190:191] op_sel_hi:[1,0,0]
	v_pk_fma_f32 v[150:151], v[150:151], v[190:191], v[190:191] op_sel_hi:[1,0,0]
	v_pk_fma_f32 v[152:153], v[152:153], v[190:191], v[190:191] op_sel_hi:[1,0,0]
	v_pk_fma_f32 v[154:155], v[154:155], v[190:191], v[190:191] op_sel_hi:[1,0,0]
	v_rcp_f32_e32 v140, v140
	v_rcp_f32_e32 v141, v141
	v_rcp_f32_e32 v142, v142
	v_rcp_f32_e32 v143, v143
	v_rcp_f32_e32 v144, v144
	v_rcp_f32_e32 v145, v145
	v_rcp_f32_e32 v146, v146
	v_rcp_f32_e32 v147, v147
	v_rcp_f32_e32 v148, v148
	v_rcp_f32_e32 v149, v149
	v_rcp_f32_e32 v150, v150
	v_rcp_f32_e32 v151, v151
	v_rcp_f32_e32 v152, v152
	v_rcp_f32_e32 v153, v153
	v_rcp_f32_e32 v154, v154
	v_rcp_f32_e32 v155, v155
	v_pk_mul_f32 v[48:49], v[48:49], v[140:141]
	v_pk_mul_f32 v[50:51], v[50:51], v[142:143]
	v_pk_mul_f32 v[44:45], v[44:45], v[144:145]
; __device__ __forceinline__ u32x4 pack8(const f32x4 a, const f32x4 b) { u32x4 w; w.x = cvt_pk_bf16(a[0], a[1]); w.y = cvt_pk_bf16(a[2], a[3]); w.z = cvt_pk_bf16(b[0], b[1]); w.w = cvt_pk_bf16(b[2], b[3]); return w; }
;     ...
;         for (int m = 0; m < 4; ++m) { bf16_t* rowp = base + (size_t)(row0 + ai * HALF + m * 16) * ldc + col0; float ls1 = 0.f, ls2 = 0.f; const float rf = rsr[ai * HALF + m * 16];
; #pragma unroll
;             for (int bj = 0; bj < 2; ++bj) { f32x4 v0 = acc[ai][bj][m][0] * rf, v1 = acc[ai][bj][m][1] * rf;
;                 if (act != 0) {
; #pragma unroll
;                     for (int e = 0; e < 4; ++e) { const float x0 = v0[e], x1 = v1[e];
;                         const float r0 = __builtin_amdgcn_rcpf(1.0f + __builtin_amdgcn_exp2f(x0 * (c0 + c1 * x0 * x0))), r1 = __builtin_amdgcn_rcpf(1.0f + __builtin_amdgcn_exp2f(x1 * (c0 + c1 * x1 * x1)));
;                         v0[e] = act == 1 ? x0 * r0 : r0; v1[e] = act == 1 ? x1 * r1 : r1; } }
;                 if (stat) {
; #pragma unroll
;                     for (int e = 0; e < 4; ++e) { ls1 += v0[e] + v1[e]; ls2 += v0[e] * v0[e] + v1[e] * v1[e]; } }
;                 *(u32x4*)(rowp + bj * HALF) = pack8(v0, v1); }
;             if (stat) { ls1 = xor_add<16>(ls1); ls1 = xor_add<32>(ls1); ls2 = xor_add<16>(ls2); ls2 = xor_add<32>(ls2);
;                 if (fq == 0) { f32x2 st2; st2.x = ls1; st2.y = ls2; *(f32x2*)(stat + (size_t)(row0 + ai * HALF + m * 16) * 16) = st2; } }
	v_pk_mul_f32 v[46:47], v[46:47], v[146:147]
	v_pk_mul_f32 v[40:41], v[40:41], v[148:149]
	v_pk_mul_f32 v[42:43], v[42:43], v[150:151]
	v_pk_mul_f32 v[36:37], v[36:37], v[152:153]
	v_pk_mul_f32 v[38:39], v[38:39], v[154:155]
	s_mov_b64 s[0:1], 0x24000
	v_lshl_add_u64 v[136:137], v[134:135], 0, s[0:1]
	v_pk_add_f32 v[192:193], v[48:49], v[50:51]
	v_pk_mul_f32 v[194:195], v[48:49], v[48:49]
	v_pk_fma_f32 v[194:195], v[50:51], v[50:51], v[194:195]
	v_pk_add_f32 v[192:193], v[192:193], v[44:45]
	v_pk_fma_f32 v[194:195], v[44:45], v[44:45], v[194:195]
	v_pk_add_f32 v[192:193], v[192:193], v[46:47]
	v_pk_fma_f32 v[194:195], v[46:47], v[46:47], v[194:195]
	v_pk_add_f32 v[192:193], v[192:193], v[40:41]
	v_pk_fma_f32 v[194:195], v[40:41], v[40:41], v[194:195]
	v_pk_add_f32 v[192:193], v[192:193], v[42:43]
	v_pk_fma_f32 v[194:195], v[42:43], v[42:43], v[194:195]
	v_pk_add_f32 v[192:193], v[192:193], v[36:37]
	v_pk_fma_f32 v[194:195], v[36:37], v[36:37], v[194:195]
	v_pk_add_f32 v[192:193], v[192:193], v[38:39]
	v_pk_fma_f32 v[194:195], v[38:39], v[38:39], v[194:195]
	v_add_f32_e32 v162, v192, v193
	v_add_f32_e32 v163, v194, v195
	ds_swizzle_b32 v161, v162 offset:swizzle(SWAP,16)
	ds_swizzle_b32 v182, v163 offset:swizzle(SWAP,16)
	v_cvt_pk_bf16_f32 v48, v48, v49
	v_cvt_pk_bf16_f32 v49, v50, v51
	v_cvt_pk_bf16_f32 v50, v44, v45
	v_cvt_pk_bf16_f32 v51, v46, v47
	global_store_dwordx4 v[136:137], v[48:51], off
	v_cvt_pk_bf16_f32 v40, v40, v41
	v_cvt_pk_bf16_f32 v41, v42, v43
	v_cvt_pk_bf16_f32 v42, v36, v37
	v_cvt_pk_bf16_f32 v43, v38, v39
	global_store_dwordx4 v[136:137], v[40:43], off offset:256
	s_waitcnt lgkmcnt(0)
	v_add_f32_e32 v162, v162, v161
	v_add_f32_e32 v163, v163, v182
	v_mov_b32_e32 v183, v162
	v_mov_b32_e32 v184, v163
	s_mov_b64 s[0:1], 0x2400
	v_lshl_add_u64 v[140:141], v[138:139], 0, s[0:1]
	v_permlane32_swap_b32_e32 v162, v183
	v_permlane32_swap_b32_e32 v163, v184
	s_mov_b64 s[8:9], exec
	s_and_b64 exec, exec, s[4:5]
	v_add_f32_e32 v162, v162, v183
	v_add_f32_e32 v163, v163, v184
	global_store_dwordx2 v[140:141], v[162:163], off
	s_mov_b64 exec, s[8:9]
	s_nop 1
	s_waitcnt lgkmcnt(0)
	v_mov_b32_e32 v156, v157
	ds_read_b32 v157, v205 offset:704
	v_mul_f32_e32 v188, v156, v156
	v_mul_f32_e32 v186, 0xc0135761, v156
	v_rcp_f32_e32 v190, v156
	v_mul_f32_e32 v188, v188, v156
	v_mul_f32_e32 v188, 0xbdd2d3e8, v188
	v_pk_mul_f32 v[140:141], v[32:33], v[32:33]
	v_pk_mul_f32 v[142:143], v[34:35], v[34:35]
	v_pk_mul_f32 v[144:145], v[28:29], v[28:29]
	v_pk_mul_f32 v[146:147], v[30:31], v[30:31]
	v_pk_mul_f32 v[148:149], v[24:25], v[24:25]
	v_pk_mul_f32 v[150:151], v[26:27], v[26:27]
	v_pk_mul_f32 v[152:153], v[20:21], v[20:21]
	v_pk_mul_f32 v[154:155], v[22:23], v[22:23]
	v_pk_fma_f32 v[140:141], v[140:141], v[188:189], v[186:187] op_sel_hi:[1,0,0]
	v_pk_fma_f32 v[142:143], v[142:143], v[188:189], v[186:187] op_sel_hi:[1,0,0]
	v_pk_fma_f32 v[144:145], v[144:145], v[188:189], v[186:187] op_sel_hi:[1,0,0]
	v_pk_fma_f32 v[146:147], v[146:147], v[188:189], v[186:187] op_sel_hi:[1,0,0]
	v_pk_fma_f32 v[148:149], v[148:149], v[188:189], v[186:187] op_sel_hi:[1,0,0]
	v_pk_fma_f32 v[150:151], v[150:151], v[188:189], v[186:187] op_sel_hi:[1,0,0]
	v_pk_fma_f32 v[152:153], v[152:153], v[188:189], v[186:187] op_sel_hi:[1,0,0]
	v_pk_fma_f32 v[154:155], v[154:155], v[188:189], v[186:187] op_sel_hi:[1,0,0]
	v_pk_mul_f32 v[140:141], v[32:33], v[140:141]
	v_pk_mul_f32 v[142:143], v[34:35], v[142:143]
	v_pk_mul_f32 v[144:145], v[28:29], v[144:145]
	v_pk_mul_f32 v[146:147], v[30:31], v[146:147]
	v_pk_mul_f32 v[148:149], v[24:25], v[148:149]
	v_pk_mul_f32 v[150:151], v[26:27], v[150:151]
	v_pk_mul_f32 v[152:153], v[20:21], v[152:153]
	v_pk_mul_f32 v[154:155], v[22:23], v[154:155]
	v_exp_f32_e32 v140, v140
	v_exp_f32_e32 v141, v141
	v_exp_f32_e32 v142, v142
	v_exp_f32_e32 v143, v143
	v_exp_f32_e32 v144, v144
	v_exp_f32_e32 v145, v145
	v_exp_f32_e32 v146, v146
	v_exp_f32_e32 v147, v147
	v_exp_f32_e32 v148, v148
	v_exp_f32_e32 v149, v149
	v_exp_f32_e32 v150, v150
	v_exp_f32_e32 v151, v151
	v_exp_f32_e32 v152, v152
	v_exp_f32_e32 v153, v153
	v_exp_f32_e32 v154, v154
	v_exp_f32_e32 v155, v155
	v_pk_fma_f32 v[140:141], v[140:141], v[190:191], v[190:191] op_sel_hi:[1,0,0]
	v_pk_fma_f32 v[142:143], v[142:143], v[190:191], v[190:191] op_sel_hi:[1,0,0]
	v_pk_fma_f32 v[144:145], v[144:145], v[190:191], v[190:191] op_sel_hi:[1,0,0]
	v_pk_fma_f32 v[146:147], v[146:147], v[190:191], v[190:191] op_sel_hi:[1,0,0]
	v_pk_fma_f32 v[148:149], v[148:149], v[190:191], v[190:191] op_sel_hi:[1,0,0]
	v_pk_fma_f32 v[150:151], v[150:151], v[190:191], v[190:191] op_sel_hi:[1,0,0]
	v_pk_fma_f32 v[152:153], v[152:153], v[190:191], v[190:191] op_sel_hi:[1,0,0]
	v_pk_fma_f32 v[154:155], v[154:155], v[190:191], v[190:191] op_sel_hi:[1,0,0]
	v_rcp_f32_e32 v140, v140
	v_rcp_f32_e32 v141, v141
	v_rcp_f32_e32 v142, v142
	v_rcp_f32_e32 v143, v143
	v_rcp_f32_e32 v144, v144
	v_rcp_f32_e32 v145, v145
	v_rcp_f32_e32 v146, v146
	v_rcp_f32_e32 v147, v147
	v_rcp_f32_e32 v148, v148
	v_rcp_f32_e32 v149, v149
	v_rcp_f32_e32 v150, v150
	v_rcp_f32_e32 v151, v151
	v_rcp_f32_e32 v152, v152
	v_rcp_f32_e32 v153, v153
	v_rcp_f32_e32 v154, v154
	v_rcp_f32_e32 v155, v155
	v_pk_mul_f32 v[32:33], v[32:33], v[140:141]
	v_pk_mul_f32 v[34:35], v[34:35], v[142:143]
	v_pk_mul_f32 v[28:29], v[28:29], v[144:145]
	v_pk_mul_f32 v[30:31], v[30:31], v[146:147]
	v_pk_mul_f32 v[24:25], v[24:25], v[148:149]
	v_pk_mul_f32 v[26:27], v[26:27], v[150:151]
	v_pk_mul_f32 v[20:21], v[20:21], v[152:153]
	v_pk_mul_f32 v[22:23], v[22:23], v[154:155]
	s_mov_b64 s[0:1], 0x28000
	v_lshl_add_u64 v[136:137], v[134:135], 0, s[0:1]
	v_pk_add_f32 v[192:193], v[32:33], v[34:35]
	v_pk_mul_f32 v[194:195], v[32:33], v[32:33]
	v_pk_fma_f32 v[194:195], v[34:35], v[34:35], v[194:195]
	v_pk_add_f32 v[192:193], v[192:193], v[28:29]
	v_pk_fma_f32 v[194:195], v[28:29], v[28:29], v[194:195]
	v_pk_add_f32 v[192:193], v[192:193], v[30:31]
	v_pk_fma_f32 v[194:195], v[30:31], v[30:31], v[194:195]
	v_pk_add_f32 v[192:193], v[192:193], v[24:25]
	v_pk_fma_f32 v[194:195], v[24:25], v[24:25], v[194:195]
	v_pk_add_f32 v[192:193], v[192:193], v[26:27]
	v_pk_fma_f32 v[194:195], v[26:27], v[26:27], v[194:195]
	v_pk_add_f32 v[192:193], v[192:193], v[20:21]
	v_pk_fma_f32 v[194:195], v[20:21], v[20:21], v[194:195]
	v_pk_add_f32 v[192:193], v[192:193], v[22:23]
	v_pk_fma_f32 v[194:195], v[22:23], v[22:23], v[194:195]
	v_add_f32_e32 v162, v192, v193
	v_add_f32_e32 v163, v194, v195
	ds_swizzle_b32 v161, v162 offset:swizzle(SWAP,16)
	ds_swizzle_b32 v182, v163 offset:swizzle(SWAP,16)
	v_cvt_pk_bf16_f32 v32, v32, v33
	v_cvt_pk_bf16_f32 v33, v34, v35
	v_cvt_pk_bf16_f32 v34, v28, v29
	v_cvt_pk_bf16_f32 v35, v30, v31
	global_store_dwordx4 v[136:137], v[32:35], off
	v_cvt_pk_bf16_f32 v24, v24, v25
	v_cvt_pk_bf16_f32 v25, v26, v27
	v_cvt_pk_bf16_f32 v26, v20, v21
	v_cvt_pk_bf16_f32 v27, v22, v23
	global_store_dwordx4 v[136:137], v[24:27], off offset:256
	s_waitcnt lgkmcnt(0)
; __device__ __forceinline__ u32x4 pack8(const f32x4 a, const f32x4 b) { u32x4 w; w.x = cvt_pk_bf16(a[0], a[1]); w.y = cvt_pk_bf16(a[2], a[3]); w.z = cvt_pk_bf16(b[0], b[1]); w.w = cvt_pk_bf16(b[2], b[3]); return w; }
;     ...
;         for (int m = 0; m < 4; ++m) { bf16_t* rowp = base + (size_t)(row0 + ai * HALF + m * 16) * ldc + col0; float ls1 = 0.f, ls2 = 0.f; const float rf = rsr[ai * HALF + m * 16];
; #pragma unroll
;             for (int bj = 0; bj < 2; ++bj) { f32x4 v0 = acc[ai][bj][m][0] * rf, v1 = acc[ai][bj][m][1] * rf;
;                 if (act != 0) {
; #pragma unroll
;                     for (int e = 0; e < 4; ++e) { const float x0 = v0[e], x1 = v1[e];
;                         const float r0 = __builtin_amdgcn_rcpf(1.0f + __builtin_amdgcn_exp2f(x0 * (c0 + c1 * x0 * x0))), r1 = __builtin_amdgcn_rcpf(1.0f + __builtin_amdgcn_exp2f(x1 * (c0 + c1 * x1 * x1)));
;                         v0[e] = act == 1 ? x0 * r0 : r0; v1[e] = act == 1 ? x1 * r1 : r1; } }
;                 if (stat) {
; #pragma unroll
;                     for (int e = 0; e < 4; ++e) { ls1 += v0[e] + v1[e]; ls2 += v0[e] * v0[e] + v1[e] * v1[e]; } }
;                 *(u32x4*)(rowp + bj * HALF) = pack8(v0, v1); }
;             if (stat) { ls1 = xor_add<16>(ls1); ls1 = xor_add<32>(ls1); ls2 = xor_add<16>(ls2); ls2 = xor_add<32>(ls2);
;                 if (fq == 0) { f32x2 st2; st2.x = ls1; st2.y = ls2; *(f32x2*)(stat + (size_t)(row0 + ai * HALF + m * 16) * 16) = st2; } }
;             asm volatile("" ::: "memory"); } }
	v_add_f32_e32 v162, v162, v161
	v_add_f32_e32 v163, v163, v182
	v_mov_b32_e32 v183, v162
	v_mov_b32_e32 v184, v163
	s_mov_b64 s[0:1], 0x2800
	v_lshl_add_u64 v[140:141], v[138:139], 0, s[0:1]
	v_permlane32_swap_b32_e32 v162, v183
	v_permlane32_swap_b32_e32 v163, v184
	s_mov_b64 s[8:9], exec
	s_and_b64 exec, exec, s[4:5]
	v_add_f32_e32 v162, v162, v183
	v_add_f32_e32 v163, v163, v184
	global_store_dwordx2 v[140:141], v[162:163], off
	s_mov_b64 exec, s[8:9]
	s_nop 1
	s_waitcnt lgkmcnt(0)
	v_mov_b32_e32 v156, v157
	v_mul_f32_e32 v188, v156, v156
	v_mul_f32_e32 v186, 0xc0135761, v156
	v_rcp_f32_e32 v190, v156
	v_mul_f32_e32 v188, v188, v156
	v_mul_f32_e32 v188, 0xbdd2d3e8, v188
	v_pk_mul_f32 v[140:141], v[16:17], v[16:17]
	v_pk_mul_f32 v[142:143], v[18:19], v[18:19]
	v_pk_mul_f32 v[144:145], v[12:13], v[12:13]
	v_pk_mul_f32 v[146:147], v[14:15], v[14:15]
	v_pk_mul_f32 v[148:149], v[8:9], v[8:9]
	v_pk_mul_f32 v[150:151], v[10:11], v[10:11]
	v_pk_mul_f32 v[152:153], v[4:5], v[4:5]
	v_pk_mul_f32 v[154:155], v[6:7], v[6:7]
	v_pk_fma_f32 v[140:141], v[140:141], v[188:189], v[186:187] op_sel_hi:[1,0,0]
	v_pk_fma_f32 v[142:143], v[142:143], v[188:189], v[186:187] op_sel_hi:[1,0,0]
	v_pk_fma_f32 v[144:145], v[144:145], v[188:189], v[186:187] op_sel_hi:[1,0,0]
	v_pk_fma_f32 v[146:147], v[146:147], v[188:189], v[186:187] op_sel_hi:[1,0,0]
	v_pk_fma_f32 v[148:149], v[148:149], v[188:189], v[186:187] op_sel_hi:[1,0,0]
	v_pk_fma_f32 v[150:151], v[150:151], v[188:189], v[186:187] op_sel_hi:[1,0,0]
	v_pk_fma_f32 v[152:153], v[152:153], v[188:189], v[186:187] op_sel_hi:[1,0,0]
	v_pk_fma_f32 v[154:155], v[154:155], v[188:189], v[186:187] op_sel_hi:[1,0,0]
	v_pk_mul_f32 v[140:141], v[16:17], v[140:141]
	v_pk_mul_f32 v[142:143], v[18:19], v[142:143]
	v_pk_mul_f32 v[144:145], v[12:13], v[144:145]
	v_pk_mul_f32 v[146:147], v[14:15], v[146:147]
	v_pk_mul_f32 v[148:149], v[8:9], v[148:149]
	v_pk_mul_f32 v[150:151], v[10:11], v[150:151]
	v_pk_mul_f32 v[152:153], v[4:5], v[152:153]
	v_pk_mul_f32 v[154:155], v[6:7], v[154:155]
	v_exp_f32_e32 v140, v140
	v_exp_f32_e32 v141, v141
	v_exp_f32_e32 v142, v142
	v_exp_f32_e32 v143, v143
	v_exp_f32_e32 v144, v144
	v_exp_f32_e32 v145, v145
	v_exp_f32_e32 v146, v146
	v_exp_f32_e32 v147, v147
	v_exp_f32_e32 v148, v148
	v_exp_f32_e32 v149, v149
	v_exp_f32_e32 v150, v150
	v_exp_f32_e32 v151, v151
	v_exp_f32_e32 v152, v152
	v_exp_f32_e32 v153, v153
	v_exp_f32_e32 v154, v154
	v_exp_f32_e32 v155, v155
	v_pk_fma_f32 v[140:141], v[140:141], v[190:191], v[190:191] op_sel_hi:[1,0,0]
	v_pk_fma_f32 v[142:143], v[142:143], v[190:191], v[190:191] op_sel_hi:[1,0,0]
	v_pk_fma_f32 v[144:145], v[144:145], v[190:191], v[190:191] op_sel_hi:[1,0,0]
	v_pk_fma_f32 v[146:147], v[146:147], v[190:191], v[190:191] op_sel_hi:[1,0,0]
	v_pk_fma_f32 v[148:149], v[148:149], v[190:191], v[190:191] op_sel_hi:[1,0,0]
	v_pk_fma_f32 v[150:151], v[150:151], v[190:191], v[190:191] op_sel_hi:[1,0,0]
	v_pk_fma_f32 v[152:153], v[152:153], v[190:191], v[190:191] op_sel_hi:[1,0,0]
	v_pk_fma_f32 v[154:155], v[154:155], v[190:191], v[190:191] op_sel_hi:[1,0,0]
	v_rcp_f32_e32 v140, v140
	v_rcp_f32_e32 v141, v141
	v_rcp_f32_e32 v142, v142
	v_rcp_f32_e32 v143, v143
	v_rcp_f32_e32 v144, v144
	v_rcp_f32_e32 v145, v145
	v_rcp_f32_e32 v146, v146
	v_rcp_f32_e32 v147, v147
	v_rcp_f32_e32 v148, v148
	v_rcp_f32_e32 v149, v149
	v_rcp_f32_e32 v150, v150
	v_rcp_f32_e32 v151, v151
	v_rcp_f32_e32 v152, v152
	v_rcp_f32_e32 v153, v153
	v_rcp_f32_e32 v154, v154
	v_rcp_f32_e32 v155, v155
	v_pk_mul_f32 v[16:17], v[16:17], v[140:141]
	v_pk_mul_f32 v[18:19], v[18:19], v[142:143]
	v_pk_mul_f32 v[12:13], v[12:13], v[144:145]
	v_pk_mul_f32 v[14:15], v[14:15], v[146:147]
	v_pk_mul_f32 v[8:9], v[8:9], v[148:149]
	v_pk_mul_f32 v[10:11], v[10:11], v[150:151]
	v_pk_mul_f32 v[4:5], v[4:5], v[152:153]
	v_pk_mul_f32 v[6:7], v[6:7], v[154:155]
	s_mov_b64 s[0:1], 0x2c000
	v_lshl_add_u64 v[136:137], v[134:135], 0, s[0:1]
	v_pk_add_f32 v[192:193], v[16:17], v[18:19]
	v_pk_mul_f32 v[194:195], v[16:17], v[16:17]
	v_pk_fma_f32 v[194:195], v[18:19], v[18:19], v[194:195]
	v_pk_add_f32 v[192:193], v[192:193], v[12:13]
	v_pk_fma_f32 v[194:195], v[12:13], v[12:13], v[194:195]
	v_pk_add_f32 v[192:193], v[192:193], v[14:15]
	v_pk_fma_f32 v[194:195], v[14:15], v[14:15], v[194:195]
	v_pk_add_f32 v[192:193], v[192:193], v[8:9]
	v_pk_fma_f32 v[194:195], v[8:9], v[8:9], v[194:195]
	v_pk_add_f32 v[192:193], v[192:193], v[10:11]
	v_pk_fma_f32 v[194:195], v[10:11], v[10:11], v[194:195]
	v_pk_add_f32 v[192:193], v[192:193], v[4:5]
	v_pk_fma_f32 v[194:195], v[4:5], v[4:5], v[194:195]
	v_pk_add_f32 v[192:193], v[192:193], v[6:7]
	v_pk_fma_f32 v[194:195], v[6:7], v[6:7], v[194:195]
	v_add_f32_e32 v162, v192, v193
	v_add_f32_e32 v163, v194, v195
	ds_swizzle_b32 v161, v162 offset:swizzle(SWAP,16)
	ds_swizzle_b32 v182, v163 offset:swizzle(SWAP,16)
	v_cvt_pk_bf16_f32 v16, v16, v17
	v_cvt_pk_bf16_f32 v17, v18, v19
	v_cvt_pk_bf16_f32 v18, v12, v13
	v_cvt_pk_bf16_f32 v19, v14, v15
	global_store_dwordx4 v[136:137], v[16:19], off
	v_cvt_pk_bf16_f32 v8, v8, v9
	v_cvt_pk_bf16_f32 v9, v10, v11
	v_cvt_pk_bf16_f32 v10, v4, v5
	v_cvt_pk_bf16_f32 v11, v6, v7
	global_store_dwordx4 v[136:137], v[8:11], off offset:256
	s_waitcnt lgkmcnt(0)
	v_add_f32_e32 v162, v162, v161
	v_add_f32_e32 v163, v163, v182
	v_mov_b32_e32 v183, v162
	v_mov_b32_e32 v184, v163
	s_mov_b64 s[0:1], 0x2c00
	v_lshl_add_u64 v[140:141], v[138:139], 0, s[0:1]
	v_permlane32_swap_b32_e32 v162, v183
	v_permlane32_swap_b32_e32 v163, v184
	s_mov_b64 s[8:9], exec
	s_and_b64 exec, exec, s[4:5]
	v_add_f32_e32 v162, v162, v183
	v_add_f32_e32 v163, v163, v184
	global_store_dwordx2 v[140:141], v[162:163], off
	s_mov_b64 exec, s[8:9]
	s_nop 1
	s_branch .Lt8_end

; #define PG8_LAS __attribute__((address_space(3)))
; __device__ __forceinline__ u32x4 pack8(const f32x4 a, const f32x4 b) { u32x4 w; w.x = cvt_pk_bf16(a[0], a[1]); w.y = cvt_pk_bf16(a[2], a[3]); w.z = cvt_pk_bf16(b[0], b[1]); w.w = cvt_pk_bf16(b[2], b[3]); return w; }
; __device__ __forceinline__ float sigm(float x) { return __builtin_amdgcn_rcpf(1.0f + __builtin_amdgcn_exp2f(-1.4426950408889634f * x)); }
;     __device__ __forceinline__ void operator()(const f32x4 (&acc)[2][2][4][2], const Unit& u, int wr, int wc, int fr, int fq) const {
;         const int rl0 = wr * 64 + fr + (u.half == 2 ? HALF : 0), row0 = u.pm * BM + rl0, col0 = u.pn * HALF + wc * 32 + 8 * fq; const PG8_LAS float* rsr = rsl + rl0;
; #pragma unroll
;         for (int ai = 0; ai < 2; ++ai) { if (ai == 1 && u.half != 0) break;
; #pragma unroll
;             for (int m = 0; m < 4; ++m) { const float rf = rsr[ai * HALF + m * 16]; f32x4 v0 = acc[ai][0][m][0] * rf, v1 = acc[ai][0][m][1] * rf; const f32x4 u0 = acc[ai][1][m][0] * rf, u1 = acc[ai][1][m][1] * rf;
; #pragma unroll
;                 for (int e = 0; e < 4; ++e) { v0[e] = v0[e] * sigm(v0[e]) * u0[e]; v1[e] = v1[e] * sigm(v1[e]) * u1[e]; }
;                 *(u32x4*)(H + (size_t)(row0 + ai * HALF + m * 16) * DFF + col0) = pack8(v0, v1); } }
.LBB0_1480:
	ds_read_b32 v236, v148
	v_lshl_or_b32 v246, s20, 7, v149
	v_lshl_add_u32 v228, s14, 8, v146
	v_ashrrev_i32_e32 v247, 31, v246
	v_mov_b64_e32 v[242:243], s[4:5]
	v_mad_i64_i32 v[242:243], s[0:1], v228, s2, v[242:243]
	v_lshlrev_b64 v[246:247], 1, v[246:247]
	v_lshl_add_u64 v[242:243], v[242:243], 0, v[246:247]
	s_waitcnt lgkmcnt(0)
	ds_read_b32 v237, v148 offset:64
	v_mul_f32_e32 v238, 0xbfb8aa3b, v236
	v_mul_f32_e32 v240, v236, v236
	v_rcp_f32_e32 v240, v240
	v_pk_mul_f32 v[228:229], v[128:129], v[238:239] op_sel_hi:[1,0]
	v_pk_mul_f32 v[230:231], v[130:131], v[238:239] op_sel_hi:[1,0]
	v_pk_mul_f32 v[232:233], v[124:125], v[238:239] op_sel_hi:[1,0]
	v_pk_mul_f32 v[234:235], v[126:127], v[238:239] op_sel_hi:[1,0]
	v_exp_f32_e32 v228, v228
	v_exp_f32_e32 v229, v229
	v_exp_f32_e32 v230, v230
	v_exp_f32_e32 v231, v231
	v_exp_f32_e32 v232, v232
	v_exp_f32_e32 v233, v233
	v_exp_f32_e32 v234, v234
	v_exp_f32_e32 v235, v235
	v_pk_fma_f32 v[228:229], v[228:229], v[240:241], v[240:241] op_sel_hi:[1,0,0]
	v_pk_fma_f32 v[230:231], v[230:231], v[240:241], v[240:241] op_sel_hi:[1,0,0]
	v_pk_fma_f32 v[232:233], v[232:233], v[240:241], v[240:241] op_sel_hi:[1,0,0]
	v_pk_fma_f32 v[234:235], v[234:235], v[240:241], v[240:241] op_sel_hi:[1,0,0]
	v_rcp_f32_e32 v228, v228
	v_rcp_f32_e32 v229, v229
	v_rcp_f32_e32 v230, v230
	v_rcp_f32_e32 v231, v231
	v_rcp_f32_e32 v232, v232
	v_rcp_f32_e32 v233, v233
	v_rcp_f32_e32 v234, v234
	v_rcp_f32_e32 v235, v235
	v_pk_mul_f32 v[120:121], v[128:129], v[120:121]
	v_pk_mul_f32 v[122:123], v[130:131], v[122:123]
	v_pk_mul_f32 v[116:117], v[124:125], v[116:117]
	v_pk_mul_f32 v[118:119], v[126:127], v[118:119]
	v_pk_mul_f32 v[128:129], v[120:121], v[228:229]
	v_pk_mul_f32 v[130:131], v[122:123], v[230:231]
	v_pk_mul_f32 v[124:125], v[116:117], v[232:233]
	v_pk_mul_f32 v[126:127], v[118:119], v[234:235]
	v_cvt_pk_bf16_f32 v128, v128, v129
	v_cvt_pk_bf16_f32 v129, v130, v131
	v_cvt_pk_bf16_f32 v130, v124, v125
	v_cvt_pk_bf16_f32 v131, v126, v127
	global_store_dwordx4 v[242:243], v[128:131], off
	s_waitcnt lgkmcnt(0)
	v_mov_b32_e32 v236, v237
	ds_read_b32 v237, v148 offset:128
	v_mul_f32_e32 v238, 0xbfb8aa3b, v236
	v_mul_f32_e32 v240, v236, v236
	v_rcp_f32_e32 v240, v240
	v_pk_mul_f32 v[228:229], v[112:113], v[238:239] op_sel_hi:[1,0]
	v_pk_mul_f32 v[230:231], v[114:115], v[238:239] op_sel_hi:[1,0]
	v_pk_mul_f32 v[232:233], v[108:109], v[238:239] op_sel_hi:[1,0]
	v_pk_mul_f32 v[234:235], v[110:111], v[238:239] op_sel_hi:[1,0]
	v_exp_f32_e32 v228, v228
	v_exp_f32_e32 v229, v229
	v_exp_f32_e32 v230, v230
	v_exp_f32_e32 v231, v231
	v_exp_f32_e32 v232, v232
	v_exp_f32_e32 v233, v233
	v_exp_f32_e32 v234, v234
	v_exp_f32_e32 v235, v235
	v_pk_fma_f32 v[228:229], v[228:229], v[240:241], v[240:241] op_sel_hi:[1,0,0]
	v_pk_fma_f32 v[230:231], v[230:231], v[240:241], v[240:241] op_sel_hi:[1,0,0]
	v_pk_fma_f32 v[232:233], v[232:233], v[240:241], v[240:241] op_sel_hi:[1,0,0]
	v_pk_fma_f32 v[234:235], v[234:235], v[240:241], v[240:241] op_sel_hi:[1,0,0]
	v_rcp_f32_e32 v228, v228
	v_rcp_f32_e32 v229, v229
	v_rcp_f32_e32 v230, v230
	v_rcp_f32_e32 v231, v231
	v_rcp_f32_e32 v232, v232
	v_rcp_f32_e32 v233, v233
	v_rcp_f32_e32 v234, v234
	v_rcp_f32_e32 v235, v235
	v_pk_mul_f32 v[104:105], v[112:113], v[104:105]
	v_pk_mul_f32 v[106:107], v[114:115], v[106:107]
	v_pk_mul_f32 v[100:101], v[108:109], v[100:101]
	v_pk_mul_f32 v[102:103], v[110:111], v[102:103]
	s_mov_b64 s[0:1], 0x16000
	v_lshl_add_u64 v[244:245], v[242:243], 0, s[0:1]
	v_pk_mul_f32 v[112:113], v[104:105], v[228:229]
	v_pk_mul_f32 v[114:115], v[106:107], v[230:231]
	v_pk_mul_f32 v[108:109], v[100:101], v[232:233]
	v_pk_mul_f32 v[110:111], v[102:103], v[234:235]
	v_cvt_pk_bf16_f32 v112, v112, v113
	v_cvt_pk_bf16_f32 v113, v114, v115
	v_cvt_pk_bf16_f32 v114, v108, v109
	v_cvt_pk_bf16_f32 v115, v110, v111
	global_store_dwordx4 v[244:245], v[112:115], off
	s_waitcnt lgkmcnt(0)
	v_mov_b32_e32 v236, v237
	ds_read_b32 v237, v148 offset:192
	v_mul_f32_e32 v238, 0xbfb8aa3b, v236
	v_mul_f32_e32 v240, v236, v236
	v_rcp_f32_e32 v240, v240
	v_pk_mul_f32 v[228:229], v[96:97], v[238:239] op_sel_hi:[1,0]
	v_pk_mul_f32 v[230:231], v[98:99], v[238:239] op_sel_hi:[1,0]
	v_pk_mul_f32 v[232:233], v[92:93], v[238:239] op_sel_hi:[1,0]
	v_pk_mul_f32 v[234:235], v[94:95], v[238:239] op_sel_hi:[1,0]
	v_exp_f32_e32 v228, v228
	v_exp_f32_e32 v229, v229
	v_exp_f32_e32 v230, v230
	v_exp_f32_e32 v231, v231
	v_exp_f32_e32 v232, v232
	v_exp_f32_e32 v233, v233
	v_exp_f32_e32 v234, v234
	v_exp_f32_e32 v235, v235
	v_pk_fma_f32 v[228:229], v[228:229], v[240:241], v[240:241] op_sel_hi:[1,0,0]
	v_pk_fma_f32 v[230:231], v[230:231], v[240:241], v[240:241] op_sel_hi:[1,0,0]
	v_pk_fma_f32 v[232:233], v[232:233], v[240:241], v[240:241] op_sel_hi:[1,0,0]
	v_pk_fma_f32 v[234:235], v[234:235], v[240:241], v[240:241] op_sel_hi:[1,0,0]
	v_rcp_f32_e32 v228, v228
	v_rcp_f32_e32 v229, v229
	v_rcp_f32_e32 v230, v230
	v_rcp_f32_e32 v231, v231
	v_rcp_f32_e32 v232, v232
	v_rcp_f32_e32 v233, v233
	v_rcp_f32_e32 v234, v234
	v_rcp_f32_e32 v235, v235
	v_pk_mul_f32 v[88:89], v[96:97], v[88:89]
	v_pk_mul_f32 v[90:91], v[98:99], v[90:91]
	v_pk_mul_f32 v[84:85], v[92:93], v[84:85]
	v_pk_mul_f32 v[86:87], v[94:95], v[86:87]
	s_mov_b64 s[0:1], 0x2c000
	v_lshl_add_u64 v[244:245], v[242:243], 0, s[0:1]
	v_pk_mul_f32 v[96:97], v[88:89], v[228:229]
	v_pk_mul_f32 v[98:99], v[90:91], v[230:231]
	v_pk_mul_f32 v[92:93], v[84:85], v[232:233]
	v_pk_mul_f32 v[94:95], v[86:87], v[234:235]
	v_cvt_pk_bf16_f32 v96, v96, v97
	v_cvt_pk_bf16_f32 v97, v98, v99
	v_cvt_pk_bf16_f32 v98, v92, v93
	v_cvt_pk_bf16_f32 v99, v94, v95
	global_store_dwordx4 v[244:245], v[96:99], off
	s_waitcnt lgkmcnt(0)
; #define PG8_LAS __attribute__((address_space(3)))
; __device__ __forceinline__ u32x4 pack8(const f32x4 a, const f32x4 b) { u32x4 w; w.x = cvt_pk_bf16(a[0], a[1]); w.y = cvt_pk_bf16(a[2], a[3]); w.z = cvt_pk_bf16(b[0], b[1]); w.w = cvt_pk_bf16(b[2], b[3]); return w; }
; __device__ __forceinline__ float sigm(float x) { return __builtin_amdgcn_rcpf(1.0f + __builtin_amdgcn_exp2f(-1.4426950408889634f * x)); }
;     __device__ __forceinline__ void operator()(const f32x4 (&acc)[2][2][4][2], const Unit& u, int wr, int wc, int fr, int fq) const {
;         const int rl0 = wr * 64 + fr + (u.half == 2 ? HALF : 0), row0 = u.pm * BM + rl0, col0 = u.pn * HALF + wc * 32 + 8 * fq; const PG8_LAS float* rsr = rsl + rl0;
; #pragma unroll
;         for (int ai = 0; ai < 2; ++ai) { if (ai == 1 && u.half != 0) break;
; #pragma unroll
;             for (int m = 0; m < 4; ++m) { const float rf = rsr[ai * HALF + m * 16]; f32x4 v0 = acc[ai][0][m][0] * rf, v1 = acc[ai][0][m][1] * rf; const f32x4 u0 = acc[ai][1][m][0] * rf, u1 = acc[ai][1][m][1] * rf;
; #pragma unroll
;                 for (int e = 0; e < 4; ++e) { v0[e] = v0[e] * sigm(v0[e]) * u0[e]; v1[e] = v1[e] * sigm(v1[e]) * u1[e]; }
;                 *(u32x4*)(H + (size_t)(row0 + ai * HALF + m * 16) * DFF + col0) = pack8(v0, v1); } }
	v_mov_b32_e32 v236, v237
	ds_read_b32 v237, v148 offset:512
	v_mul_f32_e32 v238, 0xbfb8aa3b, v236
	v_mul_f32_e32 v240, v236, v236
	v_rcp_f32_e32 v240, v240
	v_pk_mul_f32 v[228:229], v[80:81], v[238:239] op_sel_hi:[1,0]
	v_pk_mul_f32 v[230:231], v[82:83], v[238:239] op_sel_hi:[1,0]
	v_pk_mul_f32 v[232:233], v[76:77], v[238:239] op_sel_hi:[1,0]
	v_pk_mul_f32 v[234:235], v[78:79], v[238:239] op_sel_hi:[1,0]
	v_exp_f32_e32 v228, v228
	v_exp_f32_e32 v229, v229
	v_exp_f32_e32 v230, v230
	v_exp_f32_e32 v231, v231
	v_exp_f32_e32 v232, v232
	v_exp_f32_e32 v233, v233
	v_exp_f32_e32 v234, v234
	v_exp_f32_e32 v235, v235
	v_pk_fma_f32 v[228:229], v[228:229], v[240:241], v[240:241] op_sel_hi:[1,0,0]
	v_pk_fma_f32 v[230:231], v[230:231], v[240:241], v[240:241] op_sel_hi:[1,0,0]
	v_pk_fma_f32 v[232:233], v[232:233], v[240:241], v[240:241] op_sel_hi:[1,0,0]
	v_pk_fma_f32 v[234:235], v[234:235], v[240:241], v[240:241] op_sel_hi:[1,0,0]
	v_rcp_f32_e32 v228, v228
	v_rcp_f32_e32 v229, v229
	v_rcp_f32_e32 v230, v230
	v_rcp_f32_e32 v231, v231
	v_rcp_f32_e32 v232, v232
	v_rcp_f32_e32 v233, v233
	v_rcp_f32_e32 v234, v234
	v_rcp_f32_e32 v235, v235
	v_pk_mul_f32 v[72:73], v[80:81], v[72:73]
	v_pk_mul_f32 v[74:75], v[82:83], v[74:75]
	v_pk_mul_f32 v[68:69], v[76:77], v[68:69]
	v_pk_mul_f32 v[70:71], v[78:79], v[70:71]
	s_mov_b64 s[0:1], 0x42000
	v_lshl_add_u64 v[244:245], v[242:243], 0, s[0:1]
	v_pk_mul_f32 v[80:81], v[72:73], v[228:229]
	v_pk_mul_f32 v[82:83], v[74:75], v[230:231]
	v_pk_mul_f32 v[76:77], v[68:69], v[232:233]
	v_pk_mul_f32 v[78:79], v[70:71], v[234:235]
	v_cvt_pk_bf16_f32 v80, v80, v81
	v_cvt_pk_bf16_f32 v81, v82, v83
	v_cvt_pk_bf16_f32 v82, v76, v77
	v_cvt_pk_bf16_f32 v83, v78, v79
	global_store_dwordx4 v[244:245], v[80:83], off
	s_waitcnt lgkmcnt(0)
	v_mov_b32_e32 v236, v237
	ds_read_b32 v237, v148 offset:576
	v_mul_f32_e32 v238, 0xbfb8aa3b, v236
	v_mul_f32_e32 v240, v236, v236
	v_rcp_f32_e32 v240, v240
	v_pk_mul_f32 v[228:229], v[64:65], v[238:239] op_sel_hi:[1,0]
	v_pk_mul_f32 v[230:231], v[66:67], v[238:239] op_sel_hi:[1,0]
	v_pk_mul_f32 v[232:233], v[60:61], v[238:239] op_sel_hi:[1,0]
	v_pk_mul_f32 v[234:235], v[62:63], v[238:239] op_sel_hi:[1,0]
	v_exp_f32_e32 v228, v228
	v_exp_f32_e32 v229, v229
	v_exp_f32_e32 v230, v230
	v_exp_f32_e32 v231, v231
	v_exp_f32_e32 v232, v232
	v_exp_f32_e32 v233, v233
	v_exp_f32_e32 v234, v234
	v_exp_f32_e32 v235, v235
	v_pk_fma_f32 v[228:229], v[228:229], v[240:241], v[240:241] op_sel_hi:[1,0,0]
	v_pk_fma_f32 v[230:231], v[230:231], v[240:241], v[240:241] op_sel_hi:[1,0,0]
	v_pk_fma_f32 v[232:233], v[232:233], v[240:241], v[240:241] op_sel_hi:[1,0,0]
	v_pk_fma_f32 v[234:235], v[234:235], v[240:241], v[240:241] op_sel_hi:[1,0,0]
	v_rcp_f32_e32 v228, v228
	v_rcp_f32_e32 v229, v229
	v_rcp_f32_e32 v230, v230
	v_rcp_f32_e32 v231, v231
	v_rcp_f32_e32 v232, v232
	v_rcp_f32_e32 v233, v233
	v_rcp_f32_e32 v234, v234
	v_rcp_f32_e32 v235, v235
	v_pk_mul_f32 v[56:57], v[64:65], v[56:57]
	v_pk_mul_f32 v[58:59], v[66:67], v[58:59]
	v_pk_mul_f32 v[52:53], v[60:61], v[52:53]
	v_pk_mul_f32 v[54:55], v[62:63], v[54:55]
	s_mov_b64 s[0:1], 0xb0000
	v_lshl_add_u64 v[244:245], v[242:243], 0, s[0:1]
	v_pk_mul_f32 v[64:65], v[56:57], v[228:229]
	v_pk_mul_f32 v[66:67], v[58:59], v[230:231]
	v_pk_mul_f32 v[60:61], v[52:53], v[232:233]
	v_pk_mul_f32 v[62:63], v[54:55], v[234:235]
	v_cvt_pk_bf16_f32 v64, v64, v65
	v_cvt_pk_bf16_f32 v65, v66, v67
	v_cvt_pk_bf16_f32 v66, v60, v61
	v_cvt_pk_bf16_f32 v67, v62, v63
	global_store_dwordx4 v[244:245], v[64:67], off
	s_waitcnt lgkmcnt(0)
	v_mov_b32_e32 v236, v237
	ds_read_b32 v237, v148 offset:640
	v_mul_f32_e32 v238, 0xbfb8aa3b, v236
	v_mul_f32_e32 v240, v236, v236
	v_rcp_f32_e32 v240, v240
	v_pk_mul_f32 v[228:229], v[48:49], v[238:239] op_sel_hi:[1,0]
	v_pk_mul_f32 v[230:231], v[50:51], v[238:239] op_sel_hi:[1,0]
	v_pk_mul_f32 v[232:233], v[44:45], v[238:239] op_sel_hi:[1,0]
	v_pk_mul_f32 v[234:235], v[46:47], v[238:239] op_sel_hi:[1,0]
	v_exp_f32_e32 v228, v228
	v_exp_f32_e32 v229, v229
	v_exp_f32_e32 v230, v230
	v_exp_f32_e32 v231, v231
	v_exp_f32_e32 v232, v232
	v_exp_f32_e32 v233, v233
	v_exp_f32_e32 v234, v234
	v_exp_f32_e32 v235, v235
	v_pk_fma_f32 v[228:229], v[228:229], v[240:241], v[240:241] op_sel_hi:[1,0,0]
	v_pk_fma_f32 v[230:231], v[230:231], v[240:241], v[240:241] op_sel_hi:[1,0,0]
	v_pk_fma_f32 v[232:233], v[232:233], v[240:241], v[240:241] op_sel_hi:[1,0,0]
	v_pk_fma_f32 v[234:235], v[234:235], v[240:241], v[240:241] op_sel_hi:[1,0,0]
	v_rcp_f32_e32 v228, v228
	v_rcp_f32_e32 v229, v229
	v_rcp_f32_e32 v230, v230
	v_rcp_f32_e32 v231, v231
	v_rcp_f32_e32 v232, v232
	v_rcp_f32_e32 v233, v233
	v_rcp_f32_e32 v234, v234
	v_rcp_f32_e32 v235, v235
	v_pk_mul_f32 v[40:41], v[48:49], v[40:41]
	v_pk_mul_f32 v[42:43], v[50:51], v[42:43]
	v_pk_mul_f32 v[36:37], v[44:45], v[36:37]
	v_pk_mul_f32 v[38:39], v[46:47], v[38:39]
	s_mov_b64 s[0:1], 0xc6000
	v_lshl_add_u64 v[244:245], v[242:243], 0, s[0:1]
	v_pk_mul_f32 v[48:49], v[40:41], v[228:229]
	v_pk_mul_f32 v[50:51], v[42:43], v[230:231]
	v_pk_mul_f32 v[44:45], v[36:37], v[232:233]
	v_pk_mul_f32 v[46:47], v[38:39], v[234:235]
	v_cvt_pk_bf16_f32 v48, v48, v49
	v_cvt_pk_bf16_f32 v49, v50, v51
	v_cvt_pk_bf16_f32 v50, v44, v45
	v_cvt_pk_bf16_f32 v51, v46, v47
	global_store_dwordx4 v[244:245], v[48:51], off
	s_waitcnt lgkmcnt(0)
; #define PG8_LAS __attribute__((address_space(3)))
; __device__ __forceinline__ u32x4 pack8(const f32x4 a, const f32x4 b) { u32x4 w; w.x = cvt_pk_bf16(a[0], a[1]); w.y = cvt_pk_bf16(a[2], a[3]); w.z = cvt_pk_bf16(b[0], b[1]); w.w = cvt_pk_bf16(b[2], b[3]); return w; }
; #define PG8_BAR __builtin_amdgcn_s_barrier()
; __device__ __forceinline__ float sigm(float x) { return __builtin_amdgcn_rcpf(1.0f + __builtin_amdgcn_exp2f(-1.4426950408889634f * x)); }
;     __device__ __forceinline__ void operator()(const f32x4 (&acc)[2][2][4][2], const Unit& u, int wr, int wc, int fr, int fq) const {
;         const int rl0 = wr * 64 + fr + (u.half == 2 ? HALF : 0), row0 = u.pm * BM + rl0, col0 = u.pn * HALF + wc * 32 + 8 * fq; const PG8_LAS float* rsr = rsl + rl0;
; #pragma unroll
;         for (int ai = 0; ai < 2; ++ai) { if (ai == 1 && u.half != 0) break;
; #pragma unroll
;             for (int m = 0; m < 4; ++m) { const float rf = rsr[ai * HALF + m * 16]; f32x4 v0 = acc[ai][0][m][0] * rf, v1 = acc[ai][0][m][1] * rf; const f32x4 u0 = acc[ai][1][m][0] * rf, u1 = acc[ai][1][m][1] * rf;
; #pragma unroll
;                 for (int e = 0; e < 4; ++e) { v0[e] = v0[e] * sigm(v0[e]) * u0[e]; v1[e] = v1[e] * sigm(v1[e]) * u1[e]; }
;                 *(u32x4*)(H + (size_t)(row0 + ai * HALF + m * 16) * DFF + col0) = pack8(v0, v1); } }
; template <class Epi, class Sched, bool ALIGN_EPI = false, bool SP2 = false>
; __device__ __forceinline__ void gemm_phase(PG8_LAS unsigned char* lds, const Gemm g, const Sched& S, const Epi& E) {
;     ...
;         if (!has_next) break;
;         if constexpr (!Epi::CHAIN) {
; #pragma unroll
;         for (int a = 0; a < 2; ++a)
; #pragma unroll
;             for (int b = 0; b < 2; ++b)
; #pragma unroll
;                 for (int m = 0; m < 4; ++m)
; #pragma unroll
;                     for (int n = 0; n < 2; ++n) acc[a][b][m][n] = (f32x4){0.f, 0.f, 0.f, 0.f};
;         }
;         cur = nxt; cA = nA; cB = nB; ++ui;
;         if constexpr (ALIGN_EPI) { if (wr == 1) PG8_BAR; }
	v_mov_b32_e32 v236, v237
	ds_read_b32 v237, v148 offset:704
	v_mul_f32_e32 v238, 0xbfb8aa3b, v236
	v_mul_f32_e32 v240, v236, v236
	v_rcp_f32_e32 v240, v240
	v_pk_mul_f32 v[228:229], v[32:33], v[238:239] op_sel_hi:[1,0]
	v_pk_mul_f32 v[230:231], v[34:35], v[238:239] op_sel_hi:[1,0]
	v_pk_mul_f32 v[232:233], v[28:29], v[238:239] op_sel_hi:[1,0]
	v_pk_mul_f32 v[234:235], v[30:31], v[238:239] op_sel_hi:[1,0]
	v_exp_f32_e32 v228, v228
	v_exp_f32_e32 v229, v229
	v_exp_f32_e32 v230, v230
	v_exp_f32_e32 v231, v231
	v_exp_f32_e32 v232, v232
	v_exp_f32_e32 v233, v233
	v_exp_f32_e32 v234, v234
	v_exp_f32_e32 v235, v235
	v_pk_fma_f32 v[228:229], v[228:229], v[240:241], v[240:241] op_sel_hi:[1,0,0]
	v_pk_fma_f32 v[230:231], v[230:231], v[240:241], v[240:241] op_sel_hi:[1,0,0]
	v_pk_fma_f32 v[232:233], v[232:233], v[240:241], v[240:241] op_sel_hi:[1,0,0]
	v_pk_fma_f32 v[234:235], v[234:235], v[240:241], v[240:241] op_sel_hi:[1,0,0]
	v_rcp_f32_e32 v228, v228
	v_rcp_f32_e32 v229, v229
	v_rcp_f32_e32 v230, v230
	v_rcp_f32_e32 v231, v231
	v_rcp_f32_e32 v232, v232
	v_rcp_f32_e32 v233, v233
	v_rcp_f32_e32 v234, v234
	v_rcp_f32_e32 v235, v235
	v_pk_mul_f32 v[24:25], v[32:33], v[24:25]
	v_pk_mul_f32 v[26:27], v[34:35], v[26:27]
	v_pk_mul_f32 v[20:21], v[28:29], v[20:21]
	v_pk_mul_f32 v[22:23], v[30:31], v[22:23]
	s_mov_b64 s[0:1], 0xdc000
	v_lshl_add_u64 v[244:245], v[242:243], 0, s[0:1]
	v_pk_mul_f32 v[32:33], v[24:25], v[228:229]
	v_pk_mul_f32 v[34:35], v[26:27], v[230:231]
	v_pk_mul_f32 v[28:29], v[20:21], v[232:233]
	v_pk_mul_f32 v[30:31], v[22:23], v[234:235]
	v_cvt_pk_bf16_f32 v32, v32, v33
	v_cvt_pk_bf16_f32 v33, v34, v35
	v_cvt_pk_bf16_f32 v34, v28, v29
	v_cvt_pk_bf16_f32 v35, v30, v31
	global_store_dwordx4 v[244:245], v[32:35], off
	s_waitcnt lgkmcnt(0)
	v_mov_b32_e32 v236, v237
	v_mul_f32_e32 v238, 0xbfb8aa3b, v236
	v_mul_f32_e32 v240, v236, v236
	v_rcp_f32_e32 v240, v240
	v_pk_mul_f32 v[228:229], v[16:17], v[238:239] op_sel_hi:[1,0]
	v_pk_mul_f32 v[230:231], v[18:19], v[238:239] op_sel_hi:[1,0]
	v_pk_mul_f32 v[232:233], v[12:13], v[238:239] op_sel_hi:[1,0]
	v_pk_mul_f32 v[234:235], v[14:15], v[238:239] op_sel_hi:[1,0]
	v_exp_f32_e32 v228, v228
	v_exp_f32_e32 v229, v229
	v_exp_f32_e32 v230, v230
	v_exp_f32_e32 v231, v231
	v_exp_f32_e32 v232, v232
	v_exp_f32_e32 v233, v233
	v_exp_f32_e32 v234, v234
	v_exp_f32_e32 v235, v235
	v_pk_fma_f32 v[228:229], v[228:229], v[240:241], v[240:241] op_sel_hi:[1,0,0]
	v_pk_fma_f32 v[230:231], v[230:231], v[240:241], v[240:241] op_sel_hi:[1,0,0]
	v_pk_fma_f32 v[232:233], v[232:233], v[240:241], v[240:241] op_sel_hi:[1,0,0]
	v_pk_fma_f32 v[234:235], v[234:235], v[240:241], v[240:241] op_sel_hi:[1,0,0]
	v_rcp_f32_e32 v228, v228
	v_rcp_f32_e32 v229, v229
	v_rcp_f32_e32 v230, v230
	v_rcp_f32_e32 v231, v231
	v_rcp_f32_e32 v232, v232
	v_rcp_f32_e32 v233, v233
	v_rcp_f32_e32 v234, v234
	v_rcp_f32_e32 v235, v235
	v_pk_mul_f32 v[8:9], v[16:17], v[8:9]
	v_pk_mul_f32 v[10:11], v[18:19], v[10:11]
	v_pk_mul_f32 v[4:5], v[12:13], v[4:5]
	v_pk_mul_f32 v[6:7], v[14:15], v[6:7]
	s_mov_b64 s[0:1], 0xf2000
	v_lshl_add_u64 v[244:245], v[242:243], 0, s[0:1]
	v_pk_mul_f32 v[16:17], v[8:9], v[228:229]
	v_pk_mul_f32 v[18:19], v[10:11], v[230:231]
	v_pk_mul_f32 v[12:13], v[4:5], v[232:233]
	v_pk_mul_f32 v[14:15], v[6:7], v[234:235]
	v_cvt_pk_bf16_f32 v16, v16, v17
	v_cvt_pk_bf16_f32 v17, v18, v19
	v_cvt_pk_bf16_f32 v18, v12, v13
	v_cvt_pk_bf16_f32 v19, v14, v15
	global_store_dwordx4 v[244:245], v[16:19], off
	s_andn2_b64 vcc, exec, s[38:39]
	s_mov_b64 s[0:1], -1
	s_cbranch_vccnz .LBB0_1473
	s_andn2_b64 vcc, exec, s[8:9]
	s_cbranch_vccnz .LBB0_1472
	s_barrier
	s_branch .LBB0_1472
